# P5 wide loads nt
# baseline (speedup 1.0000x reference)
.LBB0_907:
	v_mov_b32_e32 v22, v105
	s_ashr_i32 s8, s14, 2
	v_ashrrev_i32_e32 v36, 5, v22
	v_and_b32_e32 v184, 31, v22
	s_ashr_i32 s9, s8, 31
	v_lshlrev_b32_e32 v52, 3, v36
	s_lshl_b64 s[74:75], s[8:9], 6
	v_ashrrev_i32_e32 v53, 31, v52
	v_or_b32_e32 v109, 32, v184
	v_lshl_add_u64 v[8:9], v[52:53], 1, s[64:65]
	v_or_b32_e32 v178, s74, v184
	v_or_b32_e32 v176, s74, v109
	v_mad_u64_u32 v[10:11], s[16:17], v178, s2, v[8:9]
	v_mad_u64_u32 v[20:21], s[16:17], v176, s2, v[8:9]
	v_mad_i32_i24 v11, s75, v202, v11
	v_mad_i32_i24 v21, s75, v202, v21
	global_load_dwordx4 v[12:15], v[10:11], off offset:256 nt
	global_load_dwordx4 v[4:7], v[10:11], off offset:288 nt
	global_load_dwordx4 v[92:95], v[10:11], off nt
	global_load_dwordx4 v[84:87], v[10:11], off offset:32 nt
	global_load_dwordx4 v[16:19], v[20:21], off offset:256 nt
	s_nop 0
	global_load_dwordx4 v[8:11], v[20:21], off offset:288 nt
	global_load_dwordx4 v[96:99], v[20:21], off nt
	global_load_dwordx4 v[88:91], v[20:21], off offset:32 nt
	s_mul_i32 s7, s75, 0xe00
	v_mad_u64_u32 v[182:183], s[16:17], v178, s2, 0
	v_mad_u64_u32 v[180:181], s[16:17], v176, s2, 0
	v_add_u32_e32 v183, s7, v183
	v_add_u32_e32 v181, s7, v181
	s_mul_hi_i32 s7, s8, 0x38000
	s_mul_i32 s8, s8, 0x38000
	s_add_u32 s8, s72, s8
	s_addc_u32 s9, s73, s7
	v_ashrrev_i32_e32 v23, 31, v22
	v_mul_lo_u32 v2, v22, s46
	v_mov_b32_e32 v179, s75
	v_mov_b32_e32 v177, s75
	v_lshl_add_u64 v[20:21], v[22:23], 1, s[8:9]
	v_add_u32_e32 v2, s4, v2
	s_mov_b32 s7, 0
	s_mov_b64 s[38:39], -1
.LBB0_908:
	s_mul_i32 s56, s7, 0x700
	v_lshl_add_u64 v[22:23], s[56:57], 1, v[20:21]
	s_mov_b64 s[8:9], 0x200
	v_lshl_add_u64 v[24:25], v[22:23], 0, s[8:9]
	global_load_ushort v26, v[22:23], off offset:512
	global_load_ushort v27, v[24:25], off offset:3584
	v_add_co_u32_e32 v24, vcc, 0x1000, v22
	v_lshl_add_u32 v60, s7, 1, v2
	s_nop 0
	v_addc_co_u32_e32 v25, vcc, 0, v23, vcc
	global_load_ushort v28, v[24:25], off offset:3584
	v_add_co_u32_e32 v24, vcc, 0x2000, v22
	s_mov_b32 s7, 32
	s_nop 0
	v_addc_co_u32_e32 v25, vcc, 0, v23, vcc
	global_load_ushort v29, v[24:25], off offset:3072
	v_add_co_u32_e32 v24, vcc, 0x3000, v22
	s_nop 1
	v_addc_co_u32_e32 v25, vcc, 0, v23, vcc
	global_load_ushort v30, v[24:25], off offset:2560
	v_add_co_u32_e32 v24, vcc, 0x4000, v22
	s_nop 1
	v_addc_co_u32_e32 v25, vcc, 0, v23, vcc
	global_load_ushort v31, v[24:25], off offset:2048
	v_add_co_u32_e32 v24, vcc, 0x5000, v22
	s_nop 1
	v_addc_co_u32_e32 v25, vcc, 0, v23, vcc
	global_load_ushort v32, v[24:25], off offset:1536
	v_add_co_u32_e32 v24, vcc, 0x6000, v22
	s_nop 1
	v_addc_co_u32_e32 v25, vcc, 0, v23, vcc
	global_load_ushort v33, v[24:25], off offset:1024
	v_add_co_u32_e32 v24, vcc, 0x7000, v22
	s_nop 1
	v_addc_co_u32_e32 v25, vcc, 0, v23, vcc
	global_load_ushort v34, v[24:25], off offset:512
	v_add_co_u32_e32 v24, vcc, s81, v22
	s_nop 1
	v_addc_co_u32_e32 v25, vcc, 0, v23, vcc
	global_load_ushort v35, v[24:25], off
	global_load_ushort v37, v[24:25], off offset:3584
	v_add_co_u32_e32 v24, vcc, 0x9000, v22
	s_nop 1
	v_addc_co_u32_e32 v25, vcc, 0, v23, vcc
	global_load_ushort v38, v[24:25], off offset:3072
	v_add_co_u32_e32 v24, vcc, s78, v22
	s_nop 1
	v_addc_co_u32_e32 v25, vcc, 0, v23, vcc
	global_load_ushort v39, v[24:25], off offset:2560
	v_add_co_u32_e32 v24, vcc, 0xb000, v22
	s_nop 1
	v_addc_co_u32_e32 v25, vcc, 0, v23, vcc
	global_load_ushort v40, v[24:25], off offset:2048
	v_add_co_u32_e32 v24, vcc, s77, v22
	s_nop 1
	v_addc_co_u32_e32 v25, vcc, 0, v23, vcc
	global_load_ushort v41, v[24:25], off offset:1536
	v_add_co_u32_e32 v24, vcc, 0xd000, v22
	s_nop 1
	v_addc_co_u32_e32 v25, vcc, 0, v23, vcc
	global_load_ushort v42, v[24:25], off offset:1024
	v_add_co_u32_e32 v24, vcc, s76, v22
	s_nop 1
	v_addc_co_u32_e32 v25, vcc, 0, v23, vcc
	global_load_ushort v43, v[24:25], off offset:512
	v_add_co_u32_e32 v24, vcc, 0xf000, v22
	s_nop 1
	v_addc_co_u32_e32 v25, vcc, 0, v23, vcc
	global_load_ushort v44, v[24:25], off
	global_load_ushort v45, v[24:25], off offset:3584
	v_add_co_u32_e32 v24, vcc, s82, v22
	s_nop 1
	v_addc_co_u32_e32 v25, vcc, 0, v23, vcc
	global_load_ushort v46, v[24:25], off offset:3072
	v_add_co_u32_e32 v24, vcc, 0x11000, v22
	s_nop 1
	v_addc_co_u32_e32 v25, vcc, 0, v23, vcc
	global_load_ushort v47, v[24:25], off offset:2560
	v_add_co_u32_e32 v24, vcc, s83, v22
	s_nop 1
	v_addc_co_u32_e32 v25, vcc, 0, v23, vcc
	global_load_ushort v48, v[24:25], off offset:2048
	v_add_co_u32_e32 v24, vcc, 0x13000, v22
	s_nop 1
	v_addc_co_u32_e32 v25, vcc, 0, v23, vcc
	global_load_ushort v49, v[24:25], off offset:1536
	v_add_co_u32_e32 v24, vcc, s80, v22
	s_nop 1
	v_addc_co_u32_e32 v25, vcc, 0, v23, vcc
	global_load_ushort v50, v[24:25], off offset:1024
	v_add_co_u32_e32 v24, vcc, 0x15000, v22
	s_nop 1
	v_addc_co_u32_e32 v25, vcc, 0, v23, vcc
	global_load_ushort v51, v[24:25], off offset:512
	v_add_co_u32_e32 v24, vcc, s79, v22
	s_nop 1
	v_addc_co_u32_e32 v25, vcc, 0, v23, vcc
	global_load_ushort v53, v[24:25], off
	global_load_ushort v54, v[24:25], off offset:3584
	v_add_co_u32_e32 v24, vcc, 0x17000, v22
	s_nop 1
	v_addc_co_u32_e32 v25, vcc, 0, v23, vcc
	global_load_ushort v55, v[24:25], off offset:3072
	v_add_co_u32_e32 v24, vcc, s62, v22
	s_nop 1
	v_addc_co_u32_e32 v25, vcc, 0, v23, vcc
	global_load_ushort v56, v[24:25], off offset:2560
	v_add_co_u32_e32 v24, vcc, 0x19000, v22
	s_nop 1
	v_addc_co_u32_e32 v25, vcc, 0, v23, vcc
	global_load_ushort v57, v[24:25], off offset:2048
	v_add_co_u32_e32 v24, vcc, s63, v22
	s_nop 1
	v_addc_co_u32_e32 v25, vcc, 0, v23, vcc
	v_add_co_u32_e32 v22, vcc, 0x1b000, v22
	global_load_ushort v58, v[24:25], off offset:1536
	s_nop 0
	v_addc_co_u32_e32 v23, vcc, 0, v23, vcc
	global_load_ushort v59, v[22:23], off offset:1024
	s_waitcnt vmcnt(0)
	v_perm_b32 v25, v33, v32, s28
	v_perm_b32 v24, v31, v30, s28
	v_perm_b32 v23, v29, v28, s28
	v_perm_b32 v22, v27, v26, s28
	ds_write_b128 v60, v[22:25]
	v_perm_b32 v25, v42, v41, s28
	v_perm_b32 v24, v40, v39, s28
	v_perm_b32 v23, v38, v37, s28
	v_perm_b32 v22, v35, v34, s28
	ds_write_b128 v60, v[22:25] offset:16
	v_perm_b32 v22, v44, v43, s28
	s_and_b64 vcc, exec, s[38:39]
	s_mov_b64 s[38:39], 0
	v_perm_b32 v23, v46, v45, s28
	v_perm_b32 v24, v48, v47, s28
	v_perm_b32 v25, v50, v49, s28
	ds_write_b128 v60, v[22:25] offset:32
	v_perm_b32 v22, v53, v51, s28
	v_perm_b32 v23, v55, v54, s28
	v_perm_b32 v24, v57, v56, s28
	v_perm_b32 v25, v59, v58, s28
	ds_write_b128 v60, v[22:25] offset:48
	s_cbranch_vccnz .LBB0_908
	s_ashr_i32 s15, s14, 31
	s_lshl_b64 s[8:9], s[14:15], 13
	s_add_u32 s8, s5, s8
	s_addc_u32 s9, s6, s9
	v_lshlrev_b32_e32 v2, 2, v184
	v_lshlrev_b32_e32 v206, 9, v36
	s_waitcnt lgkmcnt(0)
	v_lshl_add_u64 v[188:189], s[8:9], 0, v[2:3]
	v_ashrrev_i32_e32 v207, 31, v206
	v_lshl_add_u64 v[54:55], v[206:207], 2, v[188:189]
	global_load_dword v2, v[54:55], off
	global_load_dword v53, v[54:55], off offset:256
	global_load_dword v56, v[54:55], off offset:512
	global_load_dword v57, v[54:55], off offset:768
	global_load_dword v58, v[54:55], off offset:1024
	global_load_dword v59, v[54:55], off offset:1280
	global_load_dword v60, v[54:55], off offset:1536
	global_load_dword v61, v[54:55], off offset:1792
	v_mfma_f32_32x32x16_bf16 v[68:83], v[12:15], v[92:95], 0
	v_lshlrev_b32_e32 v186, 2, v36
	v_add_u32_e32 v111, s4, v52
	s_movk_i32 s46, 0x90
	v_or_b32_e32 v52, 2, v186
	v_or_b32_e32 v62, 3, v186
	v_mad_u32_u24 v113, v184, s46, v111
	ds_read2_b64 v[196:199], v113 offset1:2
	ds_read2_b64 v[208:211], v113 offset0:8 offset1:10
	v_mfma_f32_32x32x16_bf16 v[36:51], v[12:15], v[96:99], 0
	v_add_u32_e32 v12, 0x400, v206
	v_add_u32_e32 v14, 0x440, v206
	v_ashrrev_i32_e32 v13, 31, v12
	v_ashrrev_i32_e32 v15, 31, v14
	v_lshlrev_b64 v[204:205], 2, v[12:13]
	v_lshlrev_b64 v[194:195], 2, v[14:15]
	global_load_dword v115, v[54:55], off offset:896
	global_load_dword v117, v[54:55], off offset:640
	global_load_dword v119, v[54:55], off offset:384
	global_load_dword v121, v[54:55], off offset:128
	global_load_dword v123, v[54:55], off offset:1920
	global_load_dword v125, v[54:55], off offset:1664
	global_load_dword v127, v[54:55], off offset:1408
	global_load_dword v129, v[54:55], off offset:1152
	v_mfma_f32_32x32x16_bf16 v[20:35], v[16:19], v[96:99], 0
	v_add_u32_e32 v16, 0x480, v206
	v_add_u32_e32 v18, 0x4c0, v206
	v_ashrrev_i32_e32 v17, 31, v16
	v_ashrrev_i32_e32 v19, 31, v18
	v_lshlrev_b64 v[192:193], 2, v[16:17]
	v_lshlrev_b64 v[190:191], 2, v[18:19]
	v_cmp_gt_i32_e64 s[38:39], v52, v184
	v_mfma_f32_32x32x16_bf16 v[68:83], v[4:7], v[84:87], v[68:83]
	v_cmp_gt_i32_e64 s[40:41], v62, v184
	v_add_u32_e32 v100, 8, v186
	v_add_u32_e32 v101, 9, v186
	v_cmp_gt_i32_e32 vcc, v186, v184
	v_cmp_gt_i32_e64 s[42:43], v100, v184
	v_cmp_gt_i32_e64 s[44:45], v101, v184
	v_cmp_lt_i32_e64 s[52:53], v186, v184
	v_mfma_f32_32x32x16_bf16 v[36:51], v[4:7], v[88:91], v[36:51]
	s_nop 3
	v_cndmask_b32_e64 v131, v68, 0, vcc
	v_add_u32_e32 v102, 10, v186
	v_cndmask_b32_e64 v68, v131, v68, s[52:53]
	v_cndmask_b32_e64 v69, 0, v69, s[52:53]
	v_cmp_gt_i32_e64 s[48:49], v102, v184
	v_cvt_pk_bf16_f32 v100, v68, v69
	v_add_u32_e32 v103, 11, v186
	v_mfma_f32_32x32x16_bf16 v[20:35], v[8:11], v[88:91], v[20:35]
	v_cvt_pk_bf16_f32 v68, v36, v37
	v_cvt_pk_bf16_f32 v69, v38, v39
	v_cmp_gt_i32_e64 s[50:51], v103, v184
	v_add_u32_e32 v212, 0x500, v206
	v_ashrrev_i32_e32 v213, 31, v212
	v_lshl_add_u64 v[214:215], v[188:189], 0, v[204:205]
	v_lshl_add_u64 v[216:217], v[188:189], 0, v[194:195]
	v_lshl_add_u64 v[218:219], v[188:189], 0, v[192:193]
	v_lshl_add_u64 v[220:221], v[188:189], 0, v[190:191]
	v_ashrrev_i32_e32 v187, 31, v186
	v_lshlrev_b64 v[178:179], 11, v[178:179]
	v_lshl_add_u64 v[178:179], s[70:71], 0, v[178:179]
	v_readlane_b32 s16, v253, 26
	v_readlane_b32 s17, v253, 27
	s_waitcnt vmcnt(14)
	v_cvt_pk_bf16_f32 v4, v2, v53
	v_cndmask_b32_e64 v2, v70, 0, s[38:39]
	s_waitcnt vmcnt(12)
	v_cvt_pk_bf16_f32 v5, v56, v57
	v_cndmask_b32_e64 v70, v71, 0, s[40:41]
	s_waitcnt vmcnt(10)
	v_cvt_pk_bf16_f32 v6, v58, v59
	v_cndmask_b32_e64 v71, v72, 0, s[42:43]
	s_waitcnt vmcnt(8)
	v_cvt_pk_bf16_f32 v7, v60, v61
	v_cndmask_b32_e64 v72, v73, 0, s[44:45]
	v_cvt_pk_bf16_f32 v101, v2, v70
	v_mfma_f32_32x32x16_bf16 v[52:67], v[4:7], v[92:95], 0
	v_cvt_pk_bf16_f32 v102, v71, v72
	v_cvt_pk_bf16_f32 v70, v40, v41
	v_cvt_pk_bf16_f32 v71, v42, v43
	v_cndmask_b32_e64 v73, v74, 0, s[48:49]
	v_cndmask_b32_e64 v74, v75, 0, s[50:51]
	v_cndmask_b32_e64 v2, v22, 0, s[38:39]
	v_cndmask_b32_e64 v22, v23, 0, s[40:41]
	v_mfma_f32_32x32x16_bf16 v[4:19], v[4:7], v[96:99], 0
	v_cvt_pk_bf16_f32 v103, v73, v74
	v_cvt_pk_bf16_f32 v73, v2, v22
	v_cndmask_b32_e64 v2, v26, 0, s[48:49]
	v_cndmask_b32_e64 v22, v27, 0, s[50:51]
	v_cvt_pk_bf16_f32 v75, v2, v22
	v_cndmask_b32_e64 v2, v20, 0, vcc
	v_cndmask_b32_e64 v23, v24, 0, s[42:43]
	s_waitcnt lgkmcnt(1)
	v_mfma_f32_32x32x16_bf16 v[4:19], v[196:199], v[68:71], v[4:19]
	v_cndmask_b32_e64 v24, v25, 0, s[44:45]
	v_cndmask_b32_e64 v2, v2, v20, s[52:53]
	v_cndmask_b32_e64 v20, 0, v21, s[52:53]
	v_add_u32_e32 v22, 0x540, v206
	v_cvt_pk_bf16_f32 v74, v23, v24
	v_cvt_pk_bf16_f32 v72, v2, v20
	v_ashrrev_i32_e32 v23, 31, v22
	v_mfma_f32_32x32x16_bf16 v[52:67], v[196:199], v[100:103], v[52:67]
	s_waitcnt lgkmcnt(0)
	v_mfma_f32_32x32x16_bf16 v[4:19], v[208:211], v[72:75], v[4:19]
	v_lshlrev_b64 v[208:209], 2, v[212:213]
	v_lshlrev_b64 v[210:211], 2, v[22:23]
	v_lshl_add_u64 v[20:21], v[188:189], 0, v[208:209]
	v_lshl_add_u64 v[22:23], v[188:189], 0, v[210:211]
	global_load_dword v2, v[214:215], off
	global_load_dword v24, v[216:217], off
	global_load_dword v25, v[218:219], off
	global_load_dword v26, v[220:221], off
	global_load_dword v27, v[20:21], off
	global_load_dword v36, v[22:23], off
	v_add_u32_e32 v20, 0x580, v206
	v_add_u32_e32 v22, 0x5c0, v206
	v_ashrrev_i32_e32 v21, 31, v20
	v_ashrrev_i32_e32 v23, 31, v22
	v_lshlrev_b64 v[212:213], 2, v[20:21]
	v_lshlrev_b64 v[206:207], 2, v[22:23]
	v_lshl_add_u64 v[20:21], v[188:189], 0, v[212:213]
	v_lshl_add_u64 v[22:23], v[188:189], 0, v[206:207]
	global_load_dword v37, v[20:21], off
	s_nop 0
	global_load_dword v23, v[22:23], off
	s_waitcnt vmcnt(6)
	v_cvt_pk_bf16_f32 v20, v2, v24
	v_add_u32_e32 v2, 16, v186
	s_waitcnt vmcnt(4)
	v_cvt_pk_bf16_f32 v21, v25, v26
	v_cmp_gt_i32_e32 vcc, v2, v184
	s_waitcnt vmcnt(2)
	v_cvt_pk_bf16_f32 v22, v27, v36
	v_add_u32_e32 v27, 25, v186
	v_cmp_gt_i32_e64 s[42:43], v27, v184
	v_add_u32_e32 v27, 26, v186
	v_cmp_gt_i32_e64 s[44:45], v27, v184
	v_add_u32_e32 v27, 27, v186
	v_add_u32_e32 v24, 17, v186
	v_add_u32_e32 v25, 18, v186
	v_add_u32_e32 v26, 19, v186
	s_waitcnt vmcnt(0)
	v_cvt_pk_bf16_f32 v23, v37, v23
	v_cmp_gt_i32_e64 s[48:49], v27, v184
	v_add_u32_e32 v27, 24, v186
	v_mfma_f32_32x32x16_bf16 v[52:67], v[20:23], v[84:87], v[52:67]
	v_cndmask_b32_e64 v2, v76, 0, vcc
	v_cndmask_b32_e64 v28, v28, 0, vcc
	v_cmp_gt_i32_e32 vcc, v24, v184
	v_cmp_gt_i32_e64 s[38:39], v25, v184
	v_cmp_gt_i32_e64 s[40:41], v26, v184
	v_cmp_gt_i32_e64 s[50:51], v27, v184
	v_cndmask_b32_e64 v24, v77, 0, vcc
	v_mfma_f32_32x32x16_bf16 v[4:19], v[20:23], v[88:91], v[4:19]
	ds_read2_b64 v[20:23], v113 offset0:4 offset1:6
	v_cndmask_b32_e64 v25, v78, 0, s[38:39]
	v_cndmask_b32_e64 v26, v79, 0, s[40:41]
	v_cndmask_b32_e64 v27, v80, 0, s[50:51]
	v_cndmask_b32_e64 v36, v81, 0, s[42:43]
	v_cndmask_b32_e64 v37, v82, 0, s[44:45]
	v_cndmask_b32_e64 v38, v83, 0, s[48:49]
	v_cvt_pk_bf16_f32 v76, v2, v24
	v_cvt_pk_bf16_f32 v77, v25, v26
	v_cvt_pk_bf16_f32 v78, v27, v36
	v_cvt_pk_bf16_f32 v79, v37, v38
	v_cvt_pk_bf16_f32 v80, v44, v45
	v_cvt_pk_bf16_f32 v81, v46, v47
	v_cvt_pk_bf16_f32 v82, v48, v49
	v_cvt_pk_bf16_f32 v83, v50, v51
	s_waitcnt lgkmcnt(0)
	v_mfma_f32_32x32x16_bf16 v[52:67], v[20:23], v[76:79], v[52:67]
	v_cndmask_b32_e64 v2, v31, 0, s[40:41]
	v_cndmask_b32_e64 v31, v32, 0, s[50:51]
	v_cndmask_b32_e64 v30, v30, 0, s[38:39]
	ds_read2_b64 v[24:27], v113 offset0:12 offset1:14
	v_cvt_pk_bf16_f32 v197, v30, v2
	v_mad_u32_u24 v2, v109, s46, v111
	v_cndmask_b32_e64 v29, v29, 0, vcc
	v_mfma_f32_32x32x16_bf16 v[4:19], v[20:23], v[80:83], v[4:19]
	v_cndmask_b32_e64 v20, v33, 0, s[42:43]
	v_cndmask_b32_e64 v21, v34, 0, s[44:45]
	v_cndmask_b32_e64 v22, v35, 0, s[48:49]
	v_cvt_pk_bf16_f32 v198, v31, v20
	v_cvt_pk_bf16_f32 v199, v21, v22
	v_cvt_pk_bf16_f32 v20, v121, v119
	v_cvt_pk_bf16_f32 v21, v117, v115
	v_cvt_pk_bf16_f32 v22, v129, v127
	v_cvt_pk_bf16_f32 v23, v125, v123
	v_cvt_pk_bf16_f32 v196, v28, v29
	s_nop 0
	v_mfma_f32_32x32x16_bf16 v[36:51], v[20:23], v[92:95], 0
	ds_read2_b64 v[92:95], v2 offset1:2
	s_waitcnt lgkmcnt(1)
	v_mfma_f32_32x32x16_bf16 v[4:19], v[24:27], v[196:199], v[4:19]
	v_mfma_f32_32x32x16_bf16 v[20:35], v[20:23], v[96:99], 0
	v_lshl_add_u64 v[96:97], v[188:189], 0, s[34:35]
	v_lshl_add_u64 v[98:99], v[96:97], 0, v[204:205]
	v_lshl_add_u64 v[184:185], v[96:97], 0, v[190:191]
	v_lshl_add_u64 v[188:189], v[96:97], 0, v[208:209]
	v_lshl_add_u64 v[190:191], v[96:97], 0, v[210:211]
	s_waitcnt lgkmcnt(0)
	v_mfma_f32_32x32x16_bf16 v[36:51], v[92:95], v[100:103], v[36:51]
	v_lshl_add_u64 v[100:101], v[96:97], 0, v[194:195]
	v_lshl_add_u64 v[102:103], v[96:97], 0, v[192:193]
	v_lshl_add_u64 v[192:193], v[96:97], 0, v[212:213]
	v_lshl_add_u64 v[96:97], v[96:97], 0, v[206:207]
	global_load_dword v98, v[98:99], off
	s_nop 0
	global_load_dword v99, v[100:101], off
	s_nop 0
	global_load_dword v100, v[102:103], off
	global_load_dword v101, v[184:185], off
	s_nop 0
	global_load_dword v102, v[188:189], off
	global_load_dword v103, v[190:191], off
	global_load_dword v109, v[192:193], off
	s_nop 0
	global_load_dword v96, v[96:97], off
	v_lshlrev_b64 v[190:191], 1, v[186:187]
	v_lshl_add_u64 v[178:179], v[178:179], 0, v[190:191]
	v_mfma_f32_32x32x16_bf16 v[20:35], v[92:95], v[68:71], v[20:35]
	ds_read2_b64 v[68:71], v2 offset0:8 offset1:10
	s_waitcnt lgkmcnt(0)
	v_mfma_f32_32x32x16_bf16 v[20:35], v[68:71], v[72:75], v[20:35]
	s_waitcnt vmcnt(6)
	v_cvt_pk_bf16_f32 v68, v98, v99
	s_waitcnt vmcnt(4)
	v_cvt_pk_bf16_f32 v69, v100, v101
	s_waitcnt vmcnt(2)
	v_cvt_pk_bf16_f32 v70, v102, v103
	s_waitcnt vmcnt(0)
	v_cvt_pk_bf16_f32 v71, v109, v96
	s_nop 1
	v_mfma_f32_32x32x16_bf16 v[36:51], v[68:71], v[84:87], v[36:51]
	v_mfma_f32_32x32x16_bf16 v[20:35], v[68:71], v[88:91], v[20:35]
	ds_read2_b64 v[68:71], v2 offset0:4 offset1:6
	s_waitcnt lgkmcnt(0)
	v_mfma_f32_32x32x16_bf16 v[36:51], v[68:71], v[76:79], v[36:51]
	v_mfma_f32_32x32x16_bf16 v[20:35], v[68:71], v[80:83], v[20:35]
	ds_read2_b64 v[68:71], v2 offset0:12 offset1:14
	v_xor_b32_e32 v2, 32, v250
	s_nop 8
	v_mul_f32_e64 v72, v48, v48
	v_mul_f32_e64 v73, v49, v49
	v_mul_f32_e64 v74, v50, v50
	v_mul_f32_e64 v75, v51, v51
	v_pk_fma_f32 v[72:73], v[64:65], v[64:65], v[72:73]
	v_pk_fma_f32 v[74:75], v[66:67], v[66:67], v[74:75]
	s_waitcnt lgkmcnt(0)
	v_mfma_f32_32x32x16_bf16 v[20:35], v[68:71], v[196:199], v[20:35]
	v_lshl_add_u64 v[68:69], s[72:73], 0, v[182:183]
	v_lshl_add_u64 v[100:101], v[68:69], 0, v[190:191]
	v_lshl_add_u64 v[68:69], v[186:187], 2, s[22:23]
	v_lshl_add_u64 v[70:71], s[72:73], 0, v[180:181]
	v_lshl_add_u64 v[196:197], v[70:71], 0, v[190:191]
	global_load_dwordx4 v[96:99], v[68:69], off nt
	global_load_dwordx4 v[92:95], v[68:69], off offset:32 nt
	global_load_dwordx4 v[88:91], v[68:69], off offset:64 nt
	global_load_dwordx4 v[80:83], v[68:69], off offset:96 nt
	global_load_dwordx2 v[198:199], v[100:101], off offset:1024 nt
	global_load_dwordx2 v[214:215], v[100:101], off offset:1040 nt
	global_load_dwordx2 v[212:213], v[100:101], off offset:1056 nt
	global_load_dwordx2 v[208:209], v[100:101], off offset:1072 nt
	global_load_dwordx2 v[192:193], v[196:197], off offset:1024 nt
	global_load_dwordx2 v[188:189], v[196:197], off offset:1040 nt
	global_load_dwordx2 v[184:185], v[196:197], off offset:1056 nt
	global_load_dwordx2 v[180:181], v[196:197], off offset:1072 nt
	v_and_b32_e32 v70, 64, v250
	v_add_u32_e32 v113, 64, v70
	v_cmp_lt_i32_e32 vcc, v2, v113
	v_mul_f32_e32 v70, v37, v37
	v_fmac_f32_e32 v70, v53, v53
	v_cndmask_b32_e32 v2, v250, v2, vcc
	v_lshlrev_b32_e32 v109, 2, v2
	v_mul_f32_e32 v2, v36, v36
	v_fmac_f32_e32 v2, v52, v52
	v_add_f32_e32 v2, v2, v70
	v_mul_f32_e32 v70, v38, v38
	v_fmac_f32_e32 v70, v54, v54
	v_add_f32_e32 v2, v70, v2
	v_mul_f32_e32 v70, v39, v39
	v_fmac_f32_e32 v70, v55, v55
	v_add_f32_e32 v2, v70, v2
	v_mul_f32_e32 v70, v40, v40
	v_fmac_f32_e32 v70, v56, v56
	v_add_f32_e32 v2, v70, v2
	v_mul_f32_e32 v70, v41, v41
	v_fmac_f32_e32 v70, v57, v57
	v_add_f32_e32 v2, v70, v2
	v_mul_f32_e32 v70, v42, v42
	v_fmac_f32_e32 v70, v58, v58
	v_add_f32_e32 v2, v70, v2
	v_mul_f32_e32 v70, v43, v43
	v_fmac_f32_e32 v70, v59, v59
	v_add_f32_e32 v2, v70, v2
	v_mul_f32_e32 v70, v44, v44
	v_fmac_f32_e32 v70, v60, v60
	v_add_f32_e32 v2, v70, v2
	v_mul_f32_e32 v70, v45, v45
	v_fmac_f32_e32 v70, v61, v61
	v_add_f32_e32 v2, v70, v2
	v_pk_mul_f32 v[70:71], v[46:47], v[46:47]
	s_nop 0
	v_pk_fma_f32 v[70:71], v[62:63], v[62:63], v[70:71]
	s_nop 0
	v_add_f32_e32 v2, v70, v2
	v_add_f32_e32 v2, v71, v2
	v_add_f32_e32 v2, v72, v2
	v_add_f32_e32 v2, v73, v2
	v_add_f32_e32 v2, v74, v2
	v_add_f32_e32 v2, v75, v2
	ds_bpermute_b32 v102, v109, v2
	global_load_dwordx4 v[84:87], v[68:69], off offset:128 nt
	global_load_dwordx4 v[76:79], v[68:69], off offset:160 nt
	global_load_dwordx4 v[72:75], v[68:69], off offset:192 nt
	s_nop 0
	global_load_dwordx4 v[68:71], v[68:69], off offset:224 nt
	s_nop 0
	global_load_dwordx2 v[210:211], v[100:101], off offset:1088 nt
	global_load_dwordx2 v[206:207], v[100:101], off offset:1104 nt
	global_load_dwordx2 v[204:205], v[100:101], off offset:1120 nt
	global_load_dwordx2 v[194:195], v[100:101], off offset:1136 nt
	s_waitcnt lgkmcnt(0)
	v_add_f32_e32 v2, v2, v102
	v_fmamk_f32 v2, v2, 0x3c800000, v1
	v_mul_f32_e32 v102, 0x4f800000, v2
	v_cmp_gt_f32_e32 vcc, s29, v2
	s_nop 1
	v_cndmask_b32_e32 v2, v2, v102, vcc
	v_sqrt_f32_e32 v102, v2
	s_nop 0
	v_add_u32_e32 v100, -1, v102
	v_fma_f32 v101, -v100, v102, v2
	v_cmp_ge_f32_e64 s[38:39], 0, v101
	v_add_u32_e32 v101, 1, v102
	s_nop 0
	v_cndmask_b32_e64 v100, v102, v100, s[38:39]
	v_fma_f32 v102, -v101, v102, v2
	v_cmp_lt_f32_e64 s[38:39], 0, v102
	s_nop 1
	v_cndmask_b32_e64 v100, v100, v101, s[38:39]
	v_mul_f32_e32 v101, 0x37800000, v100
	v_cndmask_b32_e32 v100, v100, v101, vcc
	v_cmp_class_f32_e32 vcc, v2, v248
	s_nop 1
	v_cndmask_b32_e32 v2, v100, v2, vcc
	v_div_scale_f32 v111, s[8:9], v2, v2, 1.0
	v_rcp_f32_e32 v115, v111
	global_load_dwordx2 v[186:187], v[196:197], off offset:1088 nt
	global_load_dwordx2 v[182:183], v[196:197], off offset:1104 nt
	global_load_dwordx2 v[102:103], v[196:197], off offset:1120 nt
	global_load_dwordx2 v[100:101], v[196:197], off offset:1136 nt
	s_waitcnt vmcnt(19)
	v_lshlrev_b32_e32 v196, 16, v198
	v_and_b32_e32 v197, 0xffff0000, v198
	v_fma_f32 v117, -v111, v115, 1.0
	v_fmac_f32_e32 v115, v117, v115
	v_div_scale_f32 v117, vcc, 1.0, v2, 1.0
	v_mul_f32_e32 v119, v117, v115
	v_fma_f32 v121, -v111, v119, v117
	v_fmac_f32_e32 v119, v121, v115
	v_fma_f32 v111, -v111, v119, v117
	v_div_fmas_f32 v111, v111, v115, v119
	v_div_fixup_f32 v2, v111, v2, 1.0
	v_mul_f32_e32 v111, 0xbfb8aa3b, v196
	v_exp_f32_e32 v111, v111
	v_mul_f32_e32 v115, 0xbfb8aa3b, v197
	v_exp_f32_e32 v115, v115
	v_pk_mul_f32 v[52:53], v[52:53], v[2:3] op_sel_hi:[1,0]
	v_add_f32_e32 v111, 1.0, v111
	v_pk_mul_f32 v[52:53], v[96:97], v[52:53]
	v_rcp_f32_e32 v216, v111
	v_add_f32_e32 v111, 1.0, v115
	v_pk_mul_f32 v[52:53], v[52:53], v[196:197]
	v_lshlrev_b32_e32 v196, 16, v199
	v_rcp_f32_e32 v217, v111
	v_and_b32_e32 v197, 0xffff0000, v199
	v_mul_f32_e32 v111, 0xbfb8aa3b, v196
	v_exp_f32_e32 v111, v111
	v_mul_f32_e32 v115, 0xbfb8aa3b, v197
	v_exp_f32_e32 v115, v115
	v_pk_mul_f32 v[52:53], v[216:217], v[52:53]
	v_pk_mul_f32 v[54:55], v[54:55], v[2:3] op_sel_hi:[1,0]
	v_cvt_pk_bf16_f32 v52, v52, v53
	v_add_f32_e32 v53, 1.0, v111
	v_rcp_f32_e32 v198, v53
	v_add_f32_e32 v53, 1.0, v115
	v_rcp_f32_e32 v199, v53
	v_pk_mul_f32 v[54:55], v[98:99], v[54:55]
	v_pk_mul_f32 v[56:57], v[56:57], v[2:3] op_sel_hi:[1,0]
	v_pk_mul_f32 v[54:55], v[54:55], v[196:197]
	v_pk_mul_f32 v[56:57], v[92:93], v[56:57]
	v_pk_mul_f32 v[54:55], v[198:199], v[54:55]
	v_pk_mul_f32 v[58:59], v[58:59], v[2:3] op_sel_hi:[1,0]
	v_cvt_pk_bf16_f32 v53, v54, v55
	s_waitcnt vmcnt(18)
	v_lshlrev_b32_e32 v54, 16, v214
	v_and_b32_e32 v55, 0xffff0000, v214
	v_mul_f32_e32 v111, 0xbfb8aa3b, v54
	v_mul_f32_e32 v115, 0xbfb8aa3b, v55
	v_exp_f32_e32 v111, v111
	v_exp_f32_e32 v115, v115
	global_store_dwordx2 v[178:179], v[52:53], off offset:1024
	v_pk_mul_f32 v[54:55], v[56:57], v[54:55]
	v_add_f32_e32 v52, 1.0, v111
	v_add_f32_e32 v53, 1.0, v115
	v_rcp_f32_e32 v52, v52
	v_rcp_f32_e32 v53, v53
	v_pk_mul_f32 v[58:59], v[94:95], v[58:59]
	v_pk_mul_f32 v[36:37], v[36:37], v[2:3] op_sel_hi:[1,0]
	v_pk_mul_f32 v[38:39], v[38:39], v[2:3] op_sel_hi:[1,0]
	v_pk_mul_f32 v[52:53], v[52:53], v[54:55]
	v_lshlrev_b32_e32 v54, 16, v215
	v_and_b32_e32 v55, 0xffff0000, v215
	v_mul_f32_e32 v56, 0xbfb8aa3b, v54
	v_exp_f32_e32 v56, v56
	v_mul_f32_e32 v57, 0xbfb8aa3b, v55
	v_exp_f32_e32 v57, v57
	v_cvt_pk_bf16_f32 v52, v52, v53
	v_add_f32_e32 v53, 1.0, v56
	v_rcp_f32_e32 v56, v53
	v_add_f32_e32 v53, 1.0, v57
	v_rcp_f32_e32 v57, v53
	v_pk_mul_f32 v[54:55], v[58:59], v[54:55]
	v_pk_mul_f32 v[58:59], v[62:63], v[2:3] op_sel_hi:[1,0]
	s_waitcnt vmcnt(12)
	v_pk_mul_f32 v[36:37], v[84:85], v[36:37]
	v_pk_mul_f32 v[54:55], v[56:57], v[54:55]
	v_pk_mul_f32 v[58:59], v[90:91], v[58:59]
	v_cvt_pk_bf16_f32 v53, v54, v55
	v_lshlrev_b32_e32 v54, 16, v212
	v_and_b32_e32 v55, 0xffff0000, v212
	v_mul_f32_e32 v56, 0xbfb8aa3b, v54
	v_mul_f32_e32 v57, 0xbfb8aa3b, v55
	v_exp_f32_e32 v56, v56
	v_exp_f32_e32 v57, v57
	global_store_dwordx2 v[178:179], v[52:53], off offset:1040
	v_pk_mul_f32 v[38:39], v[86:87], v[38:39]
	v_add_f32_e32 v52, 1.0, v56
	v_add_f32_e32 v53, 1.0, v57
	v_rcp_f32_e32 v52, v52
	v_rcp_f32_e32 v53, v53
	v_pk_mul_f32 v[56:57], v[60:61], v[2:3] op_sel_hi:[1,0]
	v_pk_mul_f32 v[40:41], v[40:41], v[2:3] op_sel_hi:[1,0]
	v_pk_mul_f32 v[56:57], v[88:89], v[56:57]
	s_waitcnt vmcnt(12)
	v_pk_mul_f32 v[40:41], v[76:77], v[40:41]
	v_pk_mul_f32 v[54:55], v[56:57], v[54:55]
	v_pk_mul_f32 v[42:43], v[42:43], v[2:3] op_sel_hi:[1,0]
	v_pk_mul_f32 v[52:53], v[52:53], v[54:55]
	v_lshlrev_b32_e32 v54, 16, v213
	v_and_b32_e32 v55, 0xffff0000, v213
	v_mul_f32_e32 v56, 0xbfb8aa3b, v54
	v_exp_f32_e32 v56, v56
	v_mul_f32_e32 v57, 0xbfb8aa3b, v55
	v_exp_f32_e32 v57, v57
	v_cvt_pk_bf16_f32 v52, v52, v53
	v_add_f32_e32 v53, 1.0, v56
	v_rcp_f32_e32 v56, v53
	v_add_f32_e32 v53, 1.0, v57
	v_rcp_f32_e32 v57, v53
	v_pk_mul_f32 v[54:55], v[58:59], v[54:55]
	v_pk_mul_f32 v[58:59], v[66:67], v[2:3] op_sel_hi:[1,0]
	v_pk_mul_f32 v[42:43], v[78:79], v[42:43]
	v_pk_mul_f32 v[54:55], v[56:57], v[54:55]
	v_pk_mul_f32 v[58:59], v[82:83], v[58:59]
	v_cvt_pk_bf16_f32 v53, v54, v55
	v_lshlrev_b32_e32 v54, 16, v208
	v_and_b32_e32 v55, 0xffff0000, v208
	v_mul_f32_e32 v56, 0xbfb8aa3b, v54
	v_mul_f32_e32 v57, 0xbfb8aa3b, v55
	v_exp_f32_e32 v56, v56
	v_exp_f32_e32 v57, v57
	global_store_dwordx2 v[178:179], v[52:53], off offset:1056
	v_or_b32_e32 v208, s74, v112
	v_add_f32_e32 v52, 1.0, v56
	v_add_f32_e32 v53, 1.0, v57
	v_rcp_f32_e32 v52, v52
	v_rcp_f32_e32 v53, v53
	v_pk_mul_f32 v[56:57], v[64:65], v[2:3] op_sel_hi:[1,0]
	s_nop 0
	v_pk_mul_f32 v[56:57], v[80:81], v[56:57]
	s_nop 0
	v_pk_mul_f32 v[54:55], v[56:57], v[54:55]
	s_nop 0
	v_pk_mul_f32 v[52:53], v[52:53], v[54:55]
	v_lshlrev_b32_e32 v54, 16, v209
	v_and_b32_e32 v55, 0xffff0000, v209
	v_mul_f32_e32 v56, 0xbfb8aa3b, v54
	v_exp_f32_e32 v56, v56
	v_mul_f32_e32 v57, 0xbfb8aa3b, v55
	v_exp_f32_e32 v57, v57
	v_cvt_pk_bf16_f32 v52, v52, v53
	v_add_f32_e32 v53, 1.0, v56
	v_rcp_f32_e32 v56, v53
	v_add_f32_e32 v53, 1.0, v57
	v_rcp_f32_e32 v57, v53
	v_pk_mul_f32 v[54:55], v[58:59], v[54:55]
	v_mov_b32_e32 v209, s75
	v_pk_mul_f32 v[54:55], v[56:57], v[54:55]
	s_nop 0
	v_cvt_pk_bf16_f32 v53, v54, v55
	s_waitcnt vmcnt(10)
	v_lshlrev_b32_e32 v54, 16, v210
	v_and_b32_e32 v55, 0xffff0000, v210
	v_mul_f32_e32 v56, 0xbfb8aa3b, v54
	v_mul_f32_e32 v57, 0xbfb8aa3b, v55
	v_exp_f32_e32 v56, v56
	v_exp_f32_e32 v57, v57
	global_store_dwordx2 v[178:179], v[52:53], off offset:1072
	v_pk_mul_f32 v[36:37], v[36:37], v[54:55]
	v_add_f32_e32 v52, 1.0, v56
	v_add_f32_e32 v53, 1.0, v57
	v_rcp_f32_e32 v52, v52
	v_rcp_f32_e32 v53, v53
	s_nop 0
	v_pk_mul_f32 v[36:37], v[52:53], v[36:37]
	v_lshlrev_b32_e32 v52, 16, v211
	v_and_b32_e32 v53, 0xffff0000, v211
	v_mul_f32_e32 v54, 0xbfb8aa3b, v52
	v_exp_f32_e32 v54, v54
	v_mul_f32_e32 v55, 0xbfb8aa3b, v53
	v_exp_f32_e32 v55, v55
	v_cvt_pk_bf16_f32 v36, v36, v37
	v_add_f32_e32 v37, 1.0, v54
	v_rcp_f32_e32 v54, v37
	v_add_f32_e32 v37, 1.0, v55
	v_rcp_f32_e32 v55, v37
	v_pk_mul_f32 v[38:39], v[38:39], v[52:53]
	v_mov_b64_e32 v[210:211], s[18:19]
	v_pk_mul_f32 v[38:39], v[54:55], v[38:39]
	s_nop 0
	v_cvt_pk_bf16_f32 v37, v38, v39
	s_waitcnt vmcnt(10)
	v_lshlrev_b32_e32 v38, 16, v206
	v_and_b32_e32 v39, 0xffff0000, v206
	v_mul_f32_e32 v52, 0xbfb8aa3b, v38
	v_mul_f32_e32 v53, 0xbfb8aa3b, v39
	v_exp_f32_e32 v52, v52
	v_exp_f32_e32 v53, v53
	global_store_dwordx2 v[178:179], v[36:37], off offset:1088
	v_pk_mul_f32 v[38:39], v[40:41], v[38:39]
	v_add_f32_e32 v36, 1.0, v52
	v_add_f32_e32 v37, 1.0, v53
	v_rcp_f32_e32 v36, v36
	v_rcp_f32_e32 v37, v37
	v_or_b32_e32 v206, s74, v114
	v_pk_mul_f32 v[36:37], v[36:37], v[38:39]
	v_lshlrev_b32_e32 v38, 16, v207
	v_and_b32_e32 v39, 0xffff0000, v207
	v_mul_f32_e32 v40, 0xbfb8aa3b, v38
	v_exp_f32_e32 v40, v40
	v_mul_f32_e32 v41, 0xbfb8aa3b, v39
	v_exp_f32_e32 v41, v41
	v_cvt_pk_bf16_f32 v36, v36, v37
	v_add_f32_e32 v37, 1.0, v40
	v_rcp_f32_e32 v40, v37
	v_add_f32_e32 v37, 1.0, v41
	v_rcp_f32_e32 v41, v37
	v_pk_mul_f32 v[38:39], v[42:43], v[38:39]
	v_pk_mul_f32 v[42:43], v[46:47], v[2:3] op_sel_hi:[1,0]
	v_pk_mul_f32 v[46:47], v[34:35], v[34:35]
	v_pk_mul_f32 v[38:39], v[40:41], v[38:39]
	v_pk_mul_f32 v[42:43], v[74:75], v[42:43]
	v_cvt_pk_bf16_f32 v37, v38, v39
	s_waitcnt vmcnt(10)
	v_lshlrev_b32_e32 v38, 16, v204
	v_and_b32_e32 v39, 0xffff0000, v204
	v_mul_f32_e32 v40, 0xbfb8aa3b, v38
	v_mul_f32_e32 v41, 0xbfb8aa3b, v39
	v_exp_f32_e32 v40, v40
	v_exp_f32_e32 v41, v41
	global_store_dwordx2 v[178:179], v[36:37], off offset:1104
	v_pk_fma_f32 v[46:47], v[18:19], v[18:19], v[46:47]
	v_add_f32_e32 v36, 1.0, v40
	v_add_f32_e32 v37, 1.0, v41
	v_rcp_f32_e32 v36, v36
	v_rcp_f32_e32 v37, v37
	v_pk_mul_f32 v[40:41], v[44:45], v[2:3] op_sel_hi:[1,0]
	v_pk_mul_f32 v[44:45], v[32:33], v[32:33]
	v_pk_mul_f32 v[40:41], v[72:73], v[40:41]
	v_pk_fma_f32 v[44:45], v[16:17], v[16:17], v[44:45]
	v_pk_mul_f32 v[38:39], v[40:41], v[38:39]
	v_or_b32_e32 v204, s74, v116
	v_pk_mul_f32 v[36:37], v[36:37], v[38:39]
	v_lshlrev_b32_e32 v38, 16, v205
	v_and_b32_e32 v39, 0xffff0000, v205
	v_mul_f32_e32 v40, 0xbfb8aa3b, v38
	v_exp_f32_e32 v40, v40
	v_mul_f32_e32 v41, 0xbfb8aa3b, v39
	v_exp_f32_e32 v41, v41
	v_cvt_pk_bf16_f32 v36, v36, v37
	v_add_f32_e32 v37, 1.0, v40
	v_rcp_f32_e32 v40, v37
	v_add_f32_e32 v37, 1.0, v41
	v_rcp_f32_e32 v41, v37
	v_pk_mul_f32 v[38:39], v[42:43], v[38:39]
	v_mov_b32_e32 v207, s75
	v_mov_b32_e32 v205, s75
	v_pk_mul_f32 v[38:39], v[40:41], v[38:39]
	s_waitcnt vmcnt(10)
	v_lshlrev_b32_e32 v40, 16, v194
	v_mul_f32_e32 v37, 0xbfb8aa3b, v40
	v_exp_f32_e32 v42, v37
	v_cvt_pk_bf16_f32 v37, v38, v39
	v_and_b32_e32 v41, 0xffff0000, v194
	global_store_dwordx2 v[178:179], v[36:37], off offset:1120
	v_mul_f32_e32 v37, 0xbfb8aa3b, v41
	v_exp_f32_e32 v37, v37
	v_pk_mul_f32 v[38:39], v[48:49], v[2:3] op_sel_hi:[1,0]
	v_add_f32_e32 v36, 1.0, v42
	v_pk_mul_f32 v[38:39], v[68:69], v[38:39]
	v_add_f32_e32 v37, 1.0, v37
	v_pk_mul_f32 v[38:39], v[38:39], v[40:41]
	v_lshlrev_b32_e32 v40, 16, v195
	v_rcp_f32_e32 v36, v36
	v_rcp_f32_e32 v37, v37
	v_mul_f32_e32 v41, 0xbfb8aa3b, v40
	v_exp_f32_e32 v42, v41
	v_and_b32_e32 v41, 0xffff0000, v195
	v_pk_mul_f32 v[36:37], v[36:37], v[38:39]
	v_mul_f32_e32 v39, v21, v21
	v_cvt_pk_bf16_f32 v36, v36, v37
	v_add_f32_e32 v37, 1.0, v42
	v_rcp_f32_e32 v38, v37
	v_mul_f32_e32 v37, v20, v20
	v_fmac_f32_e32 v37, v4, v4
	v_fmac_f32_e32 v39, v5, v5
	v_add_f32_e32 v37, v37, v39
	v_mul_f32_e32 v39, v22, v22
	v_fmac_f32_e32 v39, v6, v6
	v_add_f32_e32 v37, v39, v37
	v_mul_f32_e32 v39, v23, v23
	v_fmac_f32_e32 v39, v7, v7
	v_add_f32_e32 v37, v39, v37
	v_mul_f32_e32 v39, v24, v24
	v_fmac_f32_e32 v39, v8, v8
	v_add_f32_e32 v37, v39, v37
	v_mul_f32_e32 v39, v25, v25
	v_fmac_f32_e32 v39, v9, v9
	v_add_f32_e32 v37, v39, v37
	v_mul_f32_e32 v39, v26, v26
	v_fmac_f32_e32 v39, v10, v10
	v_add_f32_e32 v37, v39, v37
	v_mul_f32_e32 v39, v27, v27
	v_fmac_f32_e32 v39, v11, v11
	v_add_f32_e32 v37, v39, v37
	v_mul_f32_e32 v39, v28, v28
	v_fmac_f32_e32 v39, v12, v12
	v_add_f32_e32 v37, v39, v37
	v_mul_f32_e32 v39, v29, v29
	v_fmac_f32_e32 v39, v13, v13
	v_pk_mul_f32 v[42:43], v[30:31], v[30:31]
	v_add_f32_e32 v37, v39, v37
	v_pk_fma_f32 v[42:43], v[14:15], v[14:15], v[42:43]
	v_or_b32_e32 v194, s74, v118
	v_add_f32_e32 v37, v42, v37
	v_add_f32_e32 v37, v43, v37
	v_add_f32_e32 v37, v44, v37
	v_add_f32_e32 v37, v45, v37
	v_add_f32_e32 v37, v46, v37
	v_add_f32_e32 v37, v47, v37
	ds_bpermute_b32 v39, v109, v37
	v_pk_mul_f32 v[42:43], v[50:51], v[2:3] op_sel_hi:[1,0]
	v_mul_f32_e32 v2, 0xbfb8aa3b, v41
	v_exp_f32_e32 v2, v2
	v_pk_mul_f32 v[42:43], v[70:71], v[42:43]
	s_waitcnt lgkmcnt(0)
	v_add_f32_e32 v37, v37, v39
	v_fmamk_f32 v37, v37, 0x3c800000, v1
	v_mul_f32_e32 v39, 0x4f800000, v37
	v_cmp_gt_f32_e32 vcc, s29, v37
	v_add_f32_e32 v2, 1.0, v2
	v_pk_mul_f32 v[40:41], v[42:43], v[40:41]
	v_cndmask_b32_e32 v37, v37, v39, vcc
	v_sqrt_f32_e32 v44, v37
	v_rcp_f32_e32 v39, v2
	v_mov_b32_e32 v195, s75
	v_add_u32_e32 v2, -1, v44
	v_fma_f32 v42, -v2, v44, v37
	v_cmp_ge_f32_e64 s[38:39], 0, v42
	v_add_u32_e32 v42, 1, v44
	v_fma_f32 v43, -v42, v44, v37
	v_cndmask_b32_e64 v2, v44, v2, s[38:39]
	v_cmp_lt_f32_e64 s[38:39], 0, v43
	v_pk_mul_f32 v[38:39], v[38:39], v[40:41]
	s_nop 0
	v_cndmask_b32_e64 v2, v2, v42, s[38:39]
	v_mul_f32_e32 v42, 0x37800000, v2
	v_cndmask_b32_e32 v2, v2, v42, vcc
	v_cmp_class_f32_e32 vcc, v37, v248
	s_nop 1
	v_cndmask_b32_e32 v2, v2, v37, vcc
	v_div_scale_f32 v42, s[8:9], v2, v2, 1.0
	v_rcp_f32_e32 v43, v42
	v_cvt_pk_bf16_f32 v37, v38, v39
	global_store_dwordx2 v[178:179], v[36:37], off offset:1136
	v_and_b32_e32 v39, 0xffff0000, v192
	v_fma_f32 v36, -v42, v43, 1.0
	v_fmac_f32_e32 v43, v36, v43
	v_div_scale_f32 v36, vcc, 1.0, v2, 1.0
	v_mul_f32_e32 v37, v36, v43
	v_fma_f32 v38, -v42, v37, v36
	v_fmac_f32_e32 v37, v38, v43
	v_lshlrev_b32_e32 v38, 16, v192
	v_mul_f32_e32 v40, 0xbfb8aa3b, v38
	v_mul_f32_e32 v41, 0xbfb8aa3b, v39
	v_exp_f32_e32 v40, v40
	v_exp_f32_e32 v41, v41
	v_fma_f32 v36, -v42, v37, v36
	v_div_fmas_f32 v36, v36, v43, v37
	v_add_f32_e32 v40, 1.0, v40
	v_add_f32_e32 v41, 1.0, v41
	v_div_fixup_f32 v2, v36, v2, 1.0
	v_rcp_f32_e32 v40, v40
	v_rcp_f32_e32 v41, v41
	v_pk_mul_f32 v[4:5], v[4:5], v[2:3] op_sel_hi:[1,0]
	v_pk_mul_f32 v[6:7], v[6:7], v[2:3] op_sel_hi:[1,0]
	v_pk_mul_f32 v[4:5], v[96:97], v[4:5]
	v_pk_mul_f32 v[6:7], v[98:99], v[6:7]
	v_pk_mul_f32 v[4:5], v[4:5], v[38:39]
	v_lshlrev_b32_e32 v38, 16, v193
	v_pk_mul_f32 v[4:5], v[40:41], v[4:5]
	v_and_b32_e32 v39, 0xffff0000, v193
	v_mul_f32_e32 v40, 0xbfb8aa3b, v38
	v_exp_f32_e32 v40, v40
	v_mul_f32_e32 v41, 0xbfb8aa3b, v39
	v_exp_f32_e32 v41, v41
	v_cvt_pk_bf16_f32 v4, v4, v5
	v_add_f32_e32 v5, 1.0, v40
	v_rcp_f32_e32 v40, v5
	v_add_f32_e32 v5, 1.0, v41
	v_rcp_f32_e32 v41, v5
	v_pk_mul_f32 v[6:7], v[6:7], v[38:39]
	v_lshlrev_b64 v[36:37], 11, v[176:177]
	v_lshl_add_u64 v[36:37], s[70:71], 0, v[36:37]
	v_pk_mul_f32 v[6:7], v[40:41], v[6:7]
	v_lshl_add_u64 v[36:37], v[36:37], 0, v[190:191]
	v_cvt_pk_bf16_f32 v5, v6, v7
	v_lshlrev_b32_e32 v6, 16, v188
	v_and_b32_e32 v7, 0xffff0000, v188
	v_mul_f32_e32 v38, 0xbfb8aa3b, v6
	v_mul_f32_e32 v39, 0xbfb8aa3b, v7
	v_exp_f32_e32 v38, v38
	v_exp_f32_e32 v39, v39
	global_store_dwordx2 v[36:37], v[4:5], off offset:1024
	v_pk_mul_f32 v[8:9], v[8:9], v[2:3] op_sel_hi:[1,0]
	v_add_f32_e32 v4, 1.0, v38
	v_add_f32_e32 v5, 1.0, v39
	v_rcp_f32_e32 v4, v4
	v_rcp_f32_e32 v5, v5
	v_pk_mul_f32 v[8:9], v[92:93], v[8:9]
	v_pk_mul_f32 v[10:11], v[10:11], v[2:3] op_sel_hi:[1,0]
	v_pk_mul_f32 v[6:7], v[8:9], v[6:7]
	v_pk_mul_f32 v[10:11], v[94:95], v[10:11]
	v_pk_mul_f32 v[4:5], v[4:5], v[6:7]
	v_lshlrev_b32_e32 v6, 16, v189
	v_and_b32_e32 v7, 0xffff0000, v189
	v_mul_f32_e32 v8, 0xbfb8aa3b, v6
	v_exp_f32_e32 v8, v8
	v_mul_f32_e32 v9, 0xbfb8aa3b, v7
	v_exp_f32_e32 v9, v9
	v_cvt_pk_bf16_f32 v4, v4, v5
	v_add_f32_e32 v5, 1.0, v8
	v_rcp_f32_e32 v8, v5
	v_add_f32_e32 v5, 1.0, v9
	v_rcp_f32_e32 v9, v5
	v_pk_mul_f32 v[6:7], v[10:11], v[6:7]
	v_pk_mul_f32 v[10:11], v[14:15], v[2:3] op_sel_hi:[1,0]
	s_add_u32 s8, s86, s10
	v_pk_mul_f32 v[6:7], v[8:9], v[6:7]
	v_pk_mul_f32 v[10:11], v[90:91], v[10:11]
	v_cvt_pk_bf16_f32 v5, v6, v7
	v_lshlrev_b32_e32 v6, 16, v184
	v_and_b32_e32 v7, 0xffff0000, v184
	v_mul_f32_e32 v8, 0xbfb8aa3b, v6
	v_mul_f32_e32 v9, 0xbfb8aa3b, v7
	v_exp_f32_e32 v8, v8
	v_exp_f32_e32 v9, v9
	global_store_dwordx2 v[36:37], v[4:5], off offset:1040
	s_addc_u32 s9, s87, s11
	v_add_f32_e32 v4, 1.0, v8
	v_add_f32_e32 v5, 1.0, v9
	v_rcp_f32_e32 v4, v4
	v_rcp_f32_e32 v5, v5
	v_pk_mul_f32 v[8:9], v[12:13], v[2:3] op_sel_hi:[1,0]
	v_or_b32_e32 v184, s74, v128
	v_pk_mul_f32 v[8:9], v[88:89], v[8:9]
	v_or_b32_e32 v178, s74, v134
	v_pk_mul_f32 v[6:7], v[8:9], v[6:7]
	v_or_b32_e32 v176, s74, v136
	v_pk_mul_f32 v[4:5], v[4:5], v[6:7]
	v_lshlrev_b32_e32 v6, 16, v185
	v_and_b32_e32 v7, 0xffff0000, v185
	v_mul_f32_e32 v8, 0xbfb8aa3b, v6
	v_exp_f32_e32 v8, v8
	v_mul_f32_e32 v9, 0xbfb8aa3b, v7
	v_exp_f32_e32 v9, v9
	v_cvt_pk_bf16_f32 v4, v4, v5
	v_add_f32_e32 v5, 1.0, v8
	v_rcp_f32_e32 v8, v5
	v_add_f32_e32 v5, 1.0, v9
	v_rcp_f32_e32 v9, v5
	v_pk_mul_f32 v[6:7], v[10:11], v[6:7]
	v_pk_mul_f32 v[10:11], v[18:19], v[2:3] op_sel_hi:[1,0]
	v_or_b32_e32 v192, s74, v120
	v_pk_mul_f32 v[6:7], v[8:9], v[6:7]
	v_pk_mul_f32 v[10:11], v[82:83], v[10:11]
	v_cvt_pk_bf16_f32 v5, v6, v7
	v_lshlrev_b32_e32 v6, 16, v180
	v_and_b32_e32 v7, 0xffff0000, v180
	v_mul_f32_e32 v8, 0xbfb8aa3b, v6
	v_mul_f32_e32 v9, 0xbfb8aa3b, v7
	v_exp_f32_e32 v8, v8
	v_exp_f32_e32 v9, v9
	global_store_dwordx2 v[36:37], v[4:5], off offset:1056
	v_or_b32_e32 v180, s74, v132
	v_add_f32_e32 v4, 1.0, v8
	v_add_f32_e32 v5, 1.0, v9
	v_rcp_f32_e32 v4, v4
	v_rcp_f32_e32 v5, v5
	v_pk_mul_f32 v[8:9], v[16:17], v[2:3] op_sel_hi:[1,0]
	v_or_b32_e32 v190, s74, v122
	v_pk_mul_f32 v[8:9], v[80:81], v[8:9]
	v_or_b32_e32 v188, s74, v124
	v_pk_mul_f32 v[6:7], v[8:9], v[6:7]
	v_mov_b32_e32 v193, s75
	v_pk_mul_f32 v[4:5], v[4:5], v[6:7]
	v_lshlrev_b32_e32 v6, 16, v181
	v_and_b32_e32 v7, 0xffff0000, v181
	v_mul_f32_e32 v8, 0xbfb8aa3b, v6
	v_exp_f32_e32 v8, v8
	v_mul_f32_e32 v9, 0xbfb8aa3b, v7
	v_exp_f32_e32 v9, v9
	v_cvt_pk_bf16_f32 v4, v4, v5
	v_add_f32_e32 v5, 1.0, v8
	v_rcp_f32_e32 v8, v5
	v_add_f32_e32 v5, 1.0, v9
	v_rcp_f32_e32 v9, v5
	v_pk_mul_f32 v[6:7], v[10:11], v[6:7]
	v_pk_mul_f32 v[10:11], v[22:23], v[2:3] op_sel_hi:[1,0]
	v_mov_b32_e32 v191, s75
	v_pk_mul_f32 v[6:7], v[8:9], v[6:7]
	v_pk_mul_f32 v[10:11], v[86:87], v[10:11]
	v_cvt_pk_bf16_f32 v5, v6, v7
	s_waitcnt vmcnt(14)
	v_lshlrev_b32_e32 v6, 16, v186
	v_and_b32_e32 v7, 0xffff0000, v186
	v_mul_f32_e32 v8, 0xbfb8aa3b, v6
	v_mul_f32_e32 v9, 0xbfb8aa3b, v7
	v_exp_f32_e32 v8, v8
	v_exp_f32_e32 v9, v9
	global_store_dwordx2 v[36:37], v[4:5], off offset:1072
	v_or_b32_e32 v186, s74, v126
	v_add_f32_e32 v4, 1.0, v8
	v_add_f32_e32 v5, 1.0, v9
	v_rcp_f32_e32 v4, v4
	v_rcp_f32_e32 v5, v5
	v_pk_mul_f32 v[8:9], v[20:21], v[2:3] op_sel_hi:[1,0]
	v_mov_b32_e32 v189, s75
	v_pk_mul_f32 v[8:9], v[84:85], v[8:9]
	s_nop 0
	v_pk_mul_f32 v[6:7], v[8:9], v[6:7]
	s_nop 0
	v_pk_mul_f32 v[4:5], v[4:5], v[6:7]
	v_lshlrev_b32_e32 v6, 16, v187
	v_and_b32_e32 v7, 0xffff0000, v187
	v_mul_f32_e32 v8, 0xbfb8aa3b, v6
	v_exp_f32_e32 v8, v8
	v_mul_f32_e32 v9, 0xbfb8aa3b, v7
	v_exp_f32_e32 v9, v9
	v_cvt_pk_bf16_f32 v4, v4, v5
	v_add_f32_e32 v5, 1.0, v8
	v_rcp_f32_e32 v8, v5
	v_add_f32_e32 v5, 1.0, v9
	v_rcp_f32_e32 v9, v5
	v_pk_mul_f32 v[6:7], v[10:11], v[6:7]
	v_pk_mul_f32 v[10:11], v[26:27], v[2:3] op_sel_hi:[1,0]
	v_mov_b32_e32 v187, s75
	v_pk_mul_f32 v[6:7], v[8:9], v[6:7]
	v_pk_mul_f32 v[10:11], v[78:79], v[10:11]
	v_cvt_pk_bf16_f32 v5, v6, v7
	s_waitcnt vmcnt(14)
	v_lshlrev_b32_e32 v6, 16, v182
	v_and_b32_e32 v7, 0xffff0000, v182
	v_mul_f32_e32 v8, 0xbfb8aa3b, v6
	v_mul_f32_e32 v9, 0xbfb8aa3b, v7
	v_exp_f32_e32 v8, v8
	v_exp_f32_e32 v9, v9
	global_store_dwordx2 v[36:37], v[4:5], off offset:1088
	v_or_b32_e32 v182, s74, v130
	v_add_f32_e32 v4, 1.0, v8
	v_add_f32_e32 v5, 1.0, v9
	v_rcp_f32_e32 v4, v4
	v_rcp_f32_e32 v5, v5
	v_pk_mul_f32 v[8:9], v[24:25], v[2:3] op_sel_hi:[1,0]
	s_nop 0
	v_pk_mul_f32 v[8:9], v[76:77], v[8:9]
	s_nop 0
	v_pk_mul_f32 v[6:7], v[8:9], v[6:7]
	s_nop 0
	v_pk_mul_f32 v[4:5], v[4:5], v[6:7]
	v_lshlrev_b32_e32 v6, 16, v183
	v_and_b32_e32 v7, 0xffff0000, v183
	v_mul_f32_e32 v8, 0xbfb8aa3b, v6
	v_exp_f32_e32 v8, v8
	v_mul_f32_e32 v9, 0xbfb8aa3b, v7
	v_exp_f32_e32 v9, v9
	v_cvt_pk_bf16_f32 v4, v4, v5
	v_add_f32_e32 v5, 1.0, v8
	v_rcp_f32_e32 v8, v5
	v_add_f32_e32 v5, 1.0, v9
	v_rcp_f32_e32 v9, v5
	v_pk_mul_f32 v[6:7], v[10:11], v[6:7]
	v_pk_mul_f32 v[10:11], v[30:31], v[2:3] op_sel_hi:[1,0]
	v_pk_mul_f32 v[6:7], v[8:9], v[6:7]
	s_nop 0
	v_cvt_pk_bf16_f32 v5, v6, v7
	s_waitcnt vmcnt(14)
	v_lshlrev_b32_e32 v6, 16, v102
	v_and_b32_e32 v7, 0xffff0000, v102
	v_mul_f32_e32 v8, 0xbfb8aa3b, v6
	v_mul_f32_e32 v9, 0xbfb8aa3b, v7
	v_exp_f32_e32 v8, v8
	v_exp_f32_e32 v9, v9
	global_store_dwordx2 v[36:37], v[4:5], off offset:1104
	v_pk_mul_f32 v[10:11], v[74:75], v[10:11]
	v_add_f32_e32 v4, 1.0, v8
	v_add_f32_e32 v5, 1.0, v9
	v_rcp_f32_e32 v4, v4
	v_rcp_f32_e32 v5, v5
	v_pk_mul_f32 v[8:9], v[28:29], v[2:3] op_sel_hi:[1,0]
	s_nop 0
	v_pk_mul_f32 v[8:9], v[72:73], v[8:9]
	s_nop 0
	v_pk_mul_f32 v[6:7], v[8:9], v[6:7]
	s_nop 0
	v_pk_mul_f32 v[4:5], v[4:5], v[6:7]
	v_lshlrev_b32_e32 v6, 16, v103
	v_and_b32_e32 v7, 0xffff0000, v103
	v_mul_f32_e32 v8, 0xbfb8aa3b, v6
	v_exp_f32_e32 v8, v8
	v_mul_f32_e32 v9, 0xbfb8aa3b, v7
	v_exp_f32_e32 v9, v9
	v_cvt_pk_bf16_f32 v4, v4, v5
	v_add_f32_e32 v5, 1.0, v8
	v_rcp_f32_e32 v8, v5
	v_add_f32_e32 v5, 1.0, v9
	v_rcp_f32_e32 v9, v5
	v_pk_mul_f32 v[6:7], v[10:11], v[6:7]
	v_pk_mul_f32 v[10:11], v[34:35], v[2:3] op_sel_hi:[1,0]
	v_pk_mul_f32 v[6:7], v[8:9], v[6:7]
	s_nop 0
	v_cvt_pk_bf16_f32 v5, v6, v7
	s_waitcnt vmcnt(14)
	v_lshlrev_b32_e32 v6, 16, v100
	v_and_b32_e32 v7, 0xffff0000, v100
	v_mul_f32_e32 v8, 0xbfb8aa3b, v6
	v_mul_f32_e32 v9, 0xbfb8aa3b, v7
	v_exp_f32_e32 v8, v8
	v_exp_f32_e32 v9, v9
	global_store_dwordx2 v[36:37], v[4:5], off offset:1120
	v_pk_mul_f32 v[10:11], v[70:71], v[10:11]
	v_add_f32_e32 v4, 1.0, v8
	v_add_f32_e32 v5, 1.0, v9
	v_rcp_f32_e32 v4, v4
	v_rcp_f32_e32 v5, v5
	v_pk_mul_f32 v[8:9], v[32:33], v[2:3] op_sel_hi:[1,0]
	s_nop 0
	v_pk_mul_f32 v[8:9], v[68:69], v[8:9]
	s_nop 0
	v_pk_mul_f32 v[6:7], v[8:9], v[6:7]
	s_nop 0
	v_pk_mul_f32 v[4:5], v[4:5], v[6:7]
	v_lshlrev_b32_e32 v6, 16, v101
	v_and_b32_e32 v7, 0xffff0000, v101
	v_mul_f32_e32 v8, 0xbfb8aa3b, v6
	v_exp_f32_e32 v8, v8
	v_mul_f32_e32 v9, 0xbfb8aa3b, v7
	v_exp_f32_e32 v9, v9
	v_cvt_pk_bf16_f32 v4, v4, v5
	v_add_f32_e32 v5, 1.0, v8
	v_rcp_f32_e32 v8, v5
	v_add_f32_e32 v5, 1.0, v9
	v_rcp_f32_e32 v9, v5
	v_pk_mul_f32 v[6:7], v[10:11], v[6:7]
	s_nop 0
	v_pk_mul_f32 v[6:7], v[8:9], v[6:7]
	s_nop 0
	v_cvt_pk_bf16_f32 v5, v6, v7
	global_store_dwordx2 v[36:37], v[4:5], off offset:1136
	s_waitcnt lgkmcnt(0)
	s_load_dwordx2 s[8:9], s[8:9], 0x98
	s_waitcnt lgkmcnt(0)
	s_add_u32 s38, s8, s20
	s_addc_u32 s39, s9, s21
	s_lshl_b64 s[40:41], s[14:15], 12
	v_or_b32_e32 v2, s40, v108
	v_mov_b32_e32 v5, s41
	v_or_b32_e32 v4, v2, v106
	v_mov_b32_e32 v21, s41
	v_or_b32_e32 v20, v2, v110
	v_lshlrev_b64 v[16:17], 1, v[4:5]
	v_lshlrev_b64 v[20:21], 1, v[20:21]
	v_lshl_add_u64 v[4:5], s[16:17], 0, v[16:17]
	v_lshl_add_u64 v[22:23], s[16:17], 0, v[20:21]
	global_load_dwordx4 v[4:7], v[4:5], off nt
	v_lshl_add_u64 v[8:9], s[12:13], 0, v[16:17]
	global_load_dwordx4 v[68:71], v[22:23], off nt
	v_lshl_add_u64 v[22:23], s[12:13], 0, v[20:21]
	global_load_dwordx4 v[8:11], v[8:9], off nt
	v_readlane_b32 s8, v253, 22
	global_load_dwordx4 v[72:75], v[22:23], off nt
	v_readlane_b32 s9, v253, 23
	v_lshl_add_u64 v[12:13], s[60:61], 0, v[16:17]
	global_load_dwordx4 v[12:15], v[12:13], off nt
	v_lshl_add_u64 v[22:23], s[8:9], 0, v[20:21]
	v_lshl_add_u64 v[20:21], s[60:61], 0, v[20:21]
	global_load_dwordx4 v[76:79], v[20:21], off nt
	v_lshl_add_u64 v[16:17], s[8:9], 0, v[16:17]
	global_load_dwordx4 v[16:19], v[16:17], off nt
	s_waitcnt vmcnt(4)
	v_mfma_f32_32x32x16_bf16 v[36:51], v[4:7], v[8:11], 0
	global_load_dwordx4 v[80:83], v[22:23], off nt
	v_or_b32_e32 v90, 16, v2
	v_or_b32_e32 v102, 32, v2
	v_or_b32_e32 v2, 48, v2
	s_lshl_b32 s7, s14, 7
	s_and_b32 s56, s7, 0x180
	s_add_i32 s14, s14, s90
	s_waitcnt vmcnt(4)
	v_mfma_f32_32x32x16_bf16 v[52:67], v[4:7], v[72:75], 0
	v_mov_b32_e32 v5, s41
	v_or_b32_e32 v4, v90, v106
	v_lshlrev_b64 v[88:89], 1, v[4:5]
	v_lshl_add_u64 v[4:5], s[16:17], 0, v[88:89]
	global_load_dwordx4 v[84:87], v[4:5], off nt
	s_cmpk_gt_i32 s14, 0x7ff
	v_mfma_f32_32x32x16_bf16 v[20:35], v[68:71], v[8:11], 0
	s_waitcnt vmcnt(2)
	v_mfma_f32_32x32x16_bf16 v[36:51], v[12:15], v[16:19], v[36:51]
	s_waitcnt vmcnt(1)
	v_mfma_f32_32x32x16_bf16 v[52:67], v[12:15], v[80:83], v[52:67]
	v_mfma_f32_32x32x16_bf16 v[20:35], v[76:79], v[16:19], v[20:35]
	v_mfma_f32_32x32x16_bf16 v[4:19], v[68:71], v[72:75], 0
	v_lshl_add_u64 v[68:69], s[12:13], 0, v[88:89]
	v_lshl_add_u64 v[72:73], s[60:61], 0, v[88:89]
	global_load_dwordx4 v[68:71], v[68:69], off nt
	s_nop 0
	global_load_dwordx4 v[72:75], v[72:73], off nt
	v_mfma_f32_32x32x16_bf16 v[4:19], v[76:79], v[80:83], v[4:19]
	v_mov_b32_e32 v81, s41
	v_or_b32_e32 v80, v90, v110
	v_lshlrev_b64 v[92:93], 1, v[80:81]
	v_lshl_add_u64 v[76:77], s[8:9], 0, v[88:89]
	v_lshl_add_u64 v[88:89], s[12:13], 0, v[92:93]
	global_load_dwordx4 v[88:91], v[88:89], off nt
	v_lshl_add_u64 v[80:81], s[16:17], 0, v[92:93]
	global_load_dwordx4 v[76:79], v[76:77], off nt
	v_lshl_add_u64 v[96:97], s[8:9], 0, v[92:93]
	global_load_dwordx4 v[80:83], v[80:81], off nt
	v_lshl_add_u64 v[92:93], s[60:61], 0, v[92:93]
	global_load_dwordx4 v[92:95], v[92:93], off nt
	s_waitcnt vmcnt(5)
	v_mfma_f32_32x32x16_bf16 v[36:51], v[84:87], v[68:71], v[36:51]
	s_waitcnt vmcnt(3)
	v_mfma_f32_32x32x16_bf16 v[52:67], v[84:87], v[88:91], v[52:67]
	global_load_dwordx4 v[84:87], v[96:97], off nt
	v_mov_b32_e32 v97, s41
	v_or_b32_e32 v96, v102, v106
	v_lshlrev_b64 v[100:101], 1, v[96:97]
	v_lshl_add_u64 v[96:97], s[16:17], 0, v[100:101]
	global_load_dwordx4 v[96:99], v[96:97], off nt
	s_waitcnt vmcnt(3)
	v_mfma_f32_32x32x16_bf16 v[20:35], v[80:83], v[68:71], v[20:35]
	v_lshl_add_u64 v[68:69], s[12:13], 0, v[100:101]
	global_load_dwordx4 v[68:71], v[68:69], off nt
	v_mfma_f32_32x32x16_bf16 v[4:19], v[80:83], v[88:91], v[4:19]
	v_mov_b32_e32 v81, s41
	v_or_b32_e32 v80, v102, v110
	v_lshlrev_b64 v[88:89], 1, v[80:81]
	v_lshl_add_u64 v[80:81], s[16:17], 0, v[88:89]
	global_load_dwordx4 v[80:83], v[80:81], off nt
	v_or_b32_e32 v102, s74, v138
	v_mfma_f32_32x32x16_bf16 v[36:51], v[72:75], v[76:79], v[36:51]
	s_waitcnt vmcnt(4)
	v_mfma_f32_32x32x16_bf16 v[20:35], v[92:95], v[76:79], v[20:35]
	v_lshl_add_u64 v[76:77], s[8:9], 0, v[100:101]
	global_load_dwordx4 v[76:79], v[76:77], off nt
	s_waitcnt vmcnt(4)
	v_mfma_f32_32x32x16_bf16 v[52:67], v[72:75], v[84:87], v[52:67]
	v_lshl_add_u64 v[72:73], s[60:61], 0, v[100:101]
	global_load_dwordx4 v[72:75], v[72:73], off nt
	v_mfma_f32_32x32x16_bf16 v[4:19], v[92:95], v[84:87], v[4:19]
	v_lshl_add_u64 v[84:85], s[12:13], 0, v[88:89]
	global_load_dwordx4 v[84:87], v[84:85], off nt
	v_lshl_add_u64 v[92:93], s[8:9], 0, v[88:89]
	v_lshl_add_u64 v[88:89], s[60:61], 0, v[88:89]
	global_load_dwordx4 v[88:91], v[88:89], off nt
	s_nop 0
	global_load_dwordx4 v[92:95], v[92:93], off nt
	s_waitcnt vmcnt(5)
	v_mfma_f32_32x32x16_bf16 v[20:35], v[80:83], v[68:71], v[20:35]
	s_waitcnt vmcnt(2)
	v_mfma_f32_32x32x16_bf16 v[4:19], v[80:83], v[84:87], v[4:19]
	v_mov_b32_e32 v81, s41
	v_or_b32_e32 v80, v2, v110
	v_mfma_f32_32x32x16_bf16 v[36:51], v[96:99], v[68:71], v[36:51]
	v_mfma_f32_32x32x16_bf16 v[52:67], v[96:99], v[84:87], v[52:67]
	v_mov_b32_e32 v97, s41
	v_or_b32_e32 v96, v2, v106
	v_lshlrev_b64 v[100:101], 1, v[96:97]
	v_lshl_add_u64 v[96:97], s[16:17], 0, v[100:101]
	global_load_dwordx4 v[96:99], v[96:97], off nt
	v_lshl_add_u64 v[68:69], s[12:13], 0, v[100:101]
	global_load_dwordx4 v[68:71], v[68:69], off nt
	s_waitcnt vmcnt(3)
	v_mfma_f32_32x32x16_bf16 v[20:35], v[88:91], v[76:79], v[20:35]
	v_lshlrev_b32_e32 v2, 2, v104
	s_waitcnt vmcnt(2)
	v_mfma_f32_32x32x16_bf16 v[4:19], v[88:91], v[92:95], v[4:19]
	v_lshlrev_b64 v[88:89], 1, v[80:81]
	v_lshl_add_u64 v[80:81], s[16:17], 0, v[88:89]
	global_load_dwordx4 v[80:83], v[80:81], off nt
	v_lshl_add_u64 v[84:85], s[12:13], 0, v[88:89]
	global_load_dwordx4 v[84:87], v[84:85], off nt
	v_mfma_f32_32x32x16_bf16 v[36:51], v[72:75], v[76:79], v[36:51]
	v_lshl_add_u64 v[76:77], s[8:9], 0, v[100:101]
	global_load_dwordx4 v[76:79], v[76:77], off nt
	v_mfma_f32_32x32x16_bf16 v[52:67], v[72:75], v[92:95], v[52:67]
	v_lshl_add_u64 v[72:73], s[60:61], 0, v[100:101]
	global_load_dwordx4 v[72:75], v[72:73], off nt
	v_lshl_add_u64 v[92:93], s[8:9], 0, v[88:89]
	v_lshl_add_u64 v[88:89], s[60:61], 0, v[88:89]
	global_load_dwordx4 v[92:95], v[92:93], off nt
	v_or_b32_e32 v100, s74, v140
	global_load_dwordx4 v[88:91], v[88:89], off nt
	s_waitcnt vmcnt(4)
	v_mfma_f32_32x32x16_bf16 v[52:67], v[96:99], v[84:87], v[52:67]
	global_load_dword v111, v2, s[38:39]
	global_load_dword v109, v107, s[38:39]
	v_lshlrev_b32_e32 v2, 1, v104
	v_mfma_f32_32x32x16_bf16 v[4:19], v[80:83], v[84:87], v[4:19]
	v_mad_u64_u32 v[84:85], s[8:9], v184, s2, v[210:211]
	v_mad_i32_i24 v85, s75, v202, v85
	v_lshl_add_u64 v[84:85], v[84:85], 0, s[56:57]
	v_lshl_add_u64 v[86:87], v[84:85], 0, v[2:3]
	v_mad_u64_u32 v[84:85], s[8:9], v182, s2, v[210:211]
	v_mad_i32_i24 v85, s75, v202, v85
	v_lshl_add_u64 v[84:85], v[84:85], 0, s[56:57]
	v_lshl_add_u64 v[212:213], v[84:85], 0, v[2:3]
	v_mad_u64_u32 v[84:85], s[8:9], v180, s2, v[210:211]
	v_mfma_f32_32x32x16_bf16 v[36:51], v[96:99], v[68:71], v[36:51]
	v_mad_i32_i24 v85, s75, v202, v85
	v_lshl_add_u64 v[84:85], v[84:85], 0, s[56:57]
	v_lshl_add_u64 v[214:215], v[84:85], 0, v[2:3]
	v_mad_u64_u32 v[84:85], s[8:9], v178, s2, v[210:211]
	v_mad_i32_i24 v85, s75, v202, v85
	v_lshl_add_u64 v[84:85], v[84:85], 0, s[56:57]
	v_mfma_f32_32x32x16_bf16 v[20:35], v[80:83], v[68:71], v[20:35]
	v_lshl_add_u64 v[216:217], v[84:85], 0, v[2:3]
	v_mad_u64_u32 v[84:85], s[8:9], v176, s2, v[210:211]
	v_mad_i32_i24 v85, s75, v202, v85
	v_lshl_add_u64 v[84:85], v[84:85], 0, s[56:57]
	v_lshl_add_u64 v[218:219], v[84:85], 0, v[2:3]
	v_mad_u64_u32 v[84:85], s[8:9], v102, s2, v[210:211]
	s_waitcnt vmcnt(3)
	v_mfma_f32_32x32x16_bf16 v[52:67], v[72:75], v[92:95], v[52:67]
	v_mad_u64_u32 v[68:69], s[8:9], v208, s2, v[210:211]
	v_mad_i32_i24 v85, s75, v202, v85
	v_mad_i32_i24 v69, s75, v202, v69
	v_lshl_add_u64 v[84:85], v[84:85], 0, s[56:57]
	v_lshl_add_u64 v[68:69], v[68:69], 0, s[56:57]
	v_lshl_add_u64 v[220:221], v[84:85], 0, v[2:3]
	v_mfma_f32_32x32x16_bf16 v[36:51], v[72:75], v[76:79], v[36:51]
	v_mad_u64_u32 v[84:85], s[8:9], v100, s2, v[210:211]
	v_lshl_add_u64 v[74:75], v[68:69], 0, v[2:3]
	v_mad_i32_i24 v85, s75, v202, v85
	v_lshl_add_u64 v[84:85], v[84:85], 0, s[56:57]
	v_or_b32_e32 v96, s74, v142
	v_lshl_add_u64 v[222:223], v[84:85], 0, v[2:3]
	s_waitcnt vmcnt(2)
	v_mfma_f32_32x32x16_bf16 v[20:35], v[88:91], v[76:79], v[20:35]
	v_mad_u64_u32 v[84:85], s[8:9], v96, s2, v[210:211]
	v_mad_i32_i24 v85, s75, v202, v85
	v_lshl_add_u64 v[84:85], v[84:85], 0, s[56:57]
	v_lshl_add_u64 v[224:225], v[84:85], 0, v[2:3]
	v_or_b32_e32 v98, s74, v146
	v_mad_u64_u32 v[68:69], s[8:9], v206, s2, v[210:211]
	v_mfma_f32_32x32x16_bf16 v[4:19], v[88:91], v[92:95], v[4:19]
	v_xor_b32_e32 v88, 16, v250
	global_load_ushort v89, v[74:75], off offset:3072
	v_cmp_lt_i32_e32 vcc, v88, v113
	v_or_b32_e32 v90, s74, v144
	v_mad_u64_u32 v[84:85], s[8:9], v90, s2, v[210:211]
	v_cndmask_b32_e32 v88, v250, v88, vcc
	v_lshlrev_b32_e32 v113, 2, v88
	v_mul_f32_e32 v88, v52, v52
	v_fmac_f32_e32 v88, v36, v36
	v_mad_i32_i24 v85, s75, v202, v85
	v_lshl_add_u64 v[84:85], v[84:85], 0, s[56:57]
	v_add_f32_dpp v88, v88, v88 quad_perm:[1,0,3,2] row_mask:0xf bank_mask:0xf bound_ctrl:1
	v_lshl_add_u64 v[196:197], v[84:85], 0, v[2:3]
	v_mad_u64_u32 v[84:85], s[8:9], v98, s2, v[210:211]
	v_add_f32_dpp v88, v88, v88 quad_perm:[2,3,0,1] row_mask:0xf bank_mask:0xf bound_ctrl:1
	v_mad_i32_i24 v85, s75, v202, v85
	v_lshl_add_u64 v[84:85], v[84:85], 0, s[56:57]
	v_add_f32_dpp v88, v88, v88 row_half_mirror row_mask:0xf bank_mask:0xf bound_ctrl:1
	v_or_b32_e32 v94, s74, v148
	v_lshl_add_u64 v[198:199], v[84:85], 0, v[2:3]
	v_add_f32_dpp v88, v88, v88 row_mirror row_mask:0xf bank_mask:0xf bound_ctrl:1
	ds_bpermute_b32 v91, v113, v88
	v_mad_u64_u32 v[84:85], s[8:9], v94, s2, v[210:211]
	v_mad_i32_i24 v85, s75, v202, v85
	v_lshl_add_u64 v[84:85], v[84:85], 0, s[56:57]
	v_lshl_add_u64 v[232:233], v[84:85], 0, v[2:3]
	s_waitcnt lgkmcnt(0)
	v_add_f32_e32 v84, v88, v91
	v_fmamk_f32 v84, v84, 0x3c800000, v1
	v_mul_f32_e32 v85, 0x4f800000, v84
	v_cmp_gt_f32_e32 vcc, s29, v84
	v_or_b32_e32 v92, s74, v150
	v_mad_i32_i24 v69, s75, v202, v69
	v_cndmask_b32_e32 v88, v84, v85, vcc
	v_sqrt_f32_e32 v91, v88
	v_mad_u64_u32 v[84:85], s[8:9], v92, s2, v[210:211]
	v_mad_i32_i24 v85, s75, v202, v85
	v_add_u32_e32 v93, -1, v91
	v_fma_f32 v95, -v93, v91, v88
	v_cmp_ge_f32_e64 s[38:39], 0, v95
	v_add_u32_e32 v95, 1, v91
	v_lshl_add_u64 v[84:85], v[84:85], 0, s[56:57]
	v_cndmask_b32_e64 v93, v91, v93, s[38:39]
	v_fma_f32 v91, -v95, v91, v88
	v_cmp_lt_f32_e64 s[38:39], 0, v91
	v_lshl_add_u64 v[234:235], v[84:85], 0, v[2:3]
	v_lshl_add_u64 v[68:69], v[68:69], 0, s[56:57]
	v_cndmask_b32_e64 v91, v93, v95, s[38:39]
	v_mul_f32_e32 v93, 0x37800000, v91
	v_cndmask_b32_e32 v91, v91, v93, vcc
	v_cmp_class_f32_e32 vcc, v88, v248
	v_lshl_add_u64 v[70:71], v[68:69], 0, v[2:3]
	v_mad_u64_u32 v[68:69], s[8:9], v204, s2, v[210:211]
	v_cndmask_b32_e32 v91, v91, v88, vcc
	v_div_scale_f32 v93, s[8:9], v91, v91, 1.0
	v_rcp_f32_e32 v95, v93
	v_div_scale_f32 v97, vcc, 1.0, v91, 1.0
	v_mad_i32_i24 v69, s75, v202, v69
	v_fma_f32 v84, -v93, v95, 1.0
	v_fmac_f32_e32 v95, v84, v95
	v_mul_f32_e32 v99, v97, v95
	v_or_b32_e32 v88, s74, v152
	v_fma_f32 v84, -v93, v99, v97
	v_lshl_add_u64 v[68:69], v[68:69], 0, s[56:57]
	v_fmac_f32_e32 v99, v84, v95
	v_mad_u64_u32 v[84:85], s[8:9], v88, s2, v[210:211]
	v_lshl_add_u64 v[76:77], v[68:69], 0, v[2:3]
	v_mad_u64_u32 v[68:69], s[8:9], v194, s2, v[210:211]
	v_mad_i32_i24 v85, s75, v202, v85
	v_mad_i32_i24 v69, s75, v202, v69
	v_lshl_add_u64 v[84:85], v[84:85], 0, s[56:57]
	v_lshl_add_u64 v[68:69], v[68:69], 0, s[56:57]
	v_lshl_add_u64 v[236:237], v[84:85], 0, v[2:3]
	v_fma_f32 v84, -v93, v99, v97
	v_lshl_add_u64 v[80:81], v[68:69], 0, v[2:3]
	v_div_fmas_f32 v85, v84, v95, v99
	global_load_ushort v93, v[74:75], off offset:3136
	global_load_ushort v95, v[70:71], off offset:3072
	global_load_ushort v97, v[70:71], off offset:3136
	global_load_ushort v99, v[76:77], off offset:3072
	global_load_ushort v101, v[76:77], off offset:3136
	global_load_ushort v103, v[80:81], off offset:3072
	global_load_ushort v177, v[80:81], off offset:3136
	v_div_fixup_f32 v91, v85, v91, 1.0
	s_waitcnt vmcnt(7)
	v_lshlrev_b32_e32 v70, 16, v89
	v_mul_f32_e32 v36, v36, v91
	v_mad_u64_u32 v[68:69], s[8:9], v192, s2, v[210:211]
	v_mad_u64_u32 v[72:73], s[8:9], v190, s2, v[210:211]
	v_mad_u64_u32 v[78:79], s[8:9], v188, s2, v[210:211]
	v_or_b32_e32 v84, s74, v154
	v_mul_f32_e32 v36, v111, v36
	v_mul_f32_e32 v71, 0xbfb8aa3b, v70
	v_mad_i32_i24 v69, s75, v202, v69
	v_mad_i32_i24 v73, s75, v202, v73
	v_mad_i32_i24 v79, s75, v202, v79
	v_mad_u64_u32 v[82:83], s[8:9], v186, s2, v[210:211]
	v_exp_f32_e32 v74, v71
	v_mul_f32_e32 v36, v36, v70
	v_mad_u64_u32 v[70:71], s[8:9], v84, s2, v[210:211]
	v_lshl_add_u64 v[68:69], v[68:69], 0, s[56:57]
	v_lshl_add_u64 v[72:73], v[72:73], 0, s[56:57]
	v_lshl_add_u64 v[78:79], v[78:79], 0, s[56:57]
	v_mad_i32_i24 v83, s75, v202, v83
	v_mad_i32_i24 v71, s75, v202, v71
	v_lshl_add_u64 v[68:69], v[68:69], 0, v[2:3]
	v_lshl_add_u64 v[72:73], v[72:73], 0, v[2:3]
	v_lshl_add_u64 v[78:79], v[78:79], 0, v[2:3]
	v_lshl_add_u64 v[82:83], v[82:83], 0, s[56:57]
	v_lshl_add_u64 v[70:71], v[70:71], 0, s[56:57]
	v_lshl_add_u64 v[82:83], v[82:83], 0, v[2:3]
	v_lshl_add_u64 v[238:239], v[70:71], 0, v[2:3]
	global_load_ushort v179, v[68:69], off offset:3072
	global_load_ushort v181, v[68:69], off offset:3136
	global_load_ushort v183, v[72:73], off offset:3072
	global_load_ushort v185, v[72:73], off offset:3136
	global_load_ushort v85, v[78:79], off offset:3072
	global_load_ushort v81, v[78:79], off offset:3136
	s_nop 0
	global_load_ushort v79, v[82:83], off offset:3072
	global_load_ushort v77, v[82:83], off offset:3136
	global_load_ushort v75, v[86:87], off offset:3072
	global_load_ushort v73, v[86:87], off offset:3136
	global_load_ushort v71, v[212:213], off offset:3072
	global_load_ushort v69, v[212:213], off offset:3136
	global_load_ushort v230, v[214:215], off offset:3072
	global_load_ushort v229, v[214:215], off offset:3136
	global_load_ushort v228, v[216:217], off offset:3072
	global_load_ushort v227, v[216:217], off offset:3136
	global_load_ushort v226, v[218:219], off offset:3072
	s_nop 0
	global_load_ushort v218, v[218:219], off offset:3136
	s_nop 0
	global_load_ushort v217, v[220:221], off offset:3072
	global_load_ushort v216, v[220:221], off offset:3136
	global_load_ushort v215, v[222:223], off offset:3072
	global_load_ushort v214, v[222:223], off offset:3136
	global_load_ushort v213, v[224:225], off offset:3072
	global_load_ushort v212, v[224:225], off offset:3136
	global_load_ushort v203, v[196:197], off offset:3072
	global_load_ushort v175, v[196:197], off offset:3136
	global_load_ushort v173, v[198:199], off offset:3072
	global_load_ushort v171, v[198:199], off offset:3136
	global_load_ushort v169, v[232:233], off offset:3072
	global_load_ushort v167, v[232:233], off offset:3136
	global_load_ushort v165, v[234:235], off offset:3072
	global_load_ushort v163, v[234:235], off offset:3136
	global_load_ushort v161, v[236:237], off offset:3072
	global_load_ushort v159, v[236:237], off offset:3136
	global_load_ushort v157, v[238:239], off offset:3072
	global_load_ushort v155, v[238:239], off offset:3136
	v_or_b32_e32 v86, s74, v156
	v_mad_u64_u32 v[82:83], s[8:9], v86, s2, v[210:211]
	v_mad_i32_i24 v83, s75, v202, v83
	v_lshl_add_u64 v[82:83], v[82:83], 0, s[56:57]
	v_lshl_add_u64 v[82:83], v[82:83], 0, v[2:3]
	global_load_ushort v153, v[82:83], off offset:3072
	global_load_ushort v151, v[82:83], off offset:3136
	v_or_b32_e32 v82, s74, v158
	v_mad_u64_u32 v[196:197], s[8:9], v82, s2, v[210:211]
	v_mad_i32_i24 v197, s75, v202, v197
	v_lshl_add_u64 v[196:197], v[196:197], 0, s[56:57]
	v_lshl_add_u64 v[196:197], v[196:197], 0, v[2:3]
	v_or_b32_e32 v80, s74, v160
	global_load_ushort v149, v[196:197], off offset:3072
	global_load_ushort v147, v[196:197], off offset:3136
	v_mad_u64_u32 v[196:197], s[8:9], v80, s2, v[210:211]
	v_mad_i32_i24 v197, s75, v202, v197
	v_lshl_add_u64 v[196:197], v[196:197], 0, s[56:57]
	v_lshl_add_u64 v[196:197], v[196:197], 0, v[2:3]
	v_or_b32_e32 v78, s74, v162
	global_load_ushort v145, v[196:197], off offset:3072
	global_load_ushort v143, v[196:197], off offset:3136
	v_mad_u64_u32 v[196:197], s[8:9], v78, s2, v[210:211]
	v_mad_i32_i24 v197, s75, v202, v197
	v_add_f32_e32 v74, 1.0, v74
	v_lshl_add_u64 v[196:197], v[196:197], 0, s[56:57]
	v_rcp_f32_e32 v74, v74
	v_lshl_add_u64 v[196:197], v[196:197], 0, v[2:3]
	v_or_b32_e32 v76, s74, v164
	global_load_ushort v141, v[196:197], off offset:3072
	global_load_ushort v139, v[196:197], off offset:3136
	v_mad_u64_u32 v[196:197], s[8:9], v76, s2, v[210:211]
	v_mad_i32_i24 v197, s75, v202, v197
	v_lshl_add_u64 v[196:197], v[196:197], 0, s[56:57]
	v_mul_f32_e32 v36, v74, v36
	v_lshl_add_u64 v[196:197], v[196:197], 0, v[2:3]
	v_or_b32_e32 v74, s74, v166
	global_load_ushort v137, v[196:197], off offset:3072
	global_load_ushort v135, v[196:197], off offset:3136
	v_mad_u64_u32 v[196:197], s[8:9], v74, s2, v[210:211]
	v_mad_i32_i24 v197, s75, v202, v197
	v_lshl_add_u64 v[196:197], v[196:197], 0, s[56:57]
	v_lshl_add_u64 v[196:197], v[196:197], 0, v[2:3]
	v_or_b32_e32 v72, s74, v168
	global_load_ushort v133, v[196:197], off offset:3072
	global_load_ushort v131, v[196:197], off offset:3136
	v_mad_u64_u32 v[196:197], s[8:9], v72, s2, v[210:211]
	v_mad_i32_i24 v197, s75, v202, v197
	v_bfe_u32 v70, v36, 16, 1
	v_lshl_add_u64 v[196:197], v[196:197], 0, s[56:57]
	v_add3_u32 v89, v36, v70, s1
	v_lshl_add_u64 v[196:197], v[196:197], 0, v[2:3]
	v_or_b32_e32 v70, s74, v170
	global_load_ushort v129, v[196:197], off offset:3072
	global_load_ushort v127, v[196:197], off offset:3136
	v_mad_u64_u32 v[196:197], s[8:9], v70, s2, v[210:211]
	v_mad_i32_i24 v197, s75, v202, v197
	v_mul_f32_e32 v52, v52, v91
	v_lshl_add_u64 v[196:197], v[196:197], 0, s[56:57]
	s_waitcnt vmcnt(56)
	v_lshlrev_b32_e32 v83, 16, v93
	v_mul_f32_e32 v52, v109, v52
	v_lshl_add_u64 v[196:197], v[196:197], 0, v[2:3]
	v_or_b32_e32 v68, s74, v172
	v_mul_f32_e32 v52, v52, v83
	v_mul_f32_e32 v83, 0xbfb8aa3b, v83
	global_load_ushort v125, v[196:197], off offset:3072
	global_load_ushort v123, v[196:197], off offset:3136
	v_mad_u64_u32 v[196:197], s[8:9], v68, s2, v[210:211]
	v_exp_f32_e32 v83, v83
	v_mad_i32_i24 v197, s75, v202, v197
	v_lshl_add_u64 v[196:197], v[196:197], 0, s[56:57]
	v_lshl_add_u64 v[196:197], v[196:197], 0, v[2:3]
	v_or_b32_e32 v36, s74, v174
	global_load_ushort v121, v[196:197], off offset:3072
	global_load_ushort v119, v[196:197], off offset:3136
	v_mad_u64_u32 v[196:197], s[8:9], v36, s2, v[210:211]
	v_add_f32_e32 v83, 1.0, v83
	v_mad_i32_i24 v197, s75, v202, v197
	v_rcp_f32_e32 v83, v83
	v_lshl_add_u64 v[196:197], v[196:197], 0, s[56:57]
	v_lshl_add_u64 v[196:197], v[196:197], 0, v[2:3]
	global_load_ushort v117, v[196:197], off offset:3072
	global_load_ushort v115, v[196:197], off offset:3136
	v_lshlrev_b64 v[196:197], 11, v[208:209]
	v_lshl_add_u64 v[196:197], s[36:37], 0, v[196:197]
	v_mul_f32_e32 v52, v83, v52
	v_lshl_add_u64 v[196:197], v[196:197], 0, s[56:57]
	v_bfe_u32 v83, v52, 16, 1
	v_lshl_add_u64 v[196:197], v[196:197], 0, v[2:3]
	v_add3_u32 v52, v52, v83, s1
	global_store_short_d16_hi v[196:197], v52, off offset:1600
	v_mul_f32_e32 v52, v53, v53
	v_fmac_f32_e32 v52, v37, v37
	global_store_short_d16_hi v[196:197], v89, off offset:1536
	v_lshlrev_b64 v[196:197], 11, v[206:207]
	v_add_f32_dpp v52, v52, v52 quad_perm:[1,0,3,2] row_mask:0xf bank_mask:0xf bound_ctrl:1
	v_lshl_add_u64 v[196:197], s[36:37], 0, v[196:197]
	v_lshl_add_u64 v[196:197], v[196:197], 0, s[56:57]
	v_add_f32_dpp v52, v52, v52 quad_perm:[2,3,0,1] row_mask:0xf bank_mask:0xf bound_ctrl:1
	v_lshl_add_u64 v[196:197], v[196:197], 0, v[2:3]
	s_nop 0
	v_add_f32_dpp v52, v52, v52 row_half_mirror row_mask:0xf bank_mask:0xf bound_ctrl:1
	s_nop 1
	v_add_f32_dpp v52, v52, v52 row_mirror row_mask:0xf bank_mask:0xf bound_ctrl:1
	ds_bpermute_b32 v83, v113, v52
	s_waitcnt lgkmcnt(0)
	v_add_f32_e32 v52, v52, v83
	v_fmamk_f32 v52, v52, 0x3c800000, v1
	v_mul_f32_e32 v83, 0x4f800000, v52
	v_cmp_gt_f32_e32 vcc, s29, v52
	s_nop 1
	v_cndmask_b32_e32 v52, v52, v83, vcc
	v_sqrt_f32_e32 v83, v52
	s_nop 0
	v_add_u32_e32 v87, -1, v83
	v_fma_f32 v89, -v87, v83, v52
	v_cmp_ge_f32_e64 s[38:39], 0, v89
	v_add_u32_e32 v89, 1, v83
	s_nop 0
	v_cndmask_b32_e64 v87, v83, v87, s[38:39]
	v_fma_f32 v83, -v89, v83, v52
	v_cmp_lt_f32_e64 s[38:39], 0, v83
	s_nop 1
	v_cndmask_b32_e64 v83, v87, v89, s[38:39]
	v_mul_f32_e32 v87, 0x37800000, v83
	v_cndmask_b32_e32 v83, v83, v87, vcc
	v_cmp_class_f32_e32 vcc, v52, v248
	s_nop 1
	v_cndmask_b32_e32 v52, v83, v52, vcc
	v_div_scale_f32 v83, s[8:9], v52, v52, 1.0
	v_rcp_f32_e32 v87, v83
	s_nop 0
	v_fma_f32 v89, -v83, v87, 1.0
	v_fmac_f32_e32 v87, v89, v87
	v_div_scale_f32 v89, vcc, 1.0, v52, 1.0
	v_mul_f32_e32 v91, v89, v87
	v_fma_f32 v93, -v83, v91, v89
	v_fmac_f32_e32 v91, v93, v87
	v_fma_f32 v83, -v83, v91, v89
	v_div_fmas_f32 v83, v83, v87, v91
	v_div_fixup_f32 v52, v83, v52, 1.0
	v_mul_f32_e32 v37, v37, v52
	s_waitcnt vmcnt(62)
	v_lshlrev_b32_e32 v83, 16, v95
	v_mul_f32_e32 v37, v111, v37
	v_mul_f32_e32 v37, v37, v83
	v_mul_f32_e32 v83, 0xbfb8aa3b, v83
	v_exp_f32_e32 v83, v83
	v_mul_f32_e32 v52, v53, v52
	v_mul_f32_e32 v52, v109, v52
	v_mov_b32_e32 v91, s75
	v_add_f32_e32 v83, 1.0, v83
	v_rcp_f32_e32 v83, v83
	v_mov_b32_e32 v95, s75
	v_mov_b32_e32 v93, s75
	v_mul_f32_e32 v37, v83, v37
	v_bfe_u32 v83, v37, 16, 1
	v_add3_u32 v37, v37, v83, s1
	global_store_short_d16_hi v[196:197], v37, off offset:1536
	v_lshlrev_b32_e32 v37, 16, v97
	v_mul_f32_e32 v52, v52, v37
	v_mul_f32_e32 v37, 0xbfb8aa3b, v37
	v_exp_f32_e32 v37, v37
	v_mov_b32_e32 v97, s75
	v_add_f32_e32 v37, 1.0, v37
	v_rcp_f32_e32 v37, v37
	s_nop 0
	v_mul_f32_e32 v37, v37, v52
	v_bfe_u32 v52, v37, 16, 1
	v_add3_u32 v37, v37, v52, s1
	global_store_short_d16_hi v[196:197], v37, off offset:1600
	v_mul_f32_e32 v37, v54, v54
	v_fmac_f32_e32 v37, v38, v38
	s_nop 1
	v_add_f32_dpp v37, v37, v37 quad_perm:[1,0,3,2] row_mask:0xf bank_mask:0xf bound_ctrl:1
	s_nop 1
	v_add_f32_dpp v37, v37, v37 quad_perm:[2,3,0,1] row_mask:0xf bank_mask:0xf bound_ctrl:1
	s_nop 1
	v_add_f32_dpp v37, v37, v37 row_half_mirror row_mask:0xf bank_mask:0xf bound_ctrl:1
	s_nop 1
	v_add_f32_dpp v37, v37, v37 row_mirror row_mask:0xf bank_mask:0xf bound_ctrl:1
	ds_bpermute_b32 v52, v113, v37
	s_waitcnt lgkmcnt(0)
	v_add_f32_e32 v37, v37, v52
	v_fmamk_f32 v37, v37, 0x3c800000, v1
	v_mul_f32_e32 v52, 0x4f800000, v37
	v_cmp_gt_f32_e32 vcc, s29, v37
	s_nop 1
	v_cndmask_b32_e32 v37, v37, v52, vcc
	v_sqrt_f32_e32 v52, v37
	s_nop 0
	v_add_u32_e32 v53, -1, v52
	v_fma_f32 v83, -v53, v52, v37
	v_cmp_ge_f32_e64 s[38:39], 0, v83
	v_add_u32_e32 v83, 1, v52
	s_nop 0
	v_cndmask_b32_e64 v53, v52, v53, s[38:39]
	v_fma_f32 v52, -v83, v52, v37
	v_cmp_lt_f32_e64 s[38:39], 0, v52
	s_nop 1
	v_cndmask_b32_e64 v52, v53, v83, s[38:39]
	v_mul_f32_e32 v53, 0x37800000, v52
	v_cndmask_b32_e32 v52, v52, v53, vcc
	v_cmp_class_f32_e32 vcc, v37, v248
	s_nop 1
	v_cndmask_b32_e32 v37, v52, v37, vcc
	v_div_scale_f32 v52, s[8:9], v37, v37, 1.0
	v_rcp_f32_e32 v53, v52
	s_nop 0
	v_fma_f32 v83, -v52, v53, 1.0
	v_fmac_f32_e32 v53, v83, v53
	v_div_scale_f32 v83, vcc, 1.0, v37, 1.0
	v_mul_f32_e32 v87, v83, v53
	v_fma_f32 v89, -v52, v87, v83
	v_fmac_f32_e32 v87, v89, v53
	v_fma_f32 v52, -v52, v87, v83
	v_div_fmas_f32 v52, v52, v53, v87
	v_div_fixup_f32 v37, v52, v37, 1.0
	v_mul_f32_e32 v38, v38, v37
	s_waitcnt vmcnt(62)
	v_lshlrev_b32_e32 v52, 16, v99
	v_mul_f32_e32 v38, v111, v38
	v_mul_f32_e32 v38, v38, v52
	v_mul_f32_e32 v52, 0xbfb8aa3b, v52
	v_exp_f32_e32 v52, v52
	v_mul_f32_e32 v37, v54, v37
	v_mul_f32_e32 v37, v109, v37
	v_mov_b32_e32 v99, s75
	v_add_f32_e32 v52, 1.0, v52
	v_rcp_f32_e32 v52, v52
	v_mov_b32_e32 v89, s75
	v_mov_b32_e32 v87, s75
	v_mul_f32_e32 v38, v52, v38
	v_bfe_u32 v52, v38, 16, 1
	v_add3_u32 v38, v38, v52, s1
	v_lshlrev_b64 v[52:53], 11, v[204:205]
	v_lshl_add_u64 v[52:53], s[36:37], 0, v[52:53]
	v_lshl_add_u64 v[52:53], v[52:53], 0, s[56:57]
	v_lshl_add_u64 v[52:53], v[52:53], 0, v[2:3]
	global_store_short_d16_hi v[52:53], v38, off offset:1536
	v_lshlrev_b32_e32 v38, 16, v101
	v_mul_f32_e32 v37, v37, v38
	v_mul_f32_e32 v38, 0xbfb8aa3b, v38
	v_exp_f32_e32 v38, v38
	v_mov_b32_e32 v101, s75
	v_add_f32_e32 v38, 1.0, v38
	v_rcp_f32_e32 v38, v38
	s_nop 0
	v_mul_f32_e32 v37, v38, v37
	v_bfe_u32 v38, v37, 16, 1
	v_add3_u32 v37, v37, v38, s1
	global_store_short_d16_hi v[52:53], v37, off offset:1600
	v_mul_f32_e32 v37, v55, v55
	v_fmac_f32_e32 v37, v39, v39
	s_nop 1
	v_add_f32_dpp v37, v37, v37 quad_perm:[1,0,3,2] row_mask:0xf bank_mask:0xf bound_ctrl:1
	s_nop 1
	v_add_f32_dpp v37, v37, v37 quad_perm:[2,3,0,1] row_mask:0xf bank_mask:0xf bound_ctrl:1
	s_nop 1
	v_add_f32_dpp v37, v37, v37 row_half_mirror row_mask:0xf bank_mask:0xf bound_ctrl:1
	s_nop 1
	v_add_f32_dpp v37, v37, v37 row_mirror row_mask:0xf bank_mask:0xf bound_ctrl:1
	ds_bpermute_b32 v38, v113, v37
	s_waitcnt lgkmcnt(0)
	v_add_f32_e32 v37, v37, v38
	v_fmamk_f32 v37, v37, 0x3c800000, v1
	v_mul_f32_e32 v38, 0x4f800000, v37
	v_cmp_gt_f32_e32 vcc, s29, v37
	s_nop 1
	v_cndmask_b32_e32 v37, v37, v38, vcc
	v_sqrt_f32_e32 v38, v37
	s_nop 0
	v_add_u32_e32 v52, -1, v38
	v_fma_f32 v53, -v52, v38, v37
	v_cmp_ge_f32_e64 s[38:39], 0, v53
	v_add_u32_e32 v53, 1, v38
	s_nop 0
	v_cndmask_b32_e64 v52, v38, v52, s[38:39]
	v_fma_f32 v38, -v53, v38, v37
	v_cmp_lt_f32_e64 s[38:39], 0, v38
	s_nop 1
	v_cndmask_b32_e64 v38, v52, v53, s[38:39]
	v_mul_f32_e32 v52, 0x37800000, v38
	v_cndmask_b32_e32 v38, v38, v52, vcc
	v_cmp_class_f32_e32 vcc, v37, v248
	s_nop 1
	v_cndmask_b32_e32 v37, v38, v37, vcc
	v_div_scale_f32 v38, s[8:9], v37, v37, 1.0
	v_rcp_f32_e32 v52, v38
	s_nop 0
	v_fma_f32 v53, -v38, v52, 1.0
	v_fmac_f32_e32 v52, v53, v52
	v_div_scale_f32 v53, vcc, 1.0, v37, 1.0
	v_mul_f32_e32 v54, v53, v52
	v_fma_f32 v83, -v38, v54, v53
	v_fmac_f32_e32 v54, v83, v52
	v_fma_f32 v38, -v38, v54, v53
	v_div_fmas_f32 v38, v38, v52, v54
	v_div_fixup_f32 v37, v38, v37, 1.0
	v_mul_f32_e32 v39, v39, v37
	s_waitcnt vmcnt(62)
	v_lshlrev_b32_e32 v38, 16, v103
	v_mul_f32_e32 v39, v111, v39
	v_mul_f32_e32 v39, v39, v38
	v_mul_f32_e32 v38, 0xbfb8aa3b, v38
	v_exp_f32_e32 v38, v38
	v_mul_f32_e32 v37, v55, v37
	v_mul_f32_e32 v37, v109, v37
	v_mov_b32_e32 v103, s75
	v_add_f32_e32 v38, 1.0, v38
	v_rcp_f32_e32 v38, v38
	v_mov_b32_e32 v83, s75
	v_mul_f32_e32 v38, v38, v39
	v_bfe_u32 v39, v38, 16, 1
	v_add3_u32 v52, v38, v39, s1
	v_lshlrev_b64 v[38:39], 11, v[194:195]
	v_lshl_add_u64 v[38:39], s[36:37], 0, v[38:39]
	v_lshl_add_u64 v[38:39], v[38:39], 0, s[56:57]
	v_lshl_add_u64 v[38:39], v[38:39], 0, v[2:3]
	global_store_short_d16_hi v[38:39], v52, off offset:1536
	v_lshlrev_b32_e32 v52, 16, v177
	v_mul_f32_e32 v37, v37, v52
	v_mul_f32_e32 v52, 0xbfb8aa3b, v52
	v_exp_f32_e32 v52, v52
	v_mov_b32_e32 v177, s75
	v_add_f32_e32 v52, 1.0, v52
	v_rcp_f32_e32 v52, v52
	s_nop 0
	v_mul_f32_e32 v37, v52, v37
	v_bfe_u32 v52, v37, 16, 1
	v_add3_u32 v37, v37, v52, s1
	global_store_short_d16_hi v[38:39], v37, off offset:1600
	v_mul_f32_e32 v37, v56, v56
	v_fmac_f32_e32 v37, v40, v40
	s_nop 1
	v_add_f32_dpp v37, v37, v37 quad_perm:[1,0,3,2] row_mask:0xf bank_mask:0xf bound_ctrl:1
	s_nop 1
	v_add_f32_dpp v37, v37, v37 quad_perm:[2,3,0,1] row_mask:0xf bank_mask:0xf bound_ctrl:1
	s_nop 1
	v_add_f32_dpp v37, v37, v37 row_half_mirror row_mask:0xf bank_mask:0xf bound_ctrl:1
	s_nop 1
	v_add_f32_dpp v37, v37, v37 row_mirror row_mask:0xf bank_mask:0xf bound_ctrl:1
	ds_bpermute_b32 v38, v113, v37
	s_waitcnt lgkmcnt(0)
	v_add_f32_e32 v37, v37, v38
	v_fmamk_f32 v37, v37, 0x3c800000, v1
	v_mul_f32_e32 v38, 0x4f800000, v37
	v_cmp_gt_f32_e32 vcc, s29, v37
	s_nop 1
	v_cndmask_b32_e32 v37, v37, v38, vcc
	v_sqrt_f32_e32 v38, v37
	s_nop 0
	v_add_u32_e32 v39, -1, v38
	v_fma_f32 v52, -v39, v38, v37
	v_cmp_ge_f32_e64 s[38:39], 0, v52
	v_add_u32_e32 v52, 1, v38
	s_nop 0
	v_cndmask_b32_e64 v39, v38, v39, s[38:39]
	v_fma_f32 v38, -v52, v38, v37
	v_cmp_lt_f32_e64 s[38:39], 0, v38
	s_nop 1
	v_cndmask_b32_e64 v38, v39, v52, s[38:39]
	v_mul_f32_e32 v39, 0x37800000, v38
	v_cndmask_b32_e32 v38, v38, v39, vcc
	v_cmp_class_f32_e32 vcc, v37, v248
	s_nop 1
	v_cndmask_b32_e32 v37, v38, v37, vcc
	v_div_scale_f32 v38, s[8:9], v37, v37, 1.0
	v_rcp_f32_e32 v39, v38
	s_nop 0
	v_fma_f32 v52, -v38, v39, 1.0
	v_fmac_f32_e32 v39, v52, v39
	v_div_scale_f32 v52, vcc, 1.0, v37, 1.0
	v_mul_f32_e32 v53, v52, v39
	v_fma_f32 v54, -v38, v53, v52
	v_fmac_f32_e32 v53, v54, v39
	v_fma_f32 v38, -v38, v53, v52
	v_div_fmas_f32 v38, v38, v39, v53
	v_div_fixup_f32 v37, v38, v37, 1.0
	v_mul_f32_e32 v39, v40, v37
	s_waitcnt vmcnt(62)
	v_lshlrev_b32_e32 v38, 16, v179
	v_mul_f32_e32 v39, v111, v39
	v_mul_f32_e32 v39, v39, v38
	v_mul_f32_e32 v38, 0xbfb8aa3b, v38
	v_exp_f32_e32 v38, v38
	v_mul_f32_e32 v37, v56, v37
	v_mul_f32_e32 v37, v109, v37
	v_mov_b32_e32 v179, s75
	v_add_f32_e32 v38, 1.0, v38
	v_rcp_f32_e32 v38, v38
	s_nop 0
	v_mul_f32_e32 v38, v38, v39
	v_bfe_u32 v39, v38, 16, 1
	v_add3_u32 v40, v38, v39, s1
	v_lshlrev_b64 v[38:39], 11, v[192:193]
	v_lshl_add_u64 v[38:39], s[36:37], 0, v[38:39]
	v_lshl_add_u64 v[38:39], v[38:39], 0, s[56:57]
	v_lshl_add_u64 v[38:39], v[38:39], 0, v[2:3]
	global_store_short_d16_hi v[38:39], v40, off offset:1536
	v_lshlrev_b32_e32 v40, 16, v181
	v_mul_f32_e32 v37, v37, v40
	v_mul_f32_e32 v40, 0xbfb8aa3b, v40
	v_exp_f32_e32 v40, v40
	v_mov_b32_e32 v181, s75
	v_add_f32_e32 v40, 1.0, v40
	v_rcp_f32_e32 v40, v40
	s_nop 0
	v_mul_f32_e32 v37, v40, v37
	v_bfe_u32 v40, v37, 16, 1
	v_add3_u32 v37, v37, v40, s1
	global_store_short_d16_hi v[38:39], v37, off offset:1600
	v_mul_f32_e32 v37, v57, v57
	v_fmac_f32_e32 v37, v41, v41
	s_nop 1
	v_add_f32_dpp v37, v37, v37 quad_perm:[1,0,3,2] row_mask:0xf bank_mask:0xf bound_ctrl:1
	s_nop 1
	v_add_f32_dpp v37, v37, v37 quad_perm:[2,3,0,1] row_mask:0xf bank_mask:0xf bound_ctrl:1
	s_nop 1
	v_add_f32_dpp v37, v37, v37 row_half_mirror row_mask:0xf bank_mask:0xf bound_ctrl:1
	s_nop 1
	v_add_f32_dpp v37, v37, v37 row_mirror row_mask:0xf bank_mask:0xf bound_ctrl:1
	ds_bpermute_b32 v38, v113, v37
	s_waitcnt lgkmcnt(0)
	v_add_f32_e32 v37, v37, v38
	v_fmamk_f32 v37, v37, 0x3c800000, v1
	v_mul_f32_e32 v38, 0x4f800000, v37
	v_cmp_gt_f32_e32 vcc, s29, v37
	s_nop 1
	v_cndmask_b32_e32 v37, v37, v38, vcc
	v_sqrt_f32_e32 v38, v37
	s_nop 0
	v_add_u32_e32 v39, -1, v38
	v_fma_f32 v40, -v39, v38, v37
	v_cmp_ge_f32_e64 s[38:39], 0, v40
	v_add_u32_e32 v40, 1, v38
	s_nop 0
	v_cndmask_b32_e64 v39, v38, v39, s[38:39]
	v_fma_f32 v38, -v40, v38, v37
	v_cmp_lt_f32_e64 s[38:39], 0, v38
	s_nop 1
	v_cndmask_b32_e64 v38, v39, v40, s[38:39]
	v_mul_f32_e32 v39, 0x37800000, v38
	v_cndmask_b32_e32 v38, v38, v39, vcc
	v_cmp_class_f32_e32 vcc, v37, v248
	s_nop 1
	v_cndmask_b32_e32 v37, v38, v37, vcc
	v_div_scale_f32 v38, s[8:9], v37, v37, 1.0
	v_rcp_f32_e32 v39, v38
	s_nop 0
	v_fma_f32 v40, -v38, v39, 1.0
	v_fmac_f32_e32 v39, v40, v39
	v_div_scale_f32 v40, vcc, 1.0, v37, 1.0
	v_mul_f32_e32 v52, v40, v39
	v_fma_f32 v53, -v38, v52, v40
	v_fmac_f32_e32 v52, v53, v39
	v_fma_f32 v38, -v38, v52, v40
	v_div_fmas_f32 v38, v38, v39, v52
	v_div_fixup_f32 v37, v38, v37, 1.0
	v_mul_f32_e32 v39, v41, v37
	s_waitcnt vmcnt(62)
	v_lshlrev_b32_e32 v38, 16, v183
	v_mul_f32_e32 v39, v111, v39
	v_mul_f32_e32 v39, v39, v38
	v_mul_f32_e32 v38, 0xbfb8aa3b, v38
	v_exp_f32_e32 v38, v38
	v_mul_f32_e32 v37, v57, v37
	v_mul_f32_e32 v37, v109, v37
	v_mov_b32_e32 v183, s75
	v_add_f32_e32 v38, 1.0, v38
	v_rcp_f32_e32 v38, v38
	s_nop 0
	v_mul_f32_e32 v38, v38, v39
	v_bfe_u32 v39, v38, 16, 1
	v_add3_u32 v40, v38, v39, s1
	v_lshlrev_b64 v[38:39], 11, v[190:191]
	v_lshl_add_u64 v[38:39], s[36:37], 0, v[38:39]
	v_lshl_add_u64 v[38:39], v[38:39], 0, s[56:57]
	v_lshl_add_u64 v[38:39], v[38:39], 0, v[2:3]
	global_store_short_d16_hi v[38:39], v40, off offset:1536
	v_lshlrev_b32_e32 v40, 16, v185
	v_mul_f32_e32 v37, v37, v40
	v_mul_f32_e32 v40, 0xbfb8aa3b, v40
	v_exp_f32_e32 v40, v40
	v_mov_b32_e32 v185, s75
	v_add_f32_e32 v40, 1.0, v40
	v_rcp_f32_e32 v40, v40
	s_nop 0
	v_mul_f32_e32 v37, v40, v37
	v_bfe_u32 v40, v37, 16, 1
	v_add3_u32 v37, v37, v40, s1
	global_store_short_d16_hi v[38:39], v37, off offset:1600
	v_mul_f32_e32 v37, v58, v58
	v_fmac_f32_e32 v37, v42, v42
	s_nop 1
	v_add_f32_dpp v37, v37, v37 quad_perm:[1,0,3,2] row_mask:0xf bank_mask:0xf bound_ctrl:1
	s_nop 1
	v_add_f32_dpp v37, v37, v37 quad_perm:[2,3,0,1] row_mask:0xf bank_mask:0xf bound_ctrl:1
	s_nop 1
	v_add_f32_dpp v37, v37, v37 row_half_mirror row_mask:0xf bank_mask:0xf bound_ctrl:1
	s_nop 1
	v_add_f32_dpp v37, v37, v37 row_mirror row_mask:0xf bank_mask:0xf bound_ctrl:1
	ds_bpermute_b32 v38, v113, v37
	s_waitcnt lgkmcnt(0)
	v_add_f32_e32 v37, v37, v38
	v_fmamk_f32 v37, v37, 0x3c800000, v1
	v_mul_f32_e32 v38, 0x4f800000, v37
	v_cmp_gt_f32_e32 vcc, s29, v37
	s_nop 1
	v_cndmask_b32_e32 v37, v37, v38, vcc
	v_sqrt_f32_e32 v38, v37
	s_nop 0
	v_add_u32_e32 v39, -1, v38
	v_fma_f32 v40, -v39, v38, v37
	v_cmp_ge_f32_e64 s[38:39], 0, v40
	v_add_u32_e32 v40, 1, v38
	s_nop 0
	v_cndmask_b32_e64 v39, v38, v39, s[38:39]
	v_fma_f32 v38, -v40, v38, v37
	v_cmp_lt_f32_e64 s[38:39], 0, v38
	s_nop 1
	v_cndmask_b32_e64 v38, v39, v40, s[38:39]
	v_mul_f32_e32 v39, 0x37800000, v38
	v_cndmask_b32_e32 v38, v38, v39, vcc
	v_cmp_class_f32_e32 vcc, v37, v248
	s_nop 1
	v_cndmask_b32_e32 v37, v38, v37, vcc
	v_div_scale_f32 v38, s[8:9], v37, v37, 1.0
	v_rcp_f32_e32 v39, v38
	s_nop 0
	v_fma_f32 v40, -v38, v39, 1.0
	v_fmac_f32_e32 v39, v40, v39
	v_div_scale_f32 v40, vcc, 1.0, v37, 1.0
	v_mul_f32_e32 v41, v40, v39
	v_fma_f32 v52, -v38, v41, v40
	v_fmac_f32_e32 v41, v52, v39
	v_fma_f32 v38, -v38, v41, v40
	v_div_fmas_f32 v38, v38, v39, v41
	v_div_fixup_f32 v37, v38, v37, 1.0
	v_mul_f32_e32 v39, v42, v37
	s_waitcnt vmcnt(62)
	v_lshlrev_b32_e32 v38, 16, v85
	v_mul_f32_e32 v39, v111, v39
	v_mul_f32_e32 v39, v39, v38
	v_mul_f32_e32 v38, 0xbfb8aa3b, v38
	v_exp_f32_e32 v38, v38
	v_mul_f32_e32 v37, v58, v37
	v_mul_f32_e32 v37, v109, v37
	v_mov_b32_e32 v85, s75
	v_add_f32_e32 v38, 1.0, v38
	v_rcp_f32_e32 v38, v38
	s_nop 0
	v_mul_f32_e32 v38, v38, v39
	v_bfe_u32 v39, v38, 16, 1
	v_add3_u32 v40, v38, v39, s1
	v_lshlrev_b64 v[38:39], 11, v[188:189]
	v_lshl_add_u64 v[38:39], s[36:37], 0, v[38:39]
	v_lshl_add_u64 v[38:39], v[38:39], 0, s[56:57]
	v_lshl_add_u64 v[38:39], v[38:39], 0, v[2:3]
	global_store_short_d16_hi v[38:39], v40, off offset:1536
	v_lshlrev_b32_e32 v40, 16, v81
	v_mul_f32_e32 v37, v37, v40
	v_mul_f32_e32 v40, 0xbfb8aa3b, v40
	v_exp_f32_e32 v40, v40
	v_mov_b32_e32 v81, s75
	v_add_f32_e32 v40, 1.0, v40
	v_rcp_f32_e32 v40, v40
	s_nop 0
	v_mul_f32_e32 v37, v40, v37
	v_bfe_u32 v40, v37, 16, 1
	v_add3_u32 v37, v37, v40, s1
	global_store_short_d16_hi v[38:39], v37, off offset:1600
	v_mul_f32_e32 v37, v59, v59
	v_fmac_f32_e32 v37, v43, v43
	s_nop 1
	v_add_f32_dpp v37, v37, v37 quad_perm:[1,0,3,2] row_mask:0xf bank_mask:0xf bound_ctrl:1
	s_nop 1
	v_add_f32_dpp v37, v37, v37 quad_perm:[2,3,0,1] row_mask:0xf bank_mask:0xf bound_ctrl:1
	s_nop 1
	v_add_f32_dpp v37, v37, v37 row_half_mirror row_mask:0xf bank_mask:0xf bound_ctrl:1
	s_nop 1
	v_add_f32_dpp v37, v37, v37 row_mirror row_mask:0xf bank_mask:0xf bound_ctrl:1
	ds_bpermute_b32 v38, v113, v37
	s_waitcnt lgkmcnt(0)
	v_add_f32_e32 v37, v37, v38
	v_fmamk_f32 v37, v37, 0x3c800000, v1
	v_mul_f32_e32 v38, 0x4f800000, v37
	v_cmp_gt_f32_e32 vcc, s29, v37
	s_nop 1
	v_cndmask_b32_e32 v37, v37, v38, vcc
	v_sqrt_f32_e32 v38, v37
	s_nop 0
	v_add_u32_e32 v39, -1, v38
	v_fma_f32 v40, -v39, v38, v37
	v_cmp_ge_f32_e64 s[38:39], 0, v40
	v_add_u32_e32 v40, 1, v38
	s_nop 0
	v_cndmask_b32_e64 v39, v38, v39, s[38:39]
	v_fma_f32 v38, -v40, v38, v37
	v_cmp_lt_f32_e64 s[38:39], 0, v38
	s_nop 1
	v_cndmask_b32_e64 v38, v39, v40, s[38:39]
	v_mul_f32_e32 v39, 0x37800000, v38
	v_cndmask_b32_e32 v38, v38, v39, vcc
	v_cmp_class_f32_e32 vcc, v37, v248
	s_nop 1
	v_cndmask_b32_e32 v37, v38, v37, vcc
	v_div_scale_f32 v38, s[8:9], v37, v37, 1.0
	v_rcp_f32_e32 v39, v38
	s_nop 0
	v_fma_f32 v40, -v38, v39, 1.0
	v_fmac_f32_e32 v39, v40, v39
	v_div_scale_f32 v40, vcc, 1.0, v37, 1.0
	v_mul_f32_e32 v41, v40, v39
	v_fma_f32 v42, -v38, v41, v40
	v_fmac_f32_e32 v41, v42, v39
	v_fma_f32 v38, -v38, v41, v40
	v_div_fmas_f32 v38, v38, v39, v41
	v_div_fixup_f32 v37, v38, v37, 1.0
	v_mul_f32_e32 v39, v43, v37
	s_waitcnt vmcnt(62)
	v_lshlrev_b32_e32 v38, 16, v79
	v_mul_f32_e32 v39, v111, v39
	v_mul_f32_e32 v39, v39, v38
	v_mul_f32_e32 v38, 0xbfb8aa3b, v38
	v_exp_f32_e32 v38, v38
	v_mul_f32_e32 v37, v59, v37
	v_mul_f32_e32 v37, v109, v37
	s_waitcnt vmcnt(56)
	v_lshlrev_b32_e32 v43, 16, v229
	v_add_f32_e32 v38, 1.0, v38
	v_rcp_f32_e32 v38, v38
	v_mov_b32_e32 v79, s75
	v_mul_f32_e32 v38, v38, v39
	v_bfe_u32 v39, v38, 16, 1
	v_add3_u32 v40, v38, v39, s1
	v_lshlrev_b64 v[38:39], 11, v[186:187]
	v_lshl_add_u64 v[38:39], s[36:37], 0, v[38:39]
	v_lshl_add_u64 v[38:39], v[38:39], 0, s[56:57]
	v_lshl_add_u64 v[38:39], v[38:39], 0, v[2:3]
	global_store_short_d16_hi v[38:39], v40, off offset:1536
	v_lshlrev_b32_e32 v40, 16, v77
	v_mul_f32_e32 v37, v37, v40
	v_mul_f32_e32 v40, 0xbfb8aa3b, v40
	v_exp_f32_e32 v40, v40
	v_mov_b32_e32 v77, s75
	v_add_f32_e32 v40, 1.0, v40
	v_rcp_f32_e32 v40, v40
	s_nop 0
	v_mul_f32_e32 v37, v40, v37
	v_bfe_u32 v40, v37, 16, 1
	v_add3_u32 v37, v37, v40, s1
	global_store_short_d16_hi v[38:39], v37, off offset:1600
	v_mul_f32_e32 v37, v60, v60
	v_fmac_f32_e32 v37, v44, v44
	s_nop 1
	v_add_f32_dpp v37, v37, v37 quad_perm:[1,0,3,2] row_mask:0xf bank_mask:0xf bound_ctrl:1
	s_nop 1
	v_add_f32_dpp v37, v37, v37 quad_perm:[2,3,0,1] row_mask:0xf bank_mask:0xf bound_ctrl:1
	s_nop 1
	v_add_f32_dpp v37, v37, v37 row_half_mirror row_mask:0xf bank_mask:0xf bound_ctrl:1
	s_nop 1
	v_add_f32_dpp v37, v37, v37 row_mirror row_mask:0xf bank_mask:0xf bound_ctrl:1
	ds_bpermute_b32 v38, v113, v37
	s_waitcnt lgkmcnt(0)
	v_add_f32_e32 v37, v37, v38
	v_fmamk_f32 v37, v37, 0x3c800000, v1
	v_mul_f32_e32 v38, 0x4f800000, v37
	v_cmp_gt_f32_e32 vcc, s29, v37
	s_nop 1
	v_cndmask_b32_e32 v37, v37, v38, vcc
	v_sqrt_f32_e32 v38, v37
	s_nop 0
	v_add_u32_e32 v39, -1, v38
	v_fma_f32 v40, -v39, v38, v37
	v_cmp_ge_f32_e64 s[38:39], 0, v40
	v_add_u32_e32 v40, 1, v38
	s_nop 0
	v_cndmask_b32_e64 v39, v38, v39, s[38:39]
	v_fma_f32 v38, -v40, v38, v37
	v_cmp_lt_f32_e64 s[38:39], 0, v38
	s_nop 1
	v_cndmask_b32_e64 v38, v39, v40, s[38:39]
	v_mul_f32_e32 v39, 0x37800000, v38
	v_cndmask_b32_e32 v38, v38, v39, vcc
	v_cmp_class_f32_e32 vcc, v37, v248
	s_nop 1
	v_cndmask_b32_e32 v37, v38, v37, vcc
	v_div_scale_f32 v38, s[8:9], v37, v37, 1.0
	v_rcp_f32_e32 v39, v38
	s_nop 0
	v_fma_f32 v40, -v38, v39, 1.0
	v_fmac_f32_e32 v39, v40, v39
	v_div_scale_f32 v40, vcc, 1.0, v37, 1.0
	v_mul_f32_e32 v41, v40, v39
	v_fma_f32 v42, -v38, v41, v40
	v_fmac_f32_e32 v41, v42, v39
	v_fma_f32 v38, -v38, v41, v40
	v_div_fmas_f32 v38, v38, v39, v41
	v_div_fixup_f32 v37, v38, v37, 1.0
	v_mul_f32_e32 v39, v44, v37
	v_lshlrev_b32_e32 v38, 16, v75
	v_mul_f32_e32 v39, v111, v39
	v_mul_f32_e32 v39, v39, v38
	v_mul_f32_e32 v38, 0xbfb8aa3b, v38
	v_exp_f32_e32 v38, v38
	v_mul_f32_e32 v37, v60, v37
	v_mul_f32_e32 v37, v109, v37
	v_mov_b32_e32 v75, s75
	v_add_f32_e32 v38, 1.0, v38
	v_rcp_f32_e32 v38, v38
	s_nop 0
	v_mul_f32_e32 v38, v38, v39
	v_bfe_u32 v39, v38, 16, 1
	v_add3_u32 v40, v38, v39, s1
	v_lshlrev_b64 v[38:39], 11, v[184:185]
	v_lshl_add_u64 v[38:39], s[36:37], 0, v[38:39]
	v_lshl_add_u64 v[38:39], v[38:39], 0, s[56:57]
	v_lshl_add_u64 v[38:39], v[38:39], 0, v[2:3]
	global_store_short_d16_hi v[38:39], v40, off offset:1536
	v_lshlrev_b32_e32 v40, 16, v73
	v_mul_f32_e32 v37, v37, v40
	v_mul_f32_e32 v40, 0xbfb8aa3b, v40
	v_exp_f32_e32 v40, v40
	v_mov_b32_e32 v73, s75
	v_add_f32_e32 v40, 1.0, v40
	v_rcp_f32_e32 v40, v40
	s_nop 0
	v_mul_f32_e32 v37, v40, v37
	v_bfe_u32 v40, v37, 16, 1
	v_add3_u32 v37, v37, v40, s1
	global_store_short_d16_hi v[38:39], v37, off offset:1600
	v_mul_f32_e32 v37, v61, v61
	v_fmac_f32_e32 v37, v45, v45
	s_nop 1
	v_add_f32_dpp v37, v37, v37 quad_perm:[1,0,3,2] row_mask:0xf bank_mask:0xf bound_ctrl:1
	s_nop 1
	v_add_f32_dpp v37, v37, v37 quad_perm:[2,3,0,1] row_mask:0xf bank_mask:0xf bound_ctrl:1
	s_nop 1
	v_add_f32_dpp v37, v37, v37 row_half_mirror row_mask:0xf bank_mask:0xf bound_ctrl:1
	s_nop 1
	v_add_f32_dpp v37, v37, v37 row_mirror row_mask:0xf bank_mask:0xf bound_ctrl:1
	ds_bpermute_b32 v38, v113, v37
	s_waitcnt lgkmcnt(0)
	v_add_f32_e32 v37, v37, v38
	v_fmamk_f32 v37, v37, 0x3c800000, v1
	v_mul_f32_e32 v38, 0x4f800000, v37
	v_cmp_gt_f32_e32 vcc, s29, v37
	s_nop 1
	v_cndmask_b32_e32 v37, v37, v38, vcc
	v_sqrt_f32_e32 v38, v37
	s_nop 0
	v_add_u32_e32 v39, -1, v38
	v_fma_f32 v40, -v39, v38, v37
	v_cmp_ge_f32_e64 s[38:39], 0, v40
	v_add_u32_e32 v40, 1, v38
	s_nop 0
	v_cndmask_b32_e64 v39, v38, v39, s[38:39]
	v_fma_f32 v38, -v40, v38, v37
	v_cmp_lt_f32_e64 s[38:39], 0, v38
	s_nop 1
	v_cndmask_b32_e64 v38, v39, v40, s[38:39]
	v_mul_f32_e32 v39, 0x37800000, v38
	v_cndmask_b32_e32 v38, v38, v39, vcc
	v_cmp_class_f32_e32 vcc, v37, v248
	s_nop 1
	v_cndmask_b32_e32 v37, v38, v37, vcc
	v_div_scale_f32 v38, s[8:9], v37, v37, 1.0
	v_rcp_f32_e32 v39, v38
	s_nop 0
	v_fma_f32 v40, -v38, v39, 1.0
	v_fmac_f32_e32 v39, v40, v39
	v_div_scale_f32 v40, vcc, 1.0, v37, 1.0
	v_mul_f32_e32 v41, v40, v39
	v_fma_f32 v42, -v38, v41, v40
	v_fmac_f32_e32 v41, v42, v39
	v_fma_f32 v38, -v38, v41, v40
	v_div_fmas_f32 v38, v38, v39, v41
	v_div_fixup_f32 v37, v38, v37, 1.0
	v_mul_f32_e32 v39, v45, v37
	v_lshlrev_b32_e32 v38, 16, v71
	v_mul_f32_e32 v39, v111, v39
	v_mul_f32_e32 v39, v39, v38
	v_mul_f32_e32 v38, 0xbfb8aa3b, v38
	v_exp_f32_e32 v38, v38
	v_mul_f32_e32 v37, v61, v37
	v_mul_f32_e32 v37, v109, v37
	v_mov_b32_e32 v71, s75
	v_add_f32_e32 v38, 1.0, v38
	v_rcp_f32_e32 v38, v38
	s_nop 0
	v_mul_f32_e32 v38, v38, v39
	v_bfe_u32 v39, v38, 16, 1
	v_add3_u32 v40, v38, v39, s1
	v_lshlrev_b64 v[38:39], 11, v[182:183]
	v_lshl_add_u64 v[38:39], s[36:37], 0, v[38:39]
	v_lshl_add_u64 v[38:39], v[38:39], 0, s[56:57]
	v_lshl_add_u64 v[38:39], v[38:39], 0, v[2:3]
	global_store_short_d16_hi v[38:39], v40, off offset:1536
	v_lshlrev_b32_e32 v40, 16, v69
	v_mul_f32_e32 v37, v37, v40
	v_mul_f32_e32 v40, 0xbfb8aa3b, v40
	v_exp_f32_e32 v40, v40
	v_mov_b32_e32 v69, s75
	v_add_f32_e32 v40, 1.0, v40
	v_rcp_f32_e32 v40, v40
	s_nop 0
	v_mul_f32_e32 v37, v40, v37
	v_bfe_u32 v40, v37, 16, 1
	v_add3_u32 v37, v37, v40, s1
	global_store_short_d16_hi v[38:39], v37, off offset:1600
	v_mul_f32_e32 v37, v62, v62
	v_fmac_f32_e32 v37, v46, v46
	s_nop 1
	v_add_f32_dpp v37, v37, v37 quad_perm:[1,0,3,2] row_mask:0xf bank_mask:0xf bound_ctrl:1
	s_nop 1
	v_add_f32_dpp v37, v37, v37 quad_perm:[2,3,0,1] row_mask:0xf bank_mask:0xf bound_ctrl:1
	s_nop 1
	v_add_f32_dpp v37, v37, v37 row_half_mirror row_mask:0xf bank_mask:0xf bound_ctrl:1
	s_nop 1
	v_add_f32_dpp v37, v37, v37 row_mirror row_mask:0xf bank_mask:0xf bound_ctrl:1
	ds_bpermute_b32 v38, v113, v37
	s_waitcnt lgkmcnt(0)
	v_add_f32_e32 v37, v37, v38
	v_fmamk_f32 v37, v37, 0x3c800000, v1
	v_mul_f32_e32 v38, 0x4f800000, v37
	v_cmp_gt_f32_e32 vcc, s29, v37
	s_nop 1
	v_cndmask_b32_e32 v37, v37, v38, vcc
	v_sqrt_f32_e32 v38, v37
	s_nop 0
	v_add_u32_e32 v39, -1, v38
	v_fma_f32 v40, -v39, v38, v37
	v_cmp_ge_f32_e64 s[38:39], 0, v40
	v_add_u32_e32 v40, 1, v38
	s_nop 0
	v_cndmask_b32_e64 v39, v38, v39, s[38:39]
	v_fma_f32 v38, -v40, v38, v37
	v_cmp_lt_f32_e64 s[38:39], 0, v38
	s_nop 1
	v_cndmask_b32_e64 v38, v39, v40, s[38:39]
	v_mul_f32_e32 v39, 0x37800000, v38
	v_cndmask_b32_e32 v38, v38, v39, vcc
	v_cmp_class_f32_e32 vcc, v37, v248
	s_nop 1
	v_cndmask_b32_e32 v38, v38, v37, vcc
	v_div_scale_f32 v37, s[8:9], v38, v38, 1.0
	v_rcp_f32_e32 v39, v37
	s_nop 0
	v_fma_f32 v40, -v37, v39, 1.0
	v_fmac_f32_e32 v39, v40, v39
	v_div_scale_f32 v40, vcc, 1.0, v38, 1.0
	v_mul_f32_e32 v41, v40, v39
	v_fma_f32 v42, -v37, v41, v40
	v_fmac_f32_e32 v41, v42, v39
	v_fma_f32 v40, -v37, v41, v40
	v_div_fmas_f32 v39, v40, v39, v41
	v_lshlrev_b32_e32 v41, 16, v230
	v_mul_f32_e32 v42, 0xbfb8aa3b, v41
	v_exp_f32_e32 v42, v42
	v_div_fixup_f32 v40, v39, v38, 1.0
	v_mul_f32_e32 v44, v46, v40
	v_mul_f32_e32 v44, v111, v44
	v_add_f32_e32 v42, 1.0, v42
	v_rcp_f32_e32 v42, v42
	v_mul_f32_e32 v41, v44, v41
	v_mul_f32_e32 v44, v63, v63
	v_fmac_f32_e32 v44, v47, v47
	v_mul_f32_e32 v41, v42, v41
	v_bfe_u32 v42, v41, 16, 1
	v_add_f32_dpp v44, v44, v44 quad_perm:[1,0,3,2] row_mask:0xf bank_mask:0xf bound_ctrl:1
	v_add3_u32 v41, v41, v42, s1
	v_mul_f32_e32 v42, 0xbfb8aa3b, v43
	v_add_f32_dpp v44, v44, v44 quad_perm:[2,3,0,1] row_mask:0xf bank_mask:0xf bound_ctrl:1
	v_lshlrev_b64 v[38:39], 11, v[180:181]
	v_exp_f32_e32 v42, v42
	v_add_f32_dpp v44, v44, v44 row_half_mirror row_mask:0xf bank_mask:0xf bound_ctrl:1
	v_lshl_add_u64 v[38:39], s[36:37], 0, v[38:39]
	v_lshl_add_u64 v[38:39], v[38:39], 0, s[56:57]
	v_add_f32_dpp v44, v44, v44 row_mirror row_mask:0xf bank_mask:0xf bound_ctrl:1
	ds_bpermute_b32 v45, v113, v44
	v_lshl_add_u64 v[38:39], v[38:39], 0, v[2:3]
	global_store_short_d16_hi v[38:39], v41, off offset:1536
	v_add_f32_e32 v41, 1.0, v42
	v_rcp_f32_e32 v41, v41
	s_waitcnt lgkmcnt(0)
	v_add_f32_e32 v42, v44, v45
	v_fmamk_f32 v42, v42, 0x3c800000, v1
	v_mul_f32_e32 v44, 0x4f800000, v42
	v_cmp_gt_f32_e32 vcc, s29, v42
	v_mul_f32_e32 v40, v62, v40
	v_mul_f32_e32 v40, v109, v40
	v_cndmask_b32_e32 v42, v42, v44, vcc
	v_sqrt_f32_e32 v44, v42
	v_mul_f32_e32 v40, v40, v43
	v_mul_f32_e32 v40, v41, v40
	v_mov_b32_e32 v37, s75
	v_add_u32_e32 v41, -1, v44
	v_fma_f32 v43, -v41, v44, v42
	v_cmp_ge_f32_e64 s[38:39], 0, v43
	v_add_u32_e32 v43, 1, v44
	s_nop 0
	v_cndmask_b32_e64 v41, v44, v41, s[38:39]
	v_fma_f32 v44, -v43, v44, v42
	v_cmp_lt_f32_e64 s[38:39], 0, v44
	v_bfe_u32 v44, v40, 16, 1
	v_add3_u32 v40, v40, v44, s1
	v_cndmask_b32_e64 v41, v41, v43, s[38:39]
	v_mul_f32_e32 v43, 0x37800000, v41
	v_cndmask_b32_e32 v41, v41, v43, vcc
	v_cmp_class_f32_e32 vcc, v42, v248
	global_store_short_d16_hi v[38:39], v40, off offset:1600
	s_nop 0
	v_cndmask_b32_e32 v41, v41, v42, vcc
	v_div_scale_f32 v42, s[8:9], v41, v41, 1.0
	v_rcp_f32_e32 v43, v42
	s_nop 0
	v_fma_f32 v38, -v42, v43, 1.0
	v_fmac_f32_e32 v43, v38, v43
	v_div_scale_f32 v38, vcc, 1.0, v41, 1.0
	v_mul_f32_e32 v39, v38, v43
	v_fma_f32 v40, -v42, v39, v38
	v_fmac_f32_e32 v39, v40, v43
	v_fma_f32 v38, -v42, v39, v38
	v_div_fmas_f32 v38, v38, v43, v39
	v_div_fixup_f32 v40, v38, v41, 1.0
	s_waitcnt vmcnt(62)
	v_lshlrev_b32_e32 v41, 16, v228
	v_mul_f32_e32 v42, 0xbfb8aa3b, v41
	v_exp_f32_e32 v42, v42
	v_mul_f32_e32 v44, v47, v40
	v_mul_f32_e32 v44, v111, v44
	v_mul_f32_e32 v41, v44, v41
	v_add_f32_e32 v42, 1.0, v42
	v_rcp_f32_e32 v42, v42
	v_mul_f32_e32 v44, v64, v64
	v_fmac_f32_e32 v44, v48, v48
	v_lshlrev_b32_e32 v43, 16, v227
	v_mul_f32_e32 v41, v42, v41
	v_add_f32_dpp v44, v44, v44 quad_perm:[1,0,3,2] row_mask:0xf bank_mask:0xf bound_ctrl:1
	v_bfe_u32 v42, v41, 16, 1
	v_add3_u32 v41, v41, v42, s1
	v_add_f32_dpp v44, v44, v44 quad_perm:[2,3,0,1] row_mask:0xf bank_mask:0xf bound_ctrl:1
	v_mul_f32_e32 v42, 0xbfb8aa3b, v43
	v_lshlrev_b64 v[38:39], 11, v[178:179]
	v_add_f32_dpp v44, v44, v44 row_half_mirror row_mask:0xf bank_mask:0xf bound_ctrl:1
	v_exp_f32_e32 v42, v42
	v_lshl_add_u64 v[38:39], s[36:37], 0, v[38:39]
	v_add_f32_dpp v44, v44, v44 row_mirror row_mask:0xf bank_mask:0xf bound_ctrl:1
	ds_bpermute_b32 v45, v113, v44
	v_lshl_add_u64 v[38:39], v[38:39], 0, s[56:57]
	v_lshl_add_u64 v[38:39], v[38:39], 0, v[2:3]
	global_store_short_d16_hi v[38:39], v41, off offset:1536
	v_add_f32_e32 v41, 1.0, v42
	s_waitcnt lgkmcnt(0)
	v_add_f32_e32 v42, v44, v45
	v_fmamk_f32 v42, v42, 0x3c800000, v1
	v_mul_f32_e32 v44, 0x4f800000, v42
	v_cmp_gt_f32_e32 vcc, s29, v42
	v_rcp_f32_e32 v41, v41
	v_mul_f32_e32 v40, v63, v40
	v_cndmask_b32_e32 v42, v42, v44, vcc
	v_sqrt_f32_e32 v44, v42
	v_mul_f32_e32 v40, v109, v40
	v_mul_f32_e32 v40, v40, v43
	v_mul_f32_e32 v40, v41, v40
	v_add_u32_e32 v41, -1, v44
	v_fma_f32 v43, -v41, v44, v42
	v_cmp_ge_f32_e64 s[38:39], 0, v43
	v_add_u32_e32 v43, 1, v44
	s_nop 0
	v_cndmask_b32_e64 v41, v44, v41, s[38:39]
	v_fma_f32 v44, -v43, v44, v42
	v_cmp_lt_f32_e64 s[38:39], 0, v44
	v_bfe_u32 v44, v40, 16, 1
	v_add3_u32 v40, v40, v44, s1
	v_cndmask_b32_e64 v41, v41, v43, s[38:39]
	v_mul_f32_e32 v43, 0x37800000, v41
	v_cndmask_b32_e32 v41, v41, v43, vcc
	v_cmp_class_f32_e32 vcc, v42, v248
	global_store_short_d16_hi v[38:39], v40, off offset:1600
	s_nop 0
	v_cndmask_b32_e32 v41, v41, v42, vcc
	v_div_scale_f32 v42, s[8:9], v41, v41, 1.0
	v_rcp_f32_e32 v43, v42
	s_nop 0
	v_fma_f32 v38, -v42, v43, 1.0
	v_fmac_f32_e32 v43, v38, v43
	v_div_scale_f32 v38, vcc, 1.0, v41, 1.0
	v_mul_f32_e32 v39, v38, v43
	v_fma_f32 v40, -v42, v39, v38
	v_fmac_f32_e32 v39, v40, v43
	v_fma_f32 v38, -v42, v39, v38
	v_div_fmas_f32 v38, v38, v43, v39
	v_div_fixup_f32 v40, v38, v41, 1.0
	s_waitcnt vmcnt(62)
	v_lshlrev_b32_e32 v41, 16, v226
	v_mul_f32_e32 v42, 0xbfb8aa3b, v41
	v_exp_f32_e32 v42, v42
	v_mul_f32_e32 v44, v48, v40
	v_mul_f32_e32 v44, v111, v44
	v_mul_f32_e32 v41, v44, v41
	v_add_f32_e32 v42, 1.0, v42
	v_rcp_f32_e32 v42, v42
	v_mul_f32_e32 v44, v65, v65
	v_fmac_f32_e32 v44, v49, v49
	v_lshlrev_b32_e32 v43, 16, v218
	v_mul_f32_e32 v41, v42, v41
	v_add_f32_dpp v44, v44, v44 quad_perm:[1,0,3,2] row_mask:0xf bank_mask:0xf bound_ctrl:1
	v_bfe_u32 v42, v41, 16, 1
	v_add3_u32 v41, v41, v42, s1
	v_add_f32_dpp v44, v44, v44 quad_perm:[2,3,0,1] row_mask:0xf bank_mask:0xf bound_ctrl:1
	v_mul_f32_e32 v42, 0xbfb8aa3b, v43
	v_lshlrev_b64 v[38:39], 11, v[176:177]
	v_add_f32_dpp v44, v44, v44 row_half_mirror row_mask:0xf bank_mask:0xf bound_ctrl:1
	v_exp_f32_e32 v42, v42
	v_lshl_add_u64 v[38:39], s[36:37], 0, v[38:39]
	v_add_f32_dpp v44, v44, v44 row_mirror row_mask:0xf bank_mask:0xf bound_ctrl:1
	ds_bpermute_b32 v45, v113, v44
	v_lshl_add_u64 v[38:39], v[38:39], 0, s[56:57]
	v_lshl_add_u64 v[38:39], v[38:39], 0, v[2:3]
	global_store_short_d16_hi v[38:39], v41, off offset:1536
	v_add_f32_e32 v41, 1.0, v42
	s_waitcnt lgkmcnt(0)
	v_add_f32_e32 v42, v44, v45
	v_fmamk_f32 v42, v42, 0x3c800000, v1
	v_mul_f32_e32 v44, 0x4f800000, v42
	v_cmp_gt_f32_e32 vcc, s29, v42
	v_rcp_f32_e32 v41, v41
	v_mul_f32_e32 v40, v64, v40
	v_cndmask_b32_e32 v42, v42, v44, vcc
	v_sqrt_f32_e32 v44, v42
	v_mul_f32_e32 v40, v109, v40
	v_mul_f32_e32 v40, v40, v43
	v_mul_f32_e32 v40, v41, v40
	v_add_u32_e32 v41, -1, v44
	v_fma_f32 v43, -v41, v44, v42
	v_cmp_ge_f32_e64 s[38:39], 0, v43
	v_add_u32_e32 v43, 1, v44
	s_nop 0
	v_cndmask_b32_e64 v41, v44, v41, s[38:39]
	v_fma_f32 v44, -v43, v44, v42
	v_cmp_lt_f32_e64 s[38:39], 0, v44
	v_bfe_u32 v44, v40, 16, 1
	v_add3_u32 v40, v40, v44, s1
	v_cndmask_b32_e64 v41, v41, v43, s[38:39]
	v_mul_f32_e32 v43, 0x37800000, v41
	v_cndmask_b32_e32 v41, v41, v43, vcc
	v_cmp_class_f32_e32 vcc, v42, v248
	global_store_short_d16_hi v[38:39], v40, off offset:1600
	s_nop 0
	v_cndmask_b32_e32 v41, v41, v42, vcc
	v_div_scale_f32 v42, s[8:9], v41, v41, 1.0
	v_rcp_f32_e32 v43, v42
	s_nop 0
	v_fma_f32 v38, -v42, v43, 1.0
	v_fmac_f32_e32 v43, v38, v43
	v_div_scale_f32 v38, vcc, 1.0, v41, 1.0
	v_mul_f32_e32 v39, v38, v43
	v_fma_f32 v40, -v42, v39, v38
	v_fmac_f32_e32 v39, v40, v43
	v_fma_f32 v38, -v42, v39, v38
	v_div_fmas_f32 v38, v38, v43, v39
	v_div_fixup_f32 v40, v38, v41, 1.0
	s_waitcnt vmcnt(62)
	v_lshlrev_b32_e32 v41, 16, v217
	v_mul_f32_e32 v42, 0xbfb8aa3b, v41
	v_exp_f32_e32 v42, v42
	v_mul_f32_e32 v44, v49, v40
	v_mul_f32_e32 v44, v111, v44
	v_mul_f32_e32 v41, v44, v41
	v_add_f32_e32 v42, 1.0, v42
	v_rcp_f32_e32 v42, v42
	v_mul_f32_e32 v44, v66, v66
	v_fmac_f32_e32 v44, v50, v50
	v_lshlrev_b32_e32 v43, 16, v216
	v_mul_f32_e32 v41, v42, v41
	v_add_f32_dpp v44, v44, v44 quad_perm:[1,0,3,2] row_mask:0xf bank_mask:0xf bound_ctrl:1
	v_bfe_u32 v42, v41, 16, 1
	v_add3_u32 v41, v41, v42, s1
	v_add_f32_dpp v44, v44, v44 quad_perm:[2,3,0,1] row_mask:0xf bank_mask:0xf bound_ctrl:1
	v_mul_f32_e32 v42, 0xbfb8aa3b, v43
	v_lshlrev_b64 v[38:39], 11, v[102:103]
	v_add_f32_dpp v44, v44, v44 row_half_mirror row_mask:0xf bank_mask:0xf bound_ctrl:1
	v_exp_f32_e32 v42, v42
	v_lshl_add_u64 v[38:39], s[36:37], 0, v[38:39]
	v_add_f32_dpp v44, v44, v44 row_mirror row_mask:0xf bank_mask:0xf bound_ctrl:1
	ds_bpermute_b32 v45, v113, v44
	v_lshl_add_u64 v[38:39], v[38:39], 0, s[56:57]
	v_lshl_add_u64 v[38:39], v[38:39], 0, v[2:3]
	global_store_short_d16_hi v[38:39], v41, off offset:1536
	v_add_f32_e32 v41, 1.0, v42
	s_waitcnt lgkmcnt(0)
	v_add_f32_e32 v42, v44, v45
	v_fmamk_f32 v42, v42, 0x3c800000, v1
	v_mul_f32_e32 v44, 0x4f800000, v42
	v_cmp_gt_f32_e32 vcc, s29, v42
	v_rcp_f32_e32 v41, v41
	v_mul_f32_e32 v40, v65, v40
	v_cndmask_b32_e32 v42, v42, v44, vcc
	v_sqrt_f32_e32 v44, v42
	v_mul_f32_e32 v40, v109, v40
	v_mul_f32_e32 v40, v40, v43
	v_mul_f32_e32 v40, v41, v40
	v_add_u32_e32 v41, -1, v44
	v_fma_f32 v43, -v41, v44, v42
	v_cmp_ge_f32_e64 s[38:39], 0, v43
	v_add_u32_e32 v43, 1, v44
	s_nop 0
	v_cndmask_b32_e64 v41, v44, v41, s[38:39]
	v_fma_f32 v44, -v43, v44, v42
	v_cmp_lt_f32_e64 s[38:39], 0, v44
	v_bfe_u32 v44, v40, 16, 1
	v_add3_u32 v40, v40, v44, s1
	v_cndmask_b32_e64 v41, v41, v43, s[38:39]
	v_mul_f32_e32 v43, 0x37800000, v41
	v_cndmask_b32_e32 v41, v41, v43, vcc
	v_cmp_class_f32_e32 vcc, v42, v248
	global_store_short_d16_hi v[38:39], v40, off offset:1600
	s_nop 0
	v_cndmask_b32_e32 v41, v41, v42, vcc
	v_div_scale_f32 v42, s[8:9], v41, v41, 1.0
	v_rcp_f32_e32 v43, v42
	s_nop 0
	v_fma_f32 v38, -v42, v43, 1.0
	v_fmac_f32_e32 v43, v38, v43
	v_div_scale_f32 v38, vcc, 1.0, v41, 1.0
	v_mul_f32_e32 v39, v38, v43
	v_fma_f32 v40, -v42, v39, v38
	v_fmac_f32_e32 v39, v40, v43
	v_fma_f32 v38, -v42, v39, v38
	v_div_fmas_f32 v38, v38, v43, v39
	v_div_fixup_f32 v40, v38, v41, 1.0
	s_waitcnt vmcnt(62)
	v_lshlrev_b32_e32 v41, 16, v215
	v_mul_f32_e32 v42, 0xbfb8aa3b, v41
	v_exp_f32_e32 v42, v42
	v_mul_f32_e32 v44, v50, v40
	v_mul_f32_e32 v44, v111, v44
	v_mul_f32_e32 v41, v44, v41
	v_add_f32_e32 v42, 1.0, v42
	v_rcp_f32_e32 v42, v42
	v_mul_f32_e32 v44, v67, v67
	v_fmac_f32_e32 v44, v51, v51
	v_lshlrev_b32_e32 v43, 16, v214
	v_mul_f32_e32 v41, v42, v41
	v_add_f32_dpp v44, v44, v44 quad_perm:[1,0,3,2] row_mask:0xf bank_mask:0xf bound_ctrl:1
	v_bfe_u32 v42, v41, 16, 1
	v_add3_u32 v41, v41, v42, s1
	v_add_f32_dpp v44, v44, v44 quad_perm:[2,3,0,1] row_mask:0xf bank_mask:0xf bound_ctrl:1
	v_mul_f32_e32 v42, 0xbfb8aa3b, v43
	v_lshlrev_b64 v[38:39], 11, v[100:101]
	v_add_f32_dpp v44, v44, v44 row_half_mirror row_mask:0xf bank_mask:0xf bound_ctrl:1
	v_exp_f32_e32 v42, v42
	v_lshl_add_u64 v[38:39], s[36:37], 0, v[38:39]
	v_add_f32_dpp v44, v44, v44 row_mirror row_mask:0xf bank_mask:0xf bound_ctrl:1
	ds_bpermute_b32 v45, v113, v44
	v_lshl_add_u64 v[38:39], v[38:39], 0, s[56:57]
	v_lshl_add_u64 v[38:39], v[38:39], 0, v[2:3]
	global_store_short_d16_hi v[38:39], v41, off offset:1536
	v_add_f32_e32 v41, 1.0, v42
	s_waitcnt lgkmcnt(0)
	v_add_f32_e32 v42, v44, v45
	v_fmamk_f32 v42, v42, 0x3c800000, v1
	v_mul_f32_e32 v44, 0x4f800000, v42
	v_cmp_gt_f32_e32 vcc, s29, v42
	v_rcp_f32_e32 v41, v41
	v_mul_f32_e32 v40, v66, v40
	v_cndmask_b32_e32 v42, v42, v44, vcc
	v_sqrt_f32_e32 v44, v42
	v_mul_f32_e32 v40, v109, v40
	v_mul_f32_e32 v40, v40, v43
	v_mul_f32_e32 v40, v41, v40
	v_add_u32_e32 v41, -1, v44
	v_fma_f32 v43, -v41, v44, v42
	v_cmp_ge_f32_e64 s[38:39], 0, v43
	v_add_u32_e32 v43, 1, v44
	s_nop 0
	v_cndmask_b32_e64 v41, v44, v41, s[38:39]
	v_fma_f32 v44, -v43, v44, v42
	v_cmp_lt_f32_e64 s[38:39], 0, v44
	v_bfe_u32 v44, v40, 16, 1
	v_add3_u32 v40, v40, v44, s1
	v_cndmask_b32_e64 v41, v41, v43, s[38:39]
	v_mul_f32_e32 v43, 0x37800000, v41
	v_cndmask_b32_e32 v41, v41, v43, vcc
	v_cmp_class_f32_e32 vcc, v42, v248
	global_store_short_d16_hi v[38:39], v40, off offset:1600
	s_nop 0
	v_cndmask_b32_e32 v41, v41, v42, vcc
	v_div_scale_f32 v42, s[8:9], v41, v41, 1.0
	v_rcp_f32_e32 v43, v42
	s_nop 0
	v_fma_f32 v38, -v42, v43, 1.0
	v_fmac_f32_e32 v43, v38, v43
	v_div_scale_f32 v38, vcc, 1.0, v41, 1.0
	v_mul_f32_e32 v39, v38, v43
	v_fma_f32 v40, -v42, v39, v38
	v_fmac_f32_e32 v39, v40, v43
	v_fma_f32 v38, -v42, v39, v38
	v_div_fmas_f32 v38, v38, v43, v39
	v_div_fixup_f32 v40, v38, v41, 1.0
	s_waitcnt vmcnt(62)
	v_lshlrev_b32_e32 v41, 16, v213
	v_mul_f32_e32 v42, 0xbfb8aa3b, v41
	v_exp_f32_e32 v42, v42
	v_mul_f32_e32 v44, v51, v40
	v_mul_f32_e32 v44, v111, v44
	v_mul_f32_e32 v41, v44, v41
	v_add_f32_e32 v42, 1.0, v42
	v_rcp_f32_e32 v42, v42
	v_mul_f32_e32 v44, v4, v4
	v_fmac_f32_e32 v44, v20, v20
	v_lshlrev_b32_e32 v43, 16, v212
	v_mul_f32_e32 v41, v42, v41
	v_add_f32_dpp v44, v44, v44 quad_perm:[1,0,3,2] row_mask:0xf bank_mask:0xf bound_ctrl:1
	v_bfe_u32 v42, v41, 16, 1
	v_add3_u32 v41, v41, v42, s1
	v_add_f32_dpp v44, v44, v44 quad_perm:[2,3,0,1] row_mask:0xf bank_mask:0xf bound_ctrl:1
	v_mul_f32_e32 v42, 0xbfb8aa3b, v43
	v_lshlrev_b64 v[38:39], 11, v[96:97]
	v_add_f32_dpp v44, v44, v44 row_half_mirror row_mask:0xf bank_mask:0xf bound_ctrl:1
	v_exp_f32_e32 v42, v42
	v_lshl_add_u64 v[38:39], s[36:37], 0, v[38:39]
	v_add_f32_dpp v44, v44, v44 row_mirror row_mask:0xf bank_mask:0xf bound_ctrl:1
	ds_bpermute_b32 v45, v113, v44
	v_lshl_add_u64 v[38:39], v[38:39], 0, s[56:57]
	v_lshl_add_u64 v[38:39], v[38:39], 0, v[2:3]
	global_store_short_d16_hi v[38:39], v41, off offset:1536
	v_add_f32_e32 v41, 1.0, v42
	s_waitcnt lgkmcnt(0)
	v_add_f32_e32 v42, v44, v45
	v_fmamk_f32 v42, v42, 0x3c800000, v1
	v_mul_f32_e32 v44, 0x4f800000, v42
	v_cmp_gt_f32_e32 vcc, s29, v42
	v_rcp_f32_e32 v41, v41
	v_mul_f32_e32 v40, v67, v40
	v_cndmask_b32_e32 v42, v42, v44, vcc
	v_sqrt_f32_e32 v44, v42
	v_mul_f32_e32 v40, v109, v40
	v_mul_f32_e32 v40, v40, v43
	v_mul_f32_e32 v40, v41, v40
	v_add_u32_e32 v41, -1, v44
	v_fma_f32 v43, -v41, v44, v42
	v_cmp_ge_f32_e64 s[38:39], 0, v43
	v_add_u32_e32 v43, 1, v44
	s_nop 0
	v_cndmask_b32_e64 v41, v44, v41, s[38:39]
	v_fma_f32 v44, -v43, v44, v42
	v_cmp_lt_f32_e64 s[38:39], 0, v44
	v_bfe_u32 v44, v40, 16, 1
	v_add3_u32 v40, v40, v44, s1
	v_cndmask_b32_e64 v41, v41, v43, s[38:39]
	v_mul_f32_e32 v43, 0x37800000, v41
	v_cndmask_b32_e32 v41, v41, v43, vcc
	v_cmp_class_f32_e32 vcc, v42, v248
	global_store_short_d16_hi v[38:39], v40, off offset:1600
	s_nop 0
	v_cndmask_b32_e32 v41, v41, v42, vcc
	v_div_scale_f32 v42, s[8:9], v41, v41, 1.0
	v_rcp_f32_e32 v43, v42
	s_nop 0
	v_fma_f32 v38, -v42, v43, 1.0
	v_fmac_f32_e32 v43, v38, v43
	v_div_scale_f32 v38, vcc, 1.0, v41, 1.0
	v_mul_f32_e32 v39, v38, v43
	v_fma_f32 v40, -v42, v39, v38
	v_fmac_f32_e32 v39, v40, v43
	v_fma_f32 v38, -v42, v39, v38
	v_div_fmas_f32 v38, v38, v43, v39
	v_div_fixup_f32 v40, v38, v41, 1.0
	s_waitcnt vmcnt(62)
	v_lshlrev_b32_e32 v41, 16, v203
	v_mul_f32_e32 v42, 0xbfb8aa3b, v41
	v_exp_f32_e32 v42, v42
	v_mul_f32_e32 v20, v20, v40
	v_mul_f32_e32 v20, v111, v20
	v_mul_f32_e32 v20, v20, v41
	v_add_f32_e32 v42, 1.0, v42
	v_rcp_f32_e32 v42, v42
	v_lshlrev_b32_e32 v43, 16, v175
	v_lshlrev_b64 v[38:39], 11, v[90:91]
	v_lshl_add_u64 v[38:39], s[36:37], 0, v[38:39]
	v_mul_f32_e32 v20, v42, v20
	v_mul_f32_e32 v42, v5, v5
	v_fmac_f32_e32 v42, v21, v21
	v_bfe_u32 v41, v20, 16, 1
	v_add3_u32 v20, v20, v41, s1
	v_add_f32_dpp v42, v42, v42 quad_perm:[1,0,3,2] row_mask:0xf bank_mask:0xf bound_ctrl:1
	v_mul_f32_e32 v41, 0xbfb8aa3b, v43
	v_exp_f32_e32 v41, v41
	v_add_f32_dpp v42, v42, v42 quad_perm:[2,3,0,1] row_mask:0xf bank_mask:0xf bound_ctrl:1
	v_lshl_add_u64 v[38:39], v[38:39], 0, s[56:57]
	v_mul_f32_e32 v4, v4, v40
	v_add_f32_dpp v42, v42, v42 row_half_mirror row_mask:0xf bank_mask:0xf bound_ctrl:1
	v_lshl_add_u64 v[38:39], v[38:39], 0, v[2:3]
	global_store_short_d16_hi v[38:39], v20, off offset:1536
	v_add_f32_dpp v42, v42, v42 row_mirror row_mask:0xf bank_mask:0xf bound_ctrl:1
	ds_bpermute_b32 v44, v113, v42
	v_add_f32_e32 v20, 1.0, v41
	v_rcp_f32_e32 v20, v20
	v_mul_f32_e32 v4, v109, v4
	v_mul_f32_e32 v4, v4, v43
	s_waitcnt lgkmcnt(0)
	v_add_f32_e32 v40, v42, v44
	v_fmamk_f32 v40, v40, 0x3c800000, v1
	v_mul_f32_e32 v41, 0x4f800000, v40
	v_cmp_gt_f32_e32 vcc, s29, v40
	v_mul_f32_e32 v4, v20, v4
	s_nop 0
	v_cndmask_b32_e32 v40, v40, v41, vcc
	v_sqrt_f32_e32 v41, v40
	s_nop 0
	v_add_u32_e32 v20, -1, v41
	v_fma_f32 v42, -v20, v41, v40
	v_cmp_ge_f32_e64 s[38:39], 0, v42
	v_add_u32_e32 v42, 1, v41
	s_nop 0
	v_cndmask_b32_e64 v20, v41, v20, s[38:39]
	v_fma_f32 v41, -v42, v41, v40
	v_cmp_lt_f32_e64 s[38:39], 0, v41
	s_nop 1
	v_cndmask_b32_e64 v20, v20, v42, s[38:39]
	v_mul_f32_e32 v41, 0x37800000, v20
	v_cndmask_b32_e32 v20, v20, v41, vcc
	v_cmp_class_f32_e32 vcc, v40, v248
	v_bfe_u32 v42, v4, 16, 1
	v_add3_u32 v4, v4, v42, s1
	v_cndmask_b32_e32 v20, v20, v40, vcc
	v_div_scale_f32 v40, s[8:9], v20, v20, 1.0
	v_rcp_f32_e32 v41, v40
	global_store_short_d16_hi v[38:39], v4, off offset:1600
	v_fma_f32 v4, -v40, v41, 1.0
	v_fmac_f32_e32 v41, v4, v41
	v_div_scale_f32 v4, vcc, 1.0, v20, 1.0
	v_mul_f32_e32 v38, v4, v41
	v_fma_f32 v39, -v40, v38, v4
	v_fmac_f32_e32 v38, v39, v41
	v_fma_f32 v4, -v40, v38, v4
	v_div_fmas_f32 v4, v4, v41, v38
	v_div_fixup_f32 v4, v4, v20, 1.0
	s_waitcnt vmcnt(62)
	v_lshlrev_b32_e32 v20, 16, v173
	v_mul_f32_e32 v40, 0xbfb8aa3b, v20
	v_exp_f32_e32 v40, v40
	v_mul_f32_e32 v21, v21, v4
	v_mul_f32_e32 v21, v111, v21
	v_mul_f32_e32 v20, v21, v20
	v_add_f32_e32 v40, 1.0, v40
	v_rcp_f32_e32 v40, v40
	v_lshlrev_b64 v[38:39], 11, v[98:99]
	v_lshlrev_b32_e32 v41, 16, v171
	v_lshl_add_u64 v[38:39], s[36:37], 0, v[38:39]
	v_mul_f32_e32 v20, v40, v20
	v_mul_f32_e32 v40, v6, v6
	v_fmac_f32_e32 v40, v22, v22
	v_bfe_u32 v21, v20, 16, 1
	v_add3_u32 v20, v20, v21, s1
	v_add_f32_dpp v40, v40, v40 quad_perm:[1,0,3,2] row_mask:0xf bank_mask:0xf bound_ctrl:1
	v_mul_f32_e32 v21, 0xbfb8aa3b, v41
	v_lshl_add_u64 v[38:39], v[38:39], 0, s[56:57]
	v_add_f32_dpp v40, v40, v40 quad_perm:[2,3,0,1] row_mask:0xf bank_mask:0xf bound_ctrl:1
	v_exp_f32_e32 v21, v21
	v_lshl_add_u64 v[38:39], v[38:39], 0, v[2:3]
	v_add_f32_dpp v40, v40, v40 row_half_mirror row_mask:0xf bank_mask:0xf bound_ctrl:1
	global_store_short_d16_hi v[38:39], v20, off offset:1536
	v_mul_f32_e32 v4, v5, v4
	v_add_f32_dpp v40, v40, v40 row_mirror row_mask:0xf bank_mask:0xf bound_ctrl:1
	ds_bpermute_b32 v42, v113, v40
	v_add_f32_e32 v5, 1.0, v21
	v_rcp_f32_e32 v5, v5
	v_mul_f32_e32 v4, v109, v4
	v_mul_f32_e32 v4, v4, v41
	s_waitcnt lgkmcnt(0)
	v_add_f32_e32 v20, v40, v42
	v_fmamk_f32 v20, v20, 0x3c800000, v1
	v_mul_f32_e32 v21, 0x4f800000, v20
	v_cmp_gt_f32_e32 vcc, s29, v20
	v_mul_f32_e32 v4, v5, v4
	s_nop 0
	v_cndmask_b32_e32 v20, v20, v21, vcc
	v_sqrt_f32_e32 v21, v20
	s_nop 0
	v_add_u32_e32 v5, -1, v21
	v_fma_f32 v40, -v5, v21, v20
	v_cmp_ge_f32_e64 s[38:39], 0, v40
	v_add_u32_e32 v40, 1, v21
	s_nop 0
	v_cndmask_b32_e64 v5, v21, v5, s[38:39]
	v_fma_f32 v21, -v40, v21, v20
	v_cmp_lt_f32_e64 s[38:39], 0, v21
	s_nop 1
	v_cndmask_b32_e64 v5, v5, v40, s[38:39]
	v_mul_f32_e32 v21, 0x37800000, v5
	v_cndmask_b32_e32 v5, v5, v21, vcc
	v_cmp_class_f32_e32 vcc, v20, v248
	v_bfe_u32 v40, v4, 16, 1
	v_add3_u32 v4, v4, v40, s1
	v_cndmask_b32_e32 v5, v5, v20, vcc
	v_div_scale_f32 v20, s[8:9], v5, v5, 1.0
	v_rcp_f32_e32 v21, v20
	global_store_short_d16_hi v[38:39], v4, off offset:1600
	v_fma_f32 v4, -v20, v21, 1.0
	v_fmac_f32_e32 v21, v4, v21
	v_div_scale_f32 v4, vcc, 1.0, v5, 1.0
	v_mul_f32_e32 v38, v4, v21
	v_fma_f32 v39, -v20, v38, v4
	v_fmac_f32_e32 v38, v39, v21
	v_fma_f32 v4, -v20, v38, v4
	v_div_fmas_f32 v4, v4, v21, v38
	s_waitcnt vmcnt(62)
	v_lshlrev_b32_e32 v21, 16, v169
	v_mul_f32_e32 v38, 0xbfb8aa3b, v21
	v_exp_f32_e32 v38, v38
	v_div_fixup_f32 v20, v4, v5, 1.0
	v_mul_f32_e32 v22, v22, v20
	v_mul_f32_e32 v22, v111, v22
	v_add_f32_e32 v38, 1.0, v38
	v_rcp_f32_e32 v38, v38
	v_mul_f32_e32 v21, v22, v21
	v_lshlrev_b64 v[4:5], 11, v[94:95]
	v_lshlrev_b32_e32 v39, 16, v167
	v_mul_f32_e32 v21, v38, v21
	v_mul_f32_e32 v38, v7, v7
	v_fmac_f32_e32 v38, v23, v23
	v_bfe_u32 v22, v21, 16, 1
	v_lshl_add_u64 v[4:5], s[36:37], 0, v[4:5]
	v_add_f32_dpp v38, v38, v38 quad_perm:[1,0,3,2] row_mask:0xf bank_mask:0xf bound_ctrl:1
	v_add3_u32 v21, v21, v22, s1
	v_mul_f32_e32 v22, 0xbfb8aa3b, v39
	v_add_f32_dpp v38, v38, v38 quad_perm:[2,3,0,1] row_mask:0xf bank_mask:0xf bound_ctrl:1
	v_lshl_add_u64 v[4:5], v[4:5], 0, s[56:57]
	v_exp_f32_e32 v22, v22
	v_add_f32_dpp v38, v38, v38 row_half_mirror row_mask:0xf bank_mask:0xf bound_ctrl:1
	v_lshl_add_u64 v[4:5], v[4:5], 0, v[2:3]
	global_store_short_d16_hi v[4:5], v21, off offset:1536
	v_add_f32_dpp v38, v38, v38 row_mirror row_mask:0xf bank_mask:0xf bound_ctrl:1
	ds_bpermute_b32 v40, v113, v38
	v_mul_f32_e32 v6, v6, v20
	v_add_f32_e32 v20, 1.0, v22
	v_rcp_f32_e32 v20, v20
	v_mul_f32_e32 v6, v109, v6
	s_waitcnt lgkmcnt(0)
	v_add_f32_e32 v21, v38, v40
	v_fmamk_f32 v21, v21, 0x3c800000, v1
	v_mul_f32_e32 v22, 0x4f800000, v21
	v_cmp_gt_f32_e32 vcc, s29, v21
	v_mul_f32_e32 v6, v6, v39
	v_mul_f32_e32 v6, v20, v6
	v_cndmask_b32_e32 v21, v21, v22, vcc
	v_sqrt_f32_e32 v22, v21
	s_nop 0
	v_add_u32_e32 v20, -1, v22
	v_fma_f32 v38, -v20, v22, v21
	v_cmp_ge_f32_e64 s[38:39], 0, v38
	v_add_u32_e32 v38, 1, v22
	s_nop 0
	v_cndmask_b32_e64 v20, v22, v20, s[38:39]
	v_fma_f32 v22, -v38, v22, v21
	v_cmp_lt_f32_e64 s[38:39], 0, v22
	s_nop 1
	v_cndmask_b32_e64 v20, v20, v38, s[38:39]
	v_mul_f32_e32 v22, 0x37800000, v20
	v_cndmask_b32_e32 v20, v20, v22, vcc
	v_cmp_class_f32_e32 vcc, v21, v248
	v_bfe_u32 v38, v6, 16, 1
	v_add3_u32 v6, v6, v38, s1
	v_cndmask_b32_e32 v20, v20, v21, vcc
	v_div_scale_f32 v21, s[8:9], v20, v20, 1.0
	v_rcp_f32_e32 v22, v21
	global_store_short_d16_hi v[4:5], v6, off offset:1600
	v_fma_f32 v4, -v21, v22, 1.0
	v_fmac_f32_e32 v22, v4, v22
	v_div_scale_f32 v4, vcc, 1.0, v20, 1.0
	v_mul_f32_e32 v5, v4, v22
	v_fma_f32 v6, -v21, v5, v4
	v_fmac_f32_e32 v5, v6, v22
	v_fma_f32 v4, -v21, v5, v4
	v_div_fmas_f32 v4, v4, v22, v5
	v_div_fixup_f32 v6, v4, v20, 1.0
	s_waitcnt vmcnt(62)
	v_lshlrev_b32_e32 v20, 16, v165
	v_mul_f32_e32 v21, 0xbfb8aa3b, v20
	v_exp_f32_e32 v21, v21
	v_mul_f32_e32 v23, v23, v6
	v_mul_f32_e32 v23, v111, v23
	v_mul_f32_e32 v20, v23, v20
	v_mul_f32_e32 v23, v8, v8
	v_add_f32_e32 v21, 1.0, v21
	v_fmac_f32_e32 v23, v24, v24
	v_rcp_f32_e32 v21, v21
	v_lshlrev_b64 v[4:5], 11, v[92:93]
	v_add_f32_dpp v23, v23, v23 quad_perm:[1,0,3,2] row_mask:0xf bank_mask:0xf bound_ctrl:1
	v_lshlrev_b32_e32 v22, 16, v163
	v_mul_f32_e32 v20, v21, v20
	v_add_f32_dpp v23, v23, v23 quad_perm:[2,3,0,1] row_mask:0xf bank_mask:0xf bound_ctrl:1
	v_bfe_u32 v21, v20, 16, 1
	v_lshl_add_u64 v[4:5], s[36:37], 0, v[4:5]
	v_add_f32_dpp v23, v23, v23 row_half_mirror row_mask:0xf bank_mask:0xf bound_ctrl:1
	v_add3_u32 v20, v20, v21, s1
	v_mul_f32_e32 v21, 0xbfb8aa3b, v22
	v_add_f32_dpp v23, v23, v23 row_mirror row_mask:0xf bank_mask:0xf bound_ctrl:1
	ds_bpermute_b32 v38, v113, v23
	v_lshl_add_u64 v[4:5], v[4:5], 0, s[56:57]
	v_exp_f32_e32 v21, v21
	v_lshl_add_u64 v[4:5], v[4:5], 0, v[2:3]
	global_store_short_d16_hi v[4:5], v20, off offset:1536
	s_waitcnt lgkmcnt(0)
	v_add_f32_e32 v20, v23, v38
	v_fmamk_f32 v20, v20, 0x3c800000, v1
	v_mul_f32_e32 v6, v7, v6
	v_add_f32_e32 v7, 1.0, v21
	v_mul_f32_e32 v21, 0x4f800000, v20
	v_cmp_gt_f32_e32 vcc, s29, v20
	v_rcp_f32_e32 v7, v7
	v_mul_f32_e32 v6, v109, v6
	v_cndmask_b32_e32 v20, v20, v21, vcc
	v_sqrt_f32_e32 v21, v20
	v_mul_f32_e32 v6, v6, v22
	v_mul_f32_e32 v6, v7, v6
	v_add_u32_e32 v7, -1, v21
	v_fma_f32 v22, -v7, v21, v20
	v_cmp_ge_f32_e64 s[38:39], 0, v22
	v_add_u32_e32 v22, 1, v21
	s_nop 0
	v_cndmask_b32_e64 v7, v21, v7, s[38:39]
	v_fma_f32 v21, -v22, v21, v20
	v_cmp_lt_f32_e64 s[38:39], 0, v21
	s_nop 1
	v_cndmask_b32_e64 v7, v7, v22, s[38:39]
	v_mul_f32_e32 v21, 0x37800000, v7
	v_cndmask_b32_e32 v7, v7, v21, vcc
	v_cmp_class_f32_e32 vcc, v20, v248
	v_bfe_u32 v22, v6, 16, 1
	v_add3_u32 v6, v6, v22, s1
	v_cndmask_b32_e32 v7, v7, v20, vcc
	v_div_scale_f32 v20, s[8:9], v7, v7, 1.0
	v_rcp_f32_e32 v21, v20
	global_store_short_d16_hi v[4:5], v6, off offset:1600
	v_fma_f32 v4, -v20, v21, 1.0
	v_fmac_f32_e32 v21, v4, v21
	v_div_scale_f32 v4, vcc, 1.0, v7, 1.0
	v_mul_f32_e32 v5, v4, v21
	v_fma_f32 v6, -v20, v5, v4
	v_fmac_f32_e32 v5, v6, v21
	v_fma_f32 v4, -v20, v5, v4
	v_div_fmas_f32 v4, v4, v21, v5
	v_div_fixup_f32 v6, v4, v7, 1.0
	s_waitcnt vmcnt(62)
	v_lshlrev_b32_e32 v7, 16, v161
	v_mul_f32_e32 v20, 0xbfb8aa3b, v7
	v_exp_f32_e32 v20, v20
	v_mul_f32_e32 v22, v24, v6
	v_mul_f32_e32 v22, v111, v22
	v_mul_f32_e32 v7, v22, v7
	v_mul_f32_e32 v22, v9, v9
	v_add_f32_e32 v20, 1.0, v20
	v_fmac_f32_e32 v22, v25, v25
	v_rcp_f32_e32 v20, v20
	v_lshlrev_b32_e32 v21, 16, v159
	v_add_f32_dpp v22, v22, v22 quad_perm:[1,0,3,2] row_mask:0xf bank_mask:0xf bound_ctrl:1
	v_lshlrev_b64 v[4:5], 11, v[88:89]
	v_mul_f32_e32 v7, v20, v7
	v_add_f32_dpp v22, v22, v22 quad_perm:[2,3,0,1] row_mask:0xf bank_mask:0xf bound_ctrl:1
	v_bfe_u32 v20, v7, 16, 1
	v_add3_u32 v7, v7, v20, s1
	v_add_f32_dpp v22, v22, v22 row_half_mirror row_mask:0xf bank_mask:0xf bound_ctrl:1
	v_mul_f32_e32 v20, 0xbfb8aa3b, v21
	v_exp_f32_e32 v20, v20
	v_add_f32_dpp v22, v22, v22 row_mirror row_mask:0xf bank_mask:0xf bound_ctrl:1
	ds_bpermute_b32 v23, v113, v22
	v_lshl_add_u64 v[4:5], s[36:37], 0, v[4:5]
	v_lshl_add_u64 v[4:5], v[4:5], 0, s[56:57]
	v_mul_f32_e32 v6, v8, v6
	v_lshl_add_u64 v[4:5], v[4:5], 0, v[2:3]
	s_waitcnt lgkmcnt(0)
	v_add_f32_e32 v8, v22, v23
	v_fmamk_f32 v8, v8, 0x3c800000, v1
	global_store_short_d16_hi v[4:5], v7, off offset:1536
	v_add_f32_e32 v7, 1.0, v20
	v_mul_f32_e32 v20, 0x4f800000, v8
	v_cmp_gt_f32_e32 vcc, s29, v8
	v_rcp_f32_e32 v7, v7
	v_mul_f32_e32 v6, v109, v6
	v_cndmask_b32_e32 v8, v8, v20, vcc
	v_sqrt_f32_e32 v20, v8
	v_mul_f32_e32 v6, v6, v21
	v_mul_f32_e32 v6, v7, v6
	v_add_u32_e32 v7, -1, v20
	v_fma_f32 v21, -v7, v20, v8
	v_cmp_ge_f32_e64 s[38:39], 0, v21
	v_add_u32_e32 v21, 1, v20
	s_nop 0
	v_cndmask_b32_e64 v7, v20, v7, s[38:39]
	v_fma_f32 v20, -v21, v20, v8
	v_cmp_lt_f32_e64 s[38:39], 0, v20
	s_nop 1
	v_cndmask_b32_e64 v7, v7, v21, s[38:39]
	v_mul_f32_e32 v20, 0x37800000, v7
	v_cndmask_b32_e32 v7, v7, v20, vcc
	v_cmp_class_f32_e32 vcc, v8, v248
	v_bfe_u32 v21, v6, 16, 1
	v_add3_u32 v6, v6, v21, s1
	v_cndmask_b32_e32 v7, v7, v8, vcc
	v_div_scale_f32 v8, s[8:9], v7, v7, 1.0
	v_rcp_f32_e32 v20, v8
	global_store_short_d16_hi v[4:5], v6, off offset:1600
	v_fma_f32 v4, -v8, v20, 1.0
	v_fmac_f32_e32 v20, v4, v20
	v_div_scale_f32 v4, vcc, 1.0, v7, 1.0
	v_mul_f32_e32 v5, v4, v20
	v_fma_f32 v6, -v8, v5, v4
	v_fmac_f32_e32 v5, v6, v20
	v_fma_f32 v4, -v8, v5, v4
	v_div_fmas_f32 v4, v4, v20, v5
	v_div_fixup_f32 v6, v4, v7, 1.0
	s_waitcnt vmcnt(62)
	v_lshlrev_b32_e32 v7, 16, v157
	v_mul_f32_e32 v8, 0xbfb8aa3b, v7
	v_exp_f32_e32 v8, v8
	v_mul_f32_e32 v21, v25, v6
	v_mul_f32_e32 v21, v111, v21
	v_mul_f32_e32 v7, v21, v7
	v_add_f32_e32 v8, 1.0, v8
	v_rcp_f32_e32 v8, v8
	v_mul_f32_e32 v21, v10, v10
	v_fmac_f32_e32 v21, v26, v26
	v_lshlrev_b32_e32 v20, 16, v155
	v_mul_f32_e32 v7, v8, v7
	v_add_f32_dpp v21, v21, v21 quad_perm:[1,0,3,2] row_mask:0xf bank_mask:0xf bound_ctrl:1
	v_bfe_u32 v8, v7, 16, 1
	v_add3_u32 v7, v7, v8, s1
	v_add_f32_dpp v21, v21, v21 quad_perm:[2,3,0,1] row_mask:0xf bank_mask:0xf bound_ctrl:1
	v_mul_f32_e32 v8, 0xbfb8aa3b, v20
	v_lshlrev_b64 v[4:5], 11, v[84:85]
	v_add_f32_dpp v21, v21, v21 row_half_mirror row_mask:0xf bank_mask:0xf bound_ctrl:1
	v_exp_f32_e32 v8, v8
	v_lshl_add_u64 v[4:5], s[36:37], 0, v[4:5]
	v_add_f32_dpp v21, v21, v21 row_mirror row_mask:0xf bank_mask:0xf bound_ctrl:1
	ds_bpermute_b32 v22, v113, v21
	v_lshl_add_u64 v[4:5], v[4:5], 0, s[56:57]
	v_lshl_add_u64 v[4:5], v[4:5], 0, v[2:3]
	global_store_short_d16_hi v[4:5], v7, off offset:1536
	v_add_f32_e32 v7, 1.0, v8
	s_waitcnt lgkmcnt(0)
	v_add_f32_e32 v8, v21, v22
	v_fmamk_f32 v8, v8, 0x3c800000, v1
	v_mul_f32_e32 v6, v9, v6
	v_mul_f32_e32 v9, 0x4f800000, v8
	v_cmp_gt_f32_e32 vcc, s29, v8
	v_rcp_f32_e32 v7, v7
	v_mul_f32_e32 v6, v109, v6
	v_cndmask_b32_e32 v8, v8, v9, vcc
	v_sqrt_f32_e32 v9, v8
	v_mul_f32_e32 v6, v6, v20
	v_mul_f32_e32 v6, v7, v6
	v_add_u32_e32 v7, -1, v9
	v_fma_f32 v20, -v7, v9, v8
	v_cmp_ge_f32_e64 s[38:39], 0, v20
	v_add_u32_e32 v20, 1, v9
	s_nop 0
	v_cndmask_b32_e64 v7, v9, v7, s[38:39]
	v_fma_f32 v9, -v20, v9, v8
	v_cmp_lt_f32_e64 s[38:39], 0, v9
	s_nop 1
	v_cndmask_b32_e64 v7, v7, v20, s[38:39]
	v_mul_f32_e32 v9, 0x37800000, v7
	v_cndmask_b32_e32 v7, v7, v9, vcc
	v_cmp_class_f32_e32 vcc, v8, v248
	v_bfe_u32 v20, v6, 16, 1
	v_add3_u32 v6, v6, v20, s1
	v_cndmask_b32_e32 v7, v7, v8, vcc
	v_div_scale_f32 v8, s[8:9], v7, v7, 1.0
	v_rcp_f32_e32 v9, v8
	global_store_short_d16_hi v[4:5], v6, off offset:1600
	v_fma_f32 v4, -v8, v9, 1.0
	v_fmac_f32_e32 v9, v4, v9
	v_div_scale_f32 v4, vcc, 1.0, v7, 1.0
	v_mul_f32_e32 v5, v4, v9
	v_fma_f32 v6, -v8, v5, v4
	v_fmac_f32_e32 v5, v6, v9
	v_fma_f32 v4, -v8, v5, v4
	v_div_fmas_f32 v4, v4, v9, v5
	v_div_fixup_f32 v6, v4, v7, 1.0
	s_waitcnt vmcnt(62)
	v_lshlrev_b32_e32 v7, 16, v153
	v_mul_f32_e32 v8, 0xbfb8aa3b, v7
	v_exp_f32_e32 v8, v8
	v_mul_f32_e32 v20, v26, v6
	v_mul_f32_e32 v20, v111, v20
	v_mul_f32_e32 v7, v20, v7
	v_add_f32_e32 v8, 1.0, v8
	v_rcp_f32_e32 v8, v8
	v_mul_f32_e32 v20, v11, v11
	v_fmac_f32_e32 v20, v27, v27
	v_lshlrev_b32_e32 v9, 16, v151
	v_mul_f32_e32 v7, v8, v7
	v_add_f32_dpp v20, v20, v20 quad_perm:[1,0,3,2] row_mask:0xf bank_mask:0xf bound_ctrl:1
	v_bfe_u32 v8, v7, 16, 1
	v_add3_u32 v7, v7, v8, s1
	v_add_f32_dpp v20, v20, v20 quad_perm:[2,3,0,1] row_mask:0xf bank_mask:0xf bound_ctrl:1
	v_mul_f32_e32 v8, 0xbfb8aa3b, v9
	v_lshlrev_b64 v[4:5], 11, v[86:87]
	v_add_f32_dpp v20, v20, v20 row_half_mirror row_mask:0xf bank_mask:0xf bound_ctrl:1
	v_exp_f32_e32 v8, v8
	v_lshl_add_u64 v[4:5], s[36:37], 0, v[4:5]
	v_add_f32_dpp v20, v20, v20 row_mirror row_mask:0xf bank_mask:0xf bound_ctrl:1
	ds_bpermute_b32 v21, v113, v20
	v_lshl_add_u64 v[4:5], v[4:5], 0, s[56:57]
	v_lshl_add_u64 v[4:5], v[4:5], 0, v[2:3]
	global_store_short_d16_hi v[4:5], v7, off offset:1536
	v_add_f32_e32 v7, 1.0, v8
	s_waitcnt lgkmcnt(0)
	v_add_f32_e32 v8, v20, v21
	v_fmamk_f32 v8, v8, 0x3c800000, v1
	v_mul_f32_e32 v6, v10, v6
	v_mul_f32_e32 v10, 0x4f800000, v8
	v_cmp_gt_f32_e32 vcc, s29, v8
	v_rcp_f32_e32 v7, v7
	v_mul_f32_e32 v6, v109, v6
	v_cndmask_b32_e32 v8, v8, v10, vcc
	v_sqrt_f32_e32 v10, v8
	v_mul_f32_e32 v6, v6, v9
	v_mul_f32_e32 v6, v7, v6
	v_add_u32_e32 v7, -1, v10
	v_fma_f32 v9, -v7, v10, v8
	v_cmp_ge_f32_e64 s[38:39], 0, v9
	v_add_u32_e32 v9, 1, v10
	s_nop 0
	v_cndmask_b32_e64 v7, v10, v7, s[38:39]
	v_fma_f32 v10, -v9, v10, v8
	v_cmp_lt_f32_e64 s[38:39], 0, v10
	v_bfe_u32 v10, v6, 16, 1
	v_add3_u32 v6, v6, v10, s1
	v_cndmask_b32_e64 v7, v7, v9, s[38:39]
	v_mul_f32_e32 v9, 0x37800000, v7
	v_cndmask_b32_e32 v7, v7, v9, vcc
	v_cmp_class_f32_e32 vcc, v8, v248
	global_store_short_d16_hi v[4:5], v6, off offset:1600
	s_nop 0
	v_cndmask_b32_e32 v7, v7, v8, vcc
	v_div_scale_f32 v8, s[8:9], v7, v7, 1.0
	v_rcp_f32_e32 v9, v8
	s_nop 0
	v_fma_f32 v4, -v8, v9, 1.0
	v_fmac_f32_e32 v9, v4, v9
	v_div_scale_f32 v4, vcc, 1.0, v7, 1.0
	v_mul_f32_e32 v5, v4, v9
	v_fma_f32 v6, -v8, v5, v4
	v_fmac_f32_e32 v5, v6, v9
	v_fma_f32 v4, -v8, v5, v4
	v_div_fmas_f32 v4, v4, v9, v5
	v_div_fixup_f32 v6, v4, v7, 1.0
	s_waitcnt vmcnt(62)
	v_lshlrev_b32_e32 v7, 16, v149
	v_mul_f32_e32 v8, 0xbfb8aa3b, v7
	v_exp_f32_e32 v8, v8
	v_mul_f32_e32 v10, v27, v6
	v_mul_f32_e32 v10, v111, v10
	v_mul_f32_e32 v7, v10, v7
	v_add_f32_e32 v8, 1.0, v8
	v_rcp_f32_e32 v8, v8
	v_mul_f32_e32 v10, v12, v12
	v_fmac_f32_e32 v10, v28, v28
	v_lshlrev_b32_e32 v9, 16, v147
	v_mul_f32_e32 v7, v8, v7
	v_add_f32_dpp v10, v10, v10 quad_perm:[1,0,3,2] row_mask:0xf bank_mask:0xf bound_ctrl:1
	v_bfe_u32 v8, v7, 16, 1
	v_add3_u32 v7, v7, v8, s1
	v_add_f32_dpp v10, v10, v10 quad_perm:[2,3,0,1] row_mask:0xf bank_mask:0xf bound_ctrl:1
	v_mul_f32_e32 v8, 0xbfb8aa3b, v9
	v_lshlrev_b64 v[4:5], 11, v[82:83]
	v_add_f32_dpp v10, v10, v10 row_half_mirror row_mask:0xf bank_mask:0xf bound_ctrl:1
	v_exp_f32_e32 v8, v8
	v_lshl_add_u64 v[4:5], s[36:37], 0, v[4:5]
	v_add_f32_dpp v10, v10, v10 row_mirror row_mask:0xf bank_mask:0xf bound_ctrl:1
	ds_bpermute_b32 v20, v113, v10
	v_lshl_add_u64 v[4:5], v[4:5], 0, s[56:57]
	v_lshl_add_u64 v[4:5], v[4:5], 0, v[2:3]
	global_store_short_d16_hi v[4:5], v7, off offset:1536
	v_add_f32_e32 v7, 1.0, v8
	s_waitcnt lgkmcnt(0)
	v_add_f32_e32 v8, v10, v20
	v_fmamk_f32 v8, v8, 0x3c800000, v1
	v_mul_f32_e32 v10, 0x4f800000, v8
	v_cmp_gt_f32_e32 vcc, s29, v8
	v_rcp_f32_e32 v7, v7
	v_mul_f32_e32 v6, v11, v6
	v_cndmask_b32_e32 v8, v8, v10, vcc
	v_sqrt_f32_e32 v10, v8
	v_mul_f32_e32 v6, v109, v6
	v_mul_f32_e32 v6, v6, v9
	v_mul_f32_e32 v6, v7, v6
	v_add_u32_e32 v7, -1, v10
	v_fma_f32 v9, -v7, v10, v8
	v_cmp_ge_f32_e64 s[38:39], 0, v9
	v_add_u32_e32 v9, 1, v10
	s_nop 0
	v_cndmask_b32_e64 v7, v10, v7, s[38:39]
	v_fma_f32 v10, -v9, v10, v8
	v_cmp_lt_f32_e64 s[38:39], 0, v10
	v_bfe_u32 v10, v6, 16, 1
	v_add3_u32 v6, v6, v10, s1
	v_cndmask_b32_e64 v7, v7, v9, s[38:39]
	v_mul_f32_e32 v9, 0x37800000, v7
	v_cndmask_b32_e32 v7, v7, v9, vcc
	v_cmp_class_f32_e32 vcc, v8, v248
	global_store_short_d16_hi v[4:5], v6, off offset:1600
	s_nop 0
	v_cndmask_b32_e32 v7, v7, v8, vcc
	v_div_scale_f32 v8, s[8:9], v7, v7, 1.0
	v_rcp_f32_e32 v9, v8
	s_nop 0
	v_fma_f32 v4, -v8, v9, 1.0
	v_fmac_f32_e32 v9, v4, v9
	v_div_scale_f32 v4, vcc, 1.0, v7, 1.0
	v_mul_f32_e32 v5, v4, v9
	v_fma_f32 v6, -v8, v5, v4
	v_fmac_f32_e32 v5, v6, v9
	v_fma_f32 v4, -v8, v5, v4
	v_div_fmas_f32 v4, v4, v9, v5
	v_div_fixup_f32 v6, v4, v7, 1.0
	s_waitcnt vmcnt(62)
	v_lshlrev_b32_e32 v7, 16, v145
	v_mul_f32_e32 v8, 0xbfb8aa3b, v7
	v_exp_f32_e32 v8, v8
	v_mul_f32_e32 v10, v28, v6
	v_mul_f32_e32 v10, v111, v10
	v_mul_f32_e32 v7, v10, v7
	v_add_f32_e32 v8, 1.0, v8
	v_rcp_f32_e32 v8, v8
	v_mul_f32_e32 v10, v13, v13
	v_fmac_f32_e32 v10, v29, v29
	v_lshlrev_b32_e32 v9, 16, v143
	v_mul_f32_e32 v7, v8, v7
	v_add_f32_dpp v10, v10, v10 quad_perm:[1,0,3,2] row_mask:0xf bank_mask:0xf bound_ctrl:1
	v_bfe_u32 v8, v7, 16, 1
	v_add3_u32 v7, v7, v8, s1
	v_add_f32_dpp v10, v10, v10 quad_perm:[2,3,0,1] row_mask:0xf bank_mask:0xf bound_ctrl:1
	v_mul_f32_e32 v8, 0xbfb8aa3b, v9
	v_lshlrev_b64 v[4:5], 11, v[80:81]
	v_add_f32_dpp v10, v10, v10 row_half_mirror row_mask:0xf bank_mask:0xf bound_ctrl:1
	v_exp_f32_e32 v8, v8
	v_lshl_add_u64 v[4:5], s[36:37], 0, v[4:5]
	v_add_f32_dpp v10, v10, v10 row_mirror row_mask:0xf bank_mask:0xf bound_ctrl:1
	ds_bpermute_b32 v11, v113, v10
	v_lshl_add_u64 v[4:5], v[4:5], 0, s[56:57]
	v_lshl_add_u64 v[4:5], v[4:5], 0, v[2:3]
	global_store_short_d16_hi v[4:5], v7, off offset:1536
	v_add_f32_e32 v7, 1.0, v8
	s_waitcnt lgkmcnt(0)
	v_add_f32_e32 v8, v10, v11
	v_fmamk_f32 v8, v8, 0x3c800000, v1
	v_mul_f32_e32 v10, 0x4f800000, v8
	v_cmp_gt_f32_e32 vcc, s29, v8
	v_rcp_f32_e32 v7, v7
	v_mul_f32_e32 v6, v12, v6
	v_cndmask_b32_e32 v8, v8, v10, vcc
	v_sqrt_f32_e32 v10, v8
	v_mul_f32_e32 v6, v109, v6
	v_mul_f32_e32 v6, v6, v9
	v_mul_f32_e32 v6, v7, v6
	v_add_u32_e32 v7, -1, v10
	v_fma_f32 v9, -v7, v10, v8
	v_cmp_ge_f32_e64 s[38:39], 0, v9
	v_add_u32_e32 v9, 1, v10
	s_nop 0
	v_cndmask_b32_e64 v7, v10, v7, s[38:39]
	v_fma_f32 v10, -v9, v10, v8
	v_cmp_lt_f32_e64 s[38:39], 0, v10
	v_bfe_u32 v10, v6, 16, 1
	v_add3_u32 v6, v6, v10, s1
	v_cndmask_b32_e64 v7, v7, v9, s[38:39]
	v_mul_f32_e32 v9, 0x37800000, v7
	v_cndmask_b32_e32 v7, v7, v9, vcc
	v_cmp_class_f32_e32 vcc, v8, v248
	global_store_short_d16_hi v[4:5], v6, off offset:1600
	s_nop 0
	v_cndmask_b32_e32 v7, v7, v8, vcc
	v_div_scale_f32 v8, s[8:9], v7, v7, 1.0
	v_rcp_f32_e32 v9, v8
	s_nop 0
	v_fma_f32 v4, -v8, v9, 1.0
	v_fmac_f32_e32 v9, v4, v9
	v_div_scale_f32 v4, vcc, 1.0, v7, 1.0
	v_mul_f32_e32 v5, v4, v9
	v_fma_f32 v6, -v8, v5, v4
	v_fmac_f32_e32 v5, v6, v9
	v_fma_f32 v4, -v8, v5, v4
	v_div_fmas_f32 v4, v4, v9, v5
	v_div_fixup_f32 v6, v4, v7, 1.0
	s_waitcnt vmcnt(62)
	v_lshlrev_b32_e32 v7, 16, v141
	v_mul_f32_e32 v8, 0xbfb8aa3b, v7
	v_exp_f32_e32 v8, v8
	v_mul_f32_e32 v10, v29, v6
	v_mul_f32_e32 v10, v111, v10
	v_mul_f32_e32 v7, v10, v7
	v_add_f32_e32 v8, 1.0, v8
	v_rcp_f32_e32 v8, v8
	v_mul_f32_e32 v10, v14, v14
	v_fmac_f32_e32 v10, v30, v30
	v_lshlrev_b32_e32 v9, 16, v139
	v_mul_f32_e32 v7, v8, v7
	v_add_f32_dpp v10, v10, v10 quad_perm:[1,0,3,2] row_mask:0xf bank_mask:0xf bound_ctrl:1
	v_bfe_u32 v8, v7, 16, 1
	v_add3_u32 v7, v7, v8, s1
	v_add_f32_dpp v10, v10, v10 quad_perm:[2,3,0,1] row_mask:0xf bank_mask:0xf bound_ctrl:1
	v_mul_f32_e32 v8, 0xbfb8aa3b, v9
	v_lshlrev_b64 v[4:5], 11, v[78:79]
	v_add_f32_dpp v10, v10, v10 row_half_mirror row_mask:0xf bank_mask:0xf bound_ctrl:1
	v_exp_f32_e32 v8, v8
	v_lshl_add_u64 v[4:5], s[36:37], 0, v[4:5]
	v_add_f32_dpp v10, v10, v10 row_mirror row_mask:0xf bank_mask:0xf bound_ctrl:1
	ds_bpermute_b32 v11, v113, v10
	v_lshl_add_u64 v[4:5], v[4:5], 0, s[56:57]
	v_lshl_add_u64 v[4:5], v[4:5], 0, v[2:3]
	global_store_short_d16_hi v[4:5], v7, off offset:1536
	v_add_f32_e32 v7, 1.0, v8
	s_waitcnt lgkmcnt(0)
	v_add_f32_e32 v8, v10, v11
	v_fmamk_f32 v8, v8, 0x3c800000, v1
	v_mul_f32_e32 v10, 0x4f800000, v8
	v_cmp_gt_f32_e32 vcc, s29, v8
	v_rcp_f32_e32 v7, v7
	v_mul_f32_e32 v6, v13, v6
	v_cndmask_b32_e32 v8, v8, v10, vcc
	v_sqrt_f32_e32 v10, v8
	v_mul_f32_e32 v6, v109, v6
	v_mul_f32_e32 v6, v6, v9
	v_mul_f32_e32 v6, v7, v6
	v_add_u32_e32 v7, -1, v10
	v_fma_f32 v9, -v7, v10, v8
	v_cmp_ge_f32_e64 s[38:39], 0, v9
	v_add_u32_e32 v9, 1, v10
	s_nop 0
	v_cndmask_b32_e64 v7, v10, v7, s[38:39]
	v_fma_f32 v10, -v9, v10, v8
	v_cmp_lt_f32_e64 s[38:39], 0, v10
	v_bfe_u32 v10, v6, 16, 1
	v_add3_u32 v6, v6, v10, s1
	v_cndmask_b32_e64 v7, v7, v9, s[38:39]
	v_mul_f32_e32 v9, 0x37800000, v7
	v_cndmask_b32_e32 v7, v7, v9, vcc
	v_cmp_class_f32_e32 vcc, v8, v248
	global_store_short_d16_hi v[4:5], v6, off offset:1600
	s_nop 0
	v_cndmask_b32_e32 v7, v7, v8, vcc
	v_div_scale_f32 v8, s[8:9], v7, v7, 1.0
	v_rcp_f32_e32 v9, v8
	s_nop 0
	v_fma_f32 v4, -v8, v9, 1.0
	v_fmac_f32_e32 v9, v4, v9
	v_div_scale_f32 v4, vcc, 1.0, v7, 1.0
	v_mul_f32_e32 v5, v4, v9
	v_fma_f32 v6, -v8, v5, v4
	v_fmac_f32_e32 v5, v6, v9
	v_fma_f32 v4, -v8, v5, v4
	v_div_fmas_f32 v4, v4, v9, v5
	v_div_fixup_f32 v6, v4, v7, 1.0
	s_waitcnt vmcnt(62)
	v_lshlrev_b32_e32 v7, 16, v137
	v_mul_f32_e32 v8, 0xbfb8aa3b, v7
	v_exp_f32_e32 v8, v8
	v_mul_f32_e32 v10, v30, v6
	v_mul_f32_e32 v10, v111, v10
	v_mul_f32_e32 v7, v10, v7
	v_add_f32_e32 v8, 1.0, v8
	v_rcp_f32_e32 v8, v8
	v_mul_f32_e32 v10, v15, v15
	v_fmac_f32_e32 v10, v31, v31
	v_lshlrev_b32_e32 v9, 16, v135
	v_mul_f32_e32 v7, v8, v7
	v_add_f32_dpp v10, v10, v10 quad_perm:[1,0,3,2] row_mask:0xf bank_mask:0xf bound_ctrl:1
	v_bfe_u32 v8, v7, 16, 1
	v_add3_u32 v7, v7, v8, s1
	v_add_f32_dpp v10, v10, v10 quad_perm:[2,3,0,1] row_mask:0xf bank_mask:0xf bound_ctrl:1
	v_mul_f32_e32 v8, 0xbfb8aa3b, v9
	v_lshlrev_b64 v[4:5], 11, v[76:77]
	v_add_f32_dpp v10, v10, v10 row_half_mirror row_mask:0xf bank_mask:0xf bound_ctrl:1
	v_exp_f32_e32 v8, v8
	v_lshl_add_u64 v[4:5], s[36:37], 0, v[4:5]
	v_add_f32_dpp v10, v10, v10 row_mirror row_mask:0xf bank_mask:0xf bound_ctrl:1
	ds_bpermute_b32 v11, v113, v10
	v_lshl_add_u64 v[4:5], v[4:5], 0, s[56:57]
	v_lshl_add_u64 v[4:5], v[4:5], 0, v[2:3]
	global_store_short_d16_hi v[4:5], v7, off offset:1536
	v_add_f32_e32 v7, 1.0, v8
	s_waitcnt lgkmcnt(0)
	v_add_f32_e32 v8, v10, v11
	v_fmamk_f32 v8, v8, 0x3c800000, v1
	v_mul_f32_e32 v10, 0x4f800000, v8
	v_cmp_gt_f32_e32 vcc, s29, v8
	v_rcp_f32_e32 v7, v7
	v_mul_f32_e32 v6, v14, v6
	v_cndmask_b32_e32 v8, v8, v10, vcc
	v_sqrt_f32_e32 v10, v8
	v_mul_f32_e32 v6, v109, v6
	v_mul_f32_e32 v6, v6, v9
	v_mul_f32_e32 v6, v7, v6
	v_add_u32_e32 v7, -1, v10
	v_fma_f32 v9, -v7, v10, v8
	v_cmp_ge_f32_e64 s[38:39], 0, v9
	v_add_u32_e32 v9, 1, v10
	s_nop 0
	v_cndmask_b32_e64 v7, v10, v7, s[38:39]
	v_fma_f32 v10, -v9, v10, v8
	v_cmp_lt_f32_e64 s[38:39], 0, v10
	v_bfe_u32 v10, v6, 16, 1
	v_add3_u32 v6, v6, v10, s1
	v_cndmask_b32_e64 v7, v7, v9, s[38:39]
	v_mul_f32_e32 v9, 0x37800000, v7
	v_cndmask_b32_e32 v7, v7, v9, vcc
	v_cmp_class_f32_e32 vcc, v8, v248
	global_store_short_d16_hi v[4:5], v6, off offset:1600
	s_nop 0
	v_cndmask_b32_e32 v7, v7, v8, vcc
	v_div_scale_f32 v8, s[8:9], v7, v7, 1.0
	v_rcp_f32_e32 v9, v8
	s_nop 0
	v_fma_f32 v4, -v8, v9, 1.0
	v_fmac_f32_e32 v9, v4, v9
	v_div_scale_f32 v4, vcc, 1.0, v7, 1.0
	v_mul_f32_e32 v5, v4, v9
	v_fma_f32 v6, -v8, v5, v4
	v_fmac_f32_e32 v5, v6, v9
	v_fma_f32 v4, -v8, v5, v4
	v_div_fmas_f32 v4, v4, v9, v5
	v_div_fixup_f32 v6, v4, v7, 1.0
	s_waitcnt vmcnt(62)
	v_lshlrev_b32_e32 v7, 16, v133
	v_mul_f32_e32 v8, 0xbfb8aa3b, v7
	v_exp_f32_e32 v8, v8
	v_mul_f32_e32 v10, v31, v6
	v_mul_f32_e32 v10, v111, v10
	v_mul_f32_e32 v7, v10, v7
	v_add_f32_e32 v8, 1.0, v8
	v_rcp_f32_e32 v8, v8
	v_mul_f32_e32 v10, v16, v16
	v_fmac_f32_e32 v10, v32, v32
	v_lshlrev_b32_e32 v9, 16, v131
	v_mul_f32_e32 v7, v8, v7
	v_add_f32_dpp v10, v10, v10 quad_perm:[1,0,3,2] row_mask:0xf bank_mask:0xf bound_ctrl:1
	v_bfe_u32 v8, v7, 16, 1
	v_add3_u32 v7, v7, v8, s1
	v_add_f32_dpp v10, v10, v10 quad_perm:[2,3,0,1] row_mask:0xf bank_mask:0xf bound_ctrl:1
	v_mul_f32_e32 v8, 0xbfb8aa3b, v9
	v_lshlrev_b64 v[4:5], 11, v[74:75]
	v_add_f32_dpp v10, v10, v10 row_half_mirror row_mask:0xf bank_mask:0xf bound_ctrl:1
	v_exp_f32_e32 v8, v8
	v_lshl_add_u64 v[4:5], s[36:37], 0, v[4:5]
	v_add_f32_dpp v10, v10, v10 row_mirror row_mask:0xf bank_mask:0xf bound_ctrl:1
	ds_bpermute_b32 v11, v113, v10
	v_lshl_add_u64 v[4:5], v[4:5], 0, s[56:57]
	v_lshl_add_u64 v[4:5], v[4:5], 0, v[2:3]
	global_store_short_d16_hi v[4:5], v7, off offset:1536
	v_add_f32_e32 v7, 1.0, v8
	s_waitcnt lgkmcnt(0)
	v_add_f32_e32 v8, v10, v11
	v_fmamk_f32 v8, v8, 0x3c800000, v1
	v_mul_f32_e32 v10, 0x4f800000, v8
	v_cmp_gt_f32_e32 vcc, s29, v8
	v_rcp_f32_e32 v7, v7
	v_mul_f32_e32 v6, v15, v6
	v_cndmask_b32_e32 v8, v8, v10, vcc
	v_sqrt_f32_e32 v10, v8
	v_mul_f32_e32 v6, v109, v6
	v_mul_f32_e32 v6, v6, v9
	v_mul_f32_e32 v6, v7, v6
	v_add_u32_e32 v7, -1, v10
	v_fma_f32 v9, -v7, v10, v8
	v_cmp_ge_f32_e64 s[38:39], 0, v9
	v_add_u32_e32 v9, 1, v10
	s_nop 0
	v_cndmask_b32_e64 v7, v10, v7, s[38:39]
	v_fma_f32 v10, -v9, v10, v8
	v_cmp_lt_f32_e64 s[38:39], 0, v10
	v_bfe_u32 v10, v6, 16, 1
	v_add3_u32 v6, v6, v10, s1
	v_cndmask_b32_e64 v7, v7, v9, s[38:39]
	v_mul_f32_e32 v9, 0x37800000, v7
	v_cndmask_b32_e32 v7, v7, v9, vcc
	v_cmp_class_f32_e32 vcc, v8, v248
	global_store_short_d16_hi v[4:5], v6, off offset:1600
	s_nop 0
	v_cndmask_b32_e32 v7, v7, v8, vcc
	v_div_scale_f32 v8, s[8:9], v7, v7, 1.0
	v_rcp_f32_e32 v9, v8
	s_nop 0
	v_fma_f32 v4, -v8, v9, 1.0
	v_fmac_f32_e32 v9, v4, v9
	v_div_scale_f32 v4, vcc, 1.0, v7, 1.0
	v_mul_f32_e32 v5, v4, v9
	v_fma_f32 v6, -v8, v5, v4
	v_fmac_f32_e32 v5, v6, v9
	v_fma_f32 v4, -v8, v5, v4
	v_div_fmas_f32 v4, v4, v9, v5
	v_div_fixup_f32 v6, v4, v7, 1.0
	s_waitcnt vmcnt(62)
	v_lshlrev_b32_e32 v7, 16, v129
	v_mul_f32_e32 v8, 0xbfb8aa3b, v7
	v_exp_f32_e32 v8, v8
	v_mul_f32_e32 v10, v32, v6
	v_mul_f32_e32 v10, v111, v10
	v_mul_f32_e32 v7, v10, v7
	v_add_f32_e32 v8, 1.0, v8
	v_rcp_f32_e32 v8, v8
	v_mul_f32_e32 v10, v17, v17
	v_fmac_f32_e32 v10, v33, v33
	v_lshlrev_b32_e32 v9, 16, v127
	v_mul_f32_e32 v7, v8, v7
	v_add_f32_dpp v10, v10, v10 quad_perm:[1,0,3,2] row_mask:0xf bank_mask:0xf bound_ctrl:1
	v_bfe_u32 v8, v7, 16, 1
	v_add3_u32 v7, v7, v8, s1
	v_add_f32_dpp v10, v10, v10 quad_perm:[2,3,0,1] row_mask:0xf bank_mask:0xf bound_ctrl:1
	v_mul_f32_e32 v8, 0xbfb8aa3b, v9
	v_lshlrev_b64 v[4:5], 11, v[72:73]
	v_add_f32_dpp v10, v10, v10 row_half_mirror row_mask:0xf bank_mask:0xf bound_ctrl:1
	v_exp_f32_e32 v8, v8
	v_lshl_add_u64 v[4:5], s[36:37], 0, v[4:5]
	v_add_f32_dpp v10, v10, v10 row_mirror row_mask:0xf bank_mask:0xf bound_ctrl:1
	ds_bpermute_b32 v11, v113, v10
	v_lshl_add_u64 v[4:5], v[4:5], 0, s[56:57]
	v_lshl_add_u64 v[4:5], v[4:5], 0, v[2:3]
	global_store_short_d16_hi v[4:5], v7, off offset:1536
	v_add_f32_e32 v7, 1.0, v8
	s_waitcnt lgkmcnt(0)
	v_add_f32_e32 v8, v10, v11
	v_fmamk_f32 v8, v8, 0x3c800000, v1
	v_mul_f32_e32 v10, 0x4f800000, v8
	v_cmp_gt_f32_e32 vcc, s29, v8
	v_rcp_f32_e32 v7, v7
	v_mul_f32_e32 v6, v16, v6
	v_cndmask_b32_e32 v8, v8, v10, vcc
	v_sqrt_f32_e32 v10, v8
	v_mul_f32_e32 v6, v109, v6
	v_mul_f32_e32 v6, v6, v9
	v_mul_f32_e32 v6, v7, v6
	v_add_u32_e32 v7, -1, v10
	v_fma_f32 v9, -v7, v10, v8
	v_cmp_ge_f32_e64 s[38:39], 0, v9
	v_add_u32_e32 v9, 1, v10
	s_nop 0
	v_cndmask_b32_e64 v7, v10, v7, s[38:39]
	v_fma_f32 v10, -v9, v10, v8
	v_cmp_lt_f32_e64 s[38:39], 0, v10
	v_bfe_u32 v10, v6, 16, 1
	v_add3_u32 v6, v6, v10, s1
	v_cndmask_b32_e64 v7, v7, v9, s[38:39]
	v_mul_f32_e32 v9, 0x37800000, v7
	v_cndmask_b32_e32 v7, v7, v9, vcc
	v_cmp_class_f32_e32 vcc, v8, v248
	global_store_short_d16_hi v[4:5], v6, off offset:1600
	s_nop 0
	v_cndmask_b32_e32 v7, v7, v8, vcc
	v_div_scale_f32 v8, s[8:9], v7, v7, 1.0
	v_rcp_f32_e32 v9, v8
	s_nop 0
	v_fma_f32 v4, -v8, v9, 1.0
	v_fmac_f32_e32 v9, v4, v9
	v_div_scale_f32 v4, vcc, 1.0, v7, 1.0
	v_mul_f32_e32 v5, v4, v9
	v_fma_f32 v6, -v8, v5, v4
	v_fmac_f32_e32 v5, v6, v9
	v_fma_f32 v4, -v8, v5, v4
	v_div_fmas_f32 v4, v4, v9, v5
	v_div_fixup_f32 v6, v4, v7, 1.0
	s_waitcnt vmcnt(62)
	v_lshlrev_b32_e32 v7, 16, v125
	v_mul_f32_e32 v8, 0xbfb8aa3b, v7
	v_exp_f32_e32 v8, v8
	v_mul_f32_e32 v10, v33, v6
	v_mul_f32_e32 v10, v111, v10
	v_mul_f32_e32 v7, v10, v7
	v_add_f32_e32 v8, 1.0, v8
	v_rcp_f32_e32 v8, v8
	v_mul_f32_e32 v10, v18, v18
	v_fmac_f32_e32 v10, v34, v34
	v_lshlrev_b32_e32 v9, 16, v123
	v_mul_f32_e32 v7, v8, v7
	v_add_f32_dpp v10, v10, v10 quad_perm:[1,0,3,2] row_mask:0xf bank_mask:0xf bound_ctrl:1
	v_bfe_u32 v8, v7, 16, 1
	v_add3_u32 v7, v7, v8, s1
	v_add_f32_dpp v10, v10, v10 quad_perm:[2,3,0,1] row_mask:0xf bank_mask:0xf bound_ctrl:1
	v_mul_f32_e32 v8, 0xbfb8aa3b, v9
	v_lshlrev_b64 v[4:5], 11, v[70:71]
	v_add_f32_dpp v10, v10, v10 row_half_mirror row_mask:0xf bank_mask:0xf bound_ctrl:1
	v_exp_f32_e32 v8, v8
	v_lshl_add_u64 v[4:5], s[36:37], 0, v[4:5]
	v_add_f32_dpp v10, v10, v10 row_mirror row_mask:0xf bank_mask:0xf bound_ctrl:1
	ds_bpermute_b32 v11, v113, v10
	v_lshl_add_u64 v[4:5], v[4:5], 0, s[56:57]
	v_lshl_add_u64 v[4:5], v[4:5], 0, v[2:3]
	global_store_short_d16_hi v[4:5], v7, off offset:1536
	v_add_f32_e32 v7, 1.0, v8
	s_waitcnt lgkmcnt(0)
	v_add_f32_e32 v8, v10, v11
	v_fmamk_f32 v8, v8, 0x3c800000, v1
	v_mul_f32_e32 v10, 0x4f800000, v8
	v_cmp_gt_f32_e32 vcc, s29, v8
	v_rcp_f32_e32 v7, v7
	v_mul_f32_e32 v6, v17, v6
	v_cndmask_b32_e32 v8, v8, v10, vcc
	v_sqrt_f32_e32 v10, v8
	v_mul_f32_e32 v6, v109, v6
	v_mul_f32_e32 v6, v6, v9
	v_mul_f32_e32 v6, v7, v6
	v_add_u32_e32 v7, -1, v10
	v_fma_f32 v9, -v7, v10, v8
	v_cmp_ge_f32_e64 s[38:39], 0, v9
	v_add_u32_e32 v9, 1, v10
	s_nop 0
	v_cndmask_b32_e64 v7, v10, v7, s[38:39]
	v_fma_f32 v10, -v9, v10, v8
	v_cmp_lt_f32_e64 s[38:39], 0, v10
	v_bfe_u32 v10, v6, 16, 1
	v_add3_u32 v6, v6, v10, s1
	v_cndmask_b32_e64 v7, v7, v9, s[38:39]
	v_mul_f32_e32 v9, 0x37800000, v7
	v_cndmask_b32_e32 v7, v7, v9, vcc
	v_cmp_class_f32_e32 vcc, v8, v248
	global_store_short_d16_hi v[4:5], v6, off offset:1600
	s_nop 0
	v_cndmask_b32_e32 v7, v7, v8, vcc
	v_div_scale_f32 v8, s[8:9], v7, v7, 1.0
	v_rcp_f32_e32 v9, v8
	s_nop 0
	v_fma_f32 v4, -v8, v9, 1.0
	v_fmac_f32_e32 v9, v4, v9
	v_div_scale_f32 v4, vcc, 1.0, v7, 1.0
	v_mul_f32_e32 v5, v4, v9
	v_fma_f32 v6, -v8, v5, v4
	v_fmac_f32_e32 v5, v6, v9
	v_fma_f32 v4, -v8, v5, v4
	v_div_fmas_f32 v4, v4, v9, v5
	v_div_fixup_f32 v6, v4, v7, 1.0
	s_waitcnt vmcnt(62)
	v_lshlrev_b32_e32 v7, 16, v121
	v_mul_f32_e32 v8, 0xbfb8aa3b, v7
	v_exp_f32_e32 v8, v8
	v_mul_f32_e32 v10, v34, v6
	v_mul_f32_e32 v10, v111, v10
	v_mul_f32_e32 v7, v10, v7
	v_add_f32_e32 v8, 1.0, v8
	v_rcp_f32_e32 v8, v8
	v_mul_f32_e32 v10, v19, v19
	v_fmac_f32_e32 v10, v35, v35
	v_lshlrev_b32_e32 v9, 16, v119
	v_mul_f32_e32 v7, v8, v7
	v_add_f32_dpp v10, v10, v10 quad_perm:[1,0,3,2] row_mask:0xf bank_mask:0xf bound_ctrl:1
	v_bfe_u32 v8, v7, 16, 1
	v_add3_u32 v7, v7, v8, s1
	v_add_f32_dpp v10, v10, v10 quad_perm:[2,3,0,1] row_mask:0xf bank_mask:0xf bound_ctrl:1
	v_mul_f32_e32 v8, 0xbfb8aa3b, v9
	v_lshlrev_b64 v[4:5], 11, v[68:69]
	v_add_f32_dpp v10, v10, v10 row_half_mirror row_mask:0xf bank_mask:0xf bound_ctrl:1
	v_exp_f32_e32 v8, v8
	v_lshl_add_u64 v[4:5], s[36:37], 0, v[4:5]
	v_add_f32_dpp v10, v10, v10 row_mirror row_mask:0xf bank_mask:0xf bound_ctrl:1
	ds_bpermute_b32 v11, v113, v10
	v_lshl_add_u64 v[4:5], v[4:5], 0, s[56:57]
	v_lshl_add_u64 v[4:5], v[4:5], 0, v[2:3]
	global_store_short_d16_hi v[4:5], v7, off offset:1536
	v_add_f32_e32 v7, 1.0, v8
	s_waitcnt lgkmcnt(0)
	v_add_f32_e32 v8, v10, v11
	v_fmamk_f32 v8, v8, 0x3c800000, v1
	v_mul_f32_e32 v10, 0x4f800000, v8
	v_cmp_gt_f32_e32 vcc, s29, v8
	v_rcp_f32_e32 v7, v7
	v_mul_f32_e32 v6, v18, v6
	v_cndmask_b32_e32 v8, v8, v10, vcc
	v_sqrt_f32_e32 v10, v8
	v_mul_f32_e32 v6, v109, v6
	v_mul_f32_e32 v6, v6, v9
	v_mul_f32_e32 v6, v7, v6
	v_add_u32_e32 v7, -1, v10
	v_fma_f32 v9, -v7, v10, v8
	v_cmp_ge_f32_e64 s[38:39], 0, v9
	v_add_u32_e32 v9, 1, v10
	s_nop 0
	v_cndmask_b32_e64 v7, v10, v7, s[38:39]
	v_fma_f32 v10, -v9, v10, v8
	v_cmp_lt_f32_e64 s[38:39], 0, v10
	v_bfe_u32 v10, v6, 16, 1
	v_add3_u32 v6, v6, v10, s1
	v_cndmask_b32_e64 v7, v7, v9, s[38:39]
	v_mul_f32_e32 v9, 0x37800000, v7
	v_cndmask_b32_e32 v7, v7, v9, vcc
	v_cmp_class_f32_e32 vcc, v8, v248
	global_store_short_d16_hi v[4:5], v6, off offset:1600
	s_nop 0
	v_cndmask_b32_e32 v7, v7, v8, vcc
	v_div_scale_f32 v8, s[8:9], v7, v7, 1.0
	v_rcp_f32_e32 v9, v8
	s_nop 0
	v_fma_f32 v4, -v8, v9, 1.0
	v_fmac_f32_e32 v9, v4, v9
	v_div_scale_f32 v4, vcc, 1.0, v7, 1.0
	v_mul_f32_e32 v5, v4, v9
	v_fma_f32 v6, -v8, v5, v4
	v_fmac_f32_e32 v5, v6, v9
	v_fma_f32 v4, -v8, v5, v4
	v_div_fmas_f32 v4, v4, v9, v5
	v_div_fixup_f32 v6, v4, v7, 1.0
	s_waitcnt vmcnt(62)
	v_lshlrev_b32_e32 v7, 16, v117
	v_mul_f32_e32 v8, 0xbfb8aa3b, v7
	v_exp_f32_e32 v8, v8
	v_lshlrev_b64 v[4:5], 11, v[36:37]
	v_lshl_add_u64 v[4:5], s[36:37], 0, v[4:5]
	v_mul_f32_e32 v9, v35, v6
	v_add_f32_e32 v8, 1.0, v8
	v_rcp_f32_e32 v8, v8
	v_lshl_add_u64 v[4:5], v[4:5], 0, s[56:57]
	v_mul_f32_e32 v9, v111, v9
	v_lshl_add_u64 v[4:5], v[4:5], 0, v[2:3]
	v_lshlrev_b32_e32 v2, 16, v115
	v_mul_f32_e32 v7, v9, v7
	v_mul_f32_e32 v7, v8, v7
	v_mul_f32_e32 v8, 0xbfb8aa3b, v2
	v_exp_f32_e32 v8, v8
	v_bfe_u32 v9, v7, 16, 1
	v_add3_u32 v7, v7, v9, s1
	global_store_short_d16_hi v[4:5], v7, off offset:1536
	v_add_f32_e32 v7, 1.0, v8
	v_rcp_f32_e32 v7, v7
	v_mul_f32_e32 v6, v19, v6
	v_mul_f32_e32 v6, v109, v6
	v_mul_f32_e32 v2, v6, v2
	v_mul_f32_e32 v2, v7, v2
	v_bfe_u32 v6, v2, 16, 1
	v_add3_u32 v2, v2, v6, s1
	global_store_short_d16_hi v[4:5], v2, off offset:1600
	s_cbranch_scc0 .LBB0_907
